# expert-index scalar loads marked glc (always served by L2, never by a scalar-cache line left by an earlier launch); otherwise as the guarded version
# speedup vs baseline: 1.0033x; 1.0033x over previous
.Lgba_1444:
	s_or_b64 exec, exec, s[2:3]
	s_waitcnt lgkmcnt(0)
	s_barrier
	s_mov_b64 exec, -1
	v_and_b32_e32 v1, 63, v0
	v_readfirstlane_b32 s16, v0
	s_load_dwordx2 s[12:13], s[0:1], 0xc0
	s_lshr_b32 s16, s16, 6
	s_and_b32 s18, s33, 7
	s_lshr_b32 s19, s33, 3
	s_lshl_b32 s19, s19, 8
	s_lshl_b32 s16, s16, 5
	s_add_i32 s16, s16, s19
	s_add_i32 s17, s16, 32
	s_add_i32 s24, s17, -1
	s_lshl_b32 s19, s18, 9
	v_lshl_add_u32 v162, v1, 3, s19
	v_mov_b32_e32 v163, 0
	s_mov_b32 s31, 0
	v_and_b32_e32 v4, 8, v1
	v_cmp_eq_u32_e64 s[8:9], 0, v4
	v_and_b32_e32 v4, 4, v1
	v_cmp_eq_u32_e64 s[10:11], 0, v4
	v_and_b32_e32 v4, 2, v1
	v_cmp_eq_u32_e64 s[14:15], 0, v4
	s_mov_b32 s2, 0x55555555
	s_mov_b32 s3, 0x55555555
	s_load_dwordx2 s[4:5], s[0:1], 0x88
	s_waitcnt lgkmcnt(0)
	v_lshl_add_u64 v[160:161], v[162:163], 2, s[4:5]
	global_load_dwordx4 v[100:103], v[160:161], off
	global_load_dwordx4 v[104:107], v[160:161], off offset:16
	s_lshl_b32 s19, s18, 20
	s_add_u32 s22, s12, 0x25c00000
	s_addc_u32 s23, s13, 0
	s_add_u32 s22, s22, s19
	s_addc_u32 s23, s23, 0
	s_add_u32 s26, s12, 0xfc00000
	s_addc_u32 s27, s13, 0
	s_add_u32 s20, s12, 0x100000
	s_addc_u32 s21, s13, 0
	v_lshl_add_u64 v[172:173], v[162:163], 1, s[20:21]
	s_add_u32 s20, s12, 0x4da00000
	s_addc_u32 s21, s13, 0
	v_mov_b32_e32 v4, v1
	v_mov_b32_e32 v5, 0
	v_lshl_add_u64 v[174:175], v[4:5], 2, s[20:21]
	s_lshl_b32 s19, s18, 22
	s_add_u32 s20, s12, 0x23c00000
	s_addc_u32 s21, s13, 0
	s_add_u32 s20, s20, s19
	s_addc_u32 s21, s21, 0
	v_lshl_add_u64 v[176:177], v[4:5], 1, s[20:21]
	s_lshl_b32 s30, s16, 13
	v_lshl_add_u64 v[160:161], v[172:173], 0, s[30:31]
	global_load_dwordx4 v[116:119], v[160:161], off
	s_lshl_b32 s30, s16, 9
	v_lshl_add_u64 v[160:161], v[174:175], 0, s[30:31]
	global_load_dword v122, v[160:161], off
	global_load_dword v123, v[160:161], off offset:256
	s_waitcnt vmcnt(0)
	s_add_u32 s40, s12, 0x4da00000
	s_addc_u32 s41, s13, 0
	s_lshl_b32 s30, s16, 9
	s_add_u32 s36, s40, s30
	s_addc_u32 s37, s41, 0
	s_load_dwordx16 s[68:83], s[36:37], 0x0 glc
	s_load_dwordx16 s[84:99], s[36:37], 0x40 glc
	s_waitcnt lgkmcnt(0)
	s_lshl_b32 s30, s68, 12
	s_add_u32 s28, s26, s30
	s_addc_u32 s29, s27, 0
	global_load_dwordx2 v[24:25], v162, s[28:29]
	s_lshl_b32 s30, s69, 12
	s_add_u32 s28, s26, s30
	s_addc_u32 s29, s27, 0
	global_load_dwordx2 v[26:27], v162, s[28:29]
	s_lshl_b32 s30, s70, 12
	s_add_u32 s28, s26, s30
	s_addc_u32 s29, s27, 0
	global_load_dwordx2 v[28:29], v162, s[28:29]
	s_lshl_b32 s30, s71, 12
	s_add_u32 s28, s26, s30
	s_addc_u32 s29, s27, 0
	global_load_dwordx2 v[30:31], v162, s[28:29]
	s_lshl_b32 s30, s72, 12
	s_add_u32 s28, s26, s30
	s_addc_u32 s29, s27, 0
	global_load_dwordx2 v[32:33], v162, s[28:29]
	s_lshl_b32 s30, s73, 12
	s_add_u32 s28, s26, s30
	s_addc_u32 s29, s27, 0
	global_load_dwordx2 v[34:35], v162, s[28:29]
	s_lshl_b32 s30, s74, 12
	s_add_u32 s28, s26, s30
	s_addc_u32 s29, s27, 0
	global_load_dwordx2 v[36:37], v162, s[28:29]
	s_lshl_b32 s30, s75, 12
	s_add_u32 s28, s26, s30
	s_addc_u32 s29, s27, 0
	global_load_dwordx2 v[38:39], v162, s[28:29]
	s_lshl_b32 s30, s76, 12
	s_add_u32 s28, s26, s30
	s_addc_u32 s29, s27, 0
	global_load_dwordx2 v[40:41], v162, s[28:29]
	s_lshl_b32 s30, s77, 12
	s_add_u32 s28, s26, s30
	s_addc_u32 s29, s27, 0
	global_load_dwordx2 v[42:43], v162, s[28:29]
	s_lshl_b32 s30, s78, 12
	s_add_u32 s28, s26, s30
	s_addc_u32 s29, s27, 0
	global_load_dwordx2 v[44:45], v162, s[28:29]
	s_lshl_b32 s30, s79, 12
	s_add_u32 s28, s26, s30
	s_addc_u32 s29, s27, 0
	global_load_dwordx2 v[46:47], v162, s[28:29]
	s_lshl_b32 s30, s80, 12
	s_add_u32 s28, s26, s30
	s_addc_u32 s29, s27, 0
	global_load_dwordx2 v[48:49], v162, s[28:29]
	s_lshl_b32 s30, s81, 12
	s_add_u32 s28, s26, s30
	s_addc_u32 s29, s27, 0
	global_load_dwordx2 v[50:51], v162, s[28:29]
	s_lshl_b32 s30, s82, 12
	s_add_u32 s28, s26, s30
	s_addc_u32 s29, s27, 0
	global_load_dwordx2 v[52:53], v162, s[28:29]
	s_lshl_b32 s30, s83, 12
	s_add_u32 s28, s26, s30
	s_addc_u32 s29, s27, 0
	global_load_dwordx2 v[54:55], v162, s[28:29]
	s_lshl_b32 s30, s84, 12
	s_add_u32 s28, s26, s30
	s_addc_u32 s29, s27, 0
	global_load_dwordx2 v[56:57], v162, s[28:29]
	s_lshl_b32 s30, s85, 12
	s_add_u32 s28, s26, s30
	s_addc_u32 s29, s27, 0
	global_load_dwordx2 v[58:59], v162, s[28:29]
	s_lshl_b32 s30, s86, 12
	s_add_u32 s28, s26, s30
	s_addc_u32 s29, s27, 0
	global_load_dwordx2 v[60:61], v162, s[28:29]
	s_lshl_b32 s30, s87, 12
	s_add_u32 s28, s26, s30
	s_addc_u32 s29, s27, 0
	global_load_dwordx2 v[62:63], v162, s[28:29]
	s_lshl_b32 s30, s88, 12
	s_add_u32 s28, s26, s30
	s_addc_u32 s29, s27, 0
	global_load_dwordx2 v[64:65], v162, s[28:29]
	s_lshl_b32 s30, s89, 12
	s_add_u32 s28, s26, s30
	s_addc_u32 s29, s27, 0
	global_load_dwordx2 v[66:67], v162, s[28:29]
	s_lshl_b32 s30, s90, 12
	s_add_u32 s28, s26, s30
	s_addc_u32 s29, s27, 0
	global_load_dwordx2 v[68:69], v162, s[28:29]
	s_lshl_b32 s30, s91, 12
	s_add_u32 s28, s26, s30
	s_addc_u32 s29, s27, 0
	global_load_dwordx2 v[70:71], v162, s[28:29]
	s_lshl_b32 s30, s92, 12
	s_add_u32 s28, s26, s30
	s_addc_u32 s29, s27, 0
	global_load_dwordx2 v[72:73], v162, s[28:29]
	s_lshl_b32 s30, s93, 12
	s_add_u32 s28, s26, s30
	s_addc_u32 s29, s27, 0
	global_load_dwordx2 v[74:75], v162, s[28:29]
	s_lshl_b32 s30, s94, 12
	s_add_u32 s28, s26, s30
	s_addc_u32 s29, s27, 0
	global_load_dwordx2 v[76:77], v162, s[28:29]
	s_lshl_b32 s30, s95, 12
	s_add_u32 s28, s26, s30
	s_addc_u32 s29, s27, 0
	global_load_dwordx2 v[78:79], v162, s[28:29]
	s_lshl_b32 s30, s96, 12
	s_add_u32 s28, s26, s30
	s_addc_u32 s29, s27, 0
	global_load_dwordx2 v[80:81], v162, s[28:29]
	s_lshl_b32 s30, s97, 12
	s_add_u32 s28, s26, s30
	s_addc_u32 s29, s27, 0
	global_load_dwordx2 v[82:83], v162, s[28:29]
	s_lshl_b32 s30, s98, 12
	s_add_u32 s28, s26, s30
	s_addc_u32 s29, s27, 0
	global_load_dwordx2 v[84:85], v162, s[28:29]
	s_lshl_b32 s30, s99, 12
	s_add_u32 s28, s26, s30
	s_addc_u32 s29, s27, 0
	global_load_dwordx2 v[86:87], v162, s[28:29]
	s_load_dwordx16 s[68:83], s[36:37], 0x80 glc
.Lpa_tok:
	v_lshlrev_b32_e32 v124, 16, v116
	v_and_b32_e32 v125, 0xffff0000, v116
	v_pk_mul_f32 v[108:109], v[124:125], v[100:101]
	v_lshlrev_b32_e32 v124, 16, v117
	v_and_b32_e32 v125, 0xffff0000, v117
	v_pk_mul_f32 v[110:111], v[124:125], v[102:103]
	v_lshlrev_b32_e32 v124, 16, v118
	v_and_b32_e32 v125, 0xffff0000, v118
	v_pk_mul_f32 v[112:113], v[124:125], v[104:105]
	v_lshlrev_b32_e32 v124, 16, v119
	v_and_b32_e32 v125, 0xffff0000, v119
	v_pk_mul_f32 v[114:115], v[124:125], v[106:107]
	v_add_f32_e32 v16, v108, v109
	v_add_f32_e32 v17, v110, v111
	v_add_f32_e32 v18, v112, v113
	v_add_f32_e32 v19, v114, v115
	v_add_f32_e32 v16, v16, v17
	v_add_f32_e32 v18, v18, v19
	v_add_f32_e32 v16, v16, v18
	s_nop 1
	v_add_f32_dpp v17, v16, v16 quad_perm:[1,0,3,2] row_mask:0xf bank_mask:0xf
	s_nop 1
	v_add_f32_dpp v16, v17, v17 quad_perm:[2,3,0,1] row_mask:0xf bank_mask:0xf
	s_nop 1
	v_add_f32_dpp v17, v16, v16 row_half_mirror row_mask:0xf bank_mask:0xf
	s_nop 1
	v_add_f32_dpp v16, v17, v17 row_ror:8 row_mask:0xf bank_mask:0xf
	v_mov_b32_e32 v17, v16
	s_nop 1
	v_permlane16_swap_b32_e32 v16, v17
	v_add_f32_e32 v16, v16, v17
	v_mov_b32_e32 v17, v16
	s_nop 1
	v_permlane32_swap_b32_e32 v16, v17
	v_add_f32_e32 v16, v16, v17
	s_lshl_b32 s30, s16, 7
	s_add_u32 s28, s22, s30
	s_addc_u32 s29, s23, 0
	v_lshlrev_b32_e32 v19, 1, v1
	s_mov_b64 exec, s[2:3]
	global_store_dword v19, v16, s[28:29]
	s_mov_b64 exec, -1
	v_mov_b32_e32 v120, v122
	v_mov_b32_e32 v121, v123
	s_lshl_b32 s30, s16, 9
	v_lshl_add_u64 v[22:23], v[176:177], 0, s[30:31]
	s_add_i32 s18, s16, 1
	s_min_i32 s18, s18, s24
	s_lshl_b32 s30, s16, 9
	s_add_u32 s36, s40, s30
	s_addc_u32 s37, s41, 0
	s_lshl_b32 s30, s18, 9
	s_add_u32 s38, s40, s30
	s_addc_u32 s39, s41, 0
	s_lshl_b32 s30, s18, 13
	v_lshl_add_u64 v[160:161], v[172:173], 0, s[30:31]
	global_load_dwordx4 v[116:119], v[160:161], off
	s_lshl_b32 s30, s18, 9
	v_lshl_add_u64 v[160:161], v[174:175], 0, s[30:31]
	global_load_dword v122, v[160:161], off
	global_load_dword v123, v[160:161], off offset:256
	s_waitcnt vmcnt(34)
	v_cvt_f32_ubyte0_e32 v124, v24
	v_cvt_f32_ubyte1_e32 v126, v24
	v_cvt_f32_ubyte2_e32 v128, v24
	v_cvt_f32_ubyte3_e32 v130, v24
	v_cvt_f32_ubyte0_e32 v132, v25
	v_cvt_f32_ubyte1_e32 v134, v25
	v_cvt_f32_ubyte2_e32 v136, v25
	v_cvt_f32_ubyte3_e32 v138, v25
	s_waitcnt lgkmcnt(0)
	s_load_dwordx16 s[84:99], s[36:37], 0xc0 glc
	s_lshl_b32 s30, s68, 12
	s_add_u32 s28, s26, s30
	s_addc_u32 s29, s27, 0
	global_load_dwordx2 v[24:25], v162, s[28:29]
	s_waitcnt vmcnt(34)
	v_cvt_f32_ubyte0_e32 v125, v26
	v_cvt_f32_ubyte1_e32 v127, v26
	v_cvt_f32_ubyte2_e32 v129, v26
	v_cvt_f32_ubyte3_e32 v131, v26
	v_cvt_f32_ubyte0_e32 v133, v27
	v_cvt_f32_ubyte1_e32 v135, v27
	v_cvt_f32_ubyte2_e32 v137, v27
	v_cvt_f32_ubyte3_e32 v139, v27
	s_lshl_b32 s30, s69, 12
	s_add_u32 s28, s26, s30
	s_addc_u32 s29, s27, 0
	global_load_dwordx2 v[26:27], v162, s[28:29]
	s_waitcnt vmcnt(34)
	v_cvt_f32_ubyte0_e32 v140, v28
	v_cvt_f32_ubyte1_e32 v142, v28
	v_cvt_f32_ubyte2_e32 v144, v28
	v_cvt_f32_ubyte3_e32 v146, v28
	v_cvt_f32_ubyte0_e32 v148, v29
	v_cvt_f32_ubyte1_e32 v150, v29
	v_cvt_f32_ubyte2_e32 v152, v29
	v_cvt_f32_ubyte3_e32 v154, v29
	s_lshl_b32 s30, s70, 12
	s_add_u32 s28, s26, s30
	s_addc_u32 s29, s27, 0
	global_load_dwordx2 v[28:29], v162, s[28:29]
	s_waitcnt vmcnt(34)
	v_cvt_f32_ubyte0_e32 v141, v30
	v_cvt_f32_ubyte1_e32 v143, v30
	v_cvt_f32_ubyte2_e32 v145, v30
	v_cvt_f32_ubyte3_e32 v147, v30
	v_cvt_f32_ubyte0_e32 v149, v31
	v_cvt_f32_ubyte1_e32 v151, v31
	v_cvt_f32_ubyte2_e32 v153, v31
	v_cvt_f32_ubyte3_e32 v155, v31
	s_lshl_b32 s30, s71, 12
	s_add_u32 s28, s26, s30
	s_addc_u32 s29, s27, 0
	global_load_dwordx2 v[30:31], v162, s[28:29]
	v_mul_f32_e32 v178, v124, v108
	v_mul_f32_e32 v179, v125, v108
	v_mul_f32_e32 v180, v140, v108
	v_mul_f32_e32 v181, v141, v108
	v_fmac_f32_e32 v178, v126, v109
	v_fmac_f32_e32 v179, v127, v109
	v_fmac_f32_e32 v180, v142, v109
	v_fmac_f32_e32 v181, v143, v109
	v_fmac_f32_e32 v178, v128, v110
	v_fmac_f32_e32 v179, v129, v110
	v_fmac_f32_e32 v180, v144, v110
	v_fmac_f32_e32 v181, v145, v110
	v_fmac_f32_e32 v178, v130, v111
	v_fmac_f32_e32 v179, v131, v111
	v_fmac_f32_e32 v180, v146, v111
	v_fmac_f32_e32 v181, v147, v111
	v_fmac_f32_e32 v178, v132, v112
	v_fmac_f32_e32 v179, v133, v112
	v_fmac_f32_e32 v180, v148, v112
	v_fmac_f32_e32 v181, v149, v112
	v_fmac_f32_e32 v178, v134, v113
	v_fmac_f32_e32 v179, v135, v113
	v_fmac_f32_e32 v180, v150, v113
	v_fmac_f32_e32 v181, v151, v113
	v_fmac_f32_e32 v178, v136, v114
	v_fmac_f32_e32 v179, v137, v114
	v_fmac_f32_e32 v180, v152, v114
	v_fmac_f32_e32 v181, v153, v114
	v_fmac_f32_e32 v178, v138, v115
	v_fmac_f32_e32 v179, v139, v115
	v_fmac_f32_e32 v180, v154, v115
	v_fmac_f32_e32 v181, v155, v115
	s_waitcnt vmcnt(34)
	v_cvt_f32_ubyte0_e32 v124, v32
	v_cvt_f32_ubyte1_e32 v126, v32
	v_cvt_f32_ubyte2_e32 v128, v32
	v_cvt_f32_ubyte3_e32 v130, v32
	v_cvt_f32_ubyte0_e32 v132, v33
	v_cvt_f32_ubyte1_e32 v134, v33
	v_cvt_f32_ubyte2_e32 v136, v33
	v_cvt_f32_ubyte3_e32 v138, v33
	s_lshl_b32 s30, s72, 12
	s_add_u32 s28, s26, s30
	s_addc_u32 s29, s27, 0
	global_load_dwordx2 v[32:33], v162, s[28:29]
	s_waitcnt vmcnt(34)
	v_cvt_f32_ubyte0_e32 v125, v34
	v_cvt_f32_ubyte1_e32 v127, v34
	v_cvt_f32_ubyte2_e32 v129, v34
	v_cvt_f32_ubyte3_e32 v131, v34
	v_cvt_f32_ubyte0_e32 v133, v35
	v_cvt_f32_ubyte1_e32 v135, v35
	v_cvt_f32_ubyte2_e32 v137, v35
	v_cvt_f32_ubyte3_e32 v139, v35
	s_lshl_b32 s30, s73, 12
	s_add_u32 s28, s26, s30
	s_addc_u32 s29, s27, 0
	global_load_dwordx2 v[34:35], v162, s[28:29]
	s_waitcnt vmcnt(34)
	v_cvt_f32_ubyte0_e32 v140, v36
	v_cvt_f32_ubyte1_e32 v142, v36
	v_cvt_f32_ubyte2_e32 v144, v36
	v_cvt_f32_ubyte3_e32 v146, v36
	v_cvt_f32_ubyte0_e32 v148, v37
	v_cvt_f32_ubyte1_e32 v150, v37
	v_cvt_f32_ubyte2_e32 v152, v37
	v_cvt_f32_ubyte3_e32 v154, v37
	s_lshl_b32 s30, s74, 12
	s_add_u32 s28, s26, s30
	s_addc_u32 s29, s27, 0
	global_load_dwordx2 v[36:37], v162, s[28:29]
	s_waitcnt vmcnt(34)
	v_cvt_f32_ubyte0_e32 v141, v38
	v_cvt_f32_ubyte1_e32 v143, v38
	v_cvt_f32_ubyte2_e32 v145, v38
	v_cvt_f32_ubyte3_e32 v147, v38
	v_cvt_f32_ubyte0_e32 v149, v39
	v_cvt_f32_ubyte1_e32 v151, v39
	v_cvt_f32_ubyte2_e32 v153, v39
	v_cvt_f32_ubyte3_e32 v155, v39
	s_lshl_b32 s30, s75, 12
	s_add_u32 s28, s26, s30
	s_addc_u32 s29, s27, 0
	global_load_dwordx2 v[38:39], v162, s[28:29]
	v_mul_f32_e32 v182, v124, v108
	v_mul_f32_e32 v183, v125, v108
	v_mul_f32_e32 v184, v140, v108
	v_mul_f32_e32 v185, v141, v108
	v_fmac_f32_e32 v182, v126, v109
	v_fmac_f32_e32 v183, v127, v109
	v_fmac_f32_e32 v184, v142, v109
	v_fmac_f32_e32 v185, v143, v109
	v_fmac_f32_e32 v182, v128, v110
	v_fmac_f32_e32 v183, v129, v110
	v_fmac_f32_e32 v184, v144, v110
	v_fmac_f32_e32 v185, v145, v110
	v_fmac_f32_e32 v182, v130, v111
	v_fmac_f32_e32 v183, v131, v111
	v_fmac_f32_e32 v184, v146, v111
	v_fmac_f32_e32 v185, v147, v111
	v_fmac_f32_e32 v182, v132, v112
	v_fmac_f32_e32 v183, v133, v112
	v_fmac_f32_e32 v184, v148, v112
	v_fmac_f32_e32 v185, v149, v112
	v_fmac_f32_e32 v182, v134, v113
	v_fmac_f32_e32 v183, v135, v113
	v_fmac_f32_e32 v184, v150, v113
	v_fmac_f32_e32 v185, v151, v113
	v_fmac_f32_e32 v182, v136, v114
	v_fmac_f32_e32 v183, v137, v114
	v_fmac_f32_e32 v184, v152, v114
	v_fmac_f32_e32 v185, v153, v114
	v_fmac_f32_e32 v182, v138, v115
	v_fmac_f32_e32 v183, v139, v115
	v_fmac_f32_e32 v184, v154, v115
	v_fmac_f32_e32 v185, v155, v115
	s_waitcnt vmcnt(34)
	v_cvt_f32_ubyte0_e32 v124, v40
	v_cvt_f32_ubyte1_e32 v126, v40
	v_cvt_f32_ubyte2_e32 v128, v40
	v_cvt_f32_ubyte3_e32 v130, v40
	v_cvt_f32_ubyte0_e32 v132, v41
	v_cvt_f32_ubyte1_e32 v134, v41
	v_cvt_f32_ubyte2_e32 v136, v41
	v_cvt_f32_ubyte3_e32 v138, v41
	s_lshl_b32 s30, s76, 12
	s_add_u32 s28, s26, s30
	s_addc_u32 s29, s27, 0
	global_load_dwordx2 v[40:41], v162, s[28:29]
	s_waitcnt vmcnt(34)
	v_cvt_f32_ubyte0_e32 v125, v42
	v_cvt_f32_ubyte1_e32 v127, v42
	v_cvt_f32_ubyte2_e32 v129, v42
	v_cvt_f32_ubyte3_e32 v131, v42
	v_cvt_f32_ubyte0_e32 v133, v43
	v_cvt_f32_ubyte1_e32 v135, v43
	v_cvt_f32_ubyte2_e32 v137, v43
	v_cvt_f32_ubyte3_e32 v139, v43
	s_lshl_b32 s30, s77, 12
	s_add_u32 s28, s26, s30
	s_addc_u32 s29, s27, 0
	global_load_dwordx2 v[42:43], v162, s[28:29]
	s_waitcnt vmcnt(34)
	v_cvt_f32_ubyte0_e32 v140, v44
	v_cvt_f32_ubyte1_e32 v142, v44
	v_cvt_f32_ubyte2_e32 v144, v44
	v_cvt_f32_ubyte3_e32 v146, v44
	v_cvt_f32_ubyte0_e32 v148, v45
	v_cvt_f32_ubyte1_e32 v150, v45
	v_cvt_f32_ubyte2_e32 v152, v45
	v_cvt_f32_ubyte3_e32 v154, v45
	s_lshl_b32 s30, s78, 12
	s_add_u32 s28, s26, s30
	s_addc_u32 s29, s27, 0
	global_load_dwordx2 v[44:45], v162, s[28:29]
	s_waitcnt vmcnt(34)
	v_cvt_f32_ubyte0_e32 v141, v46
	v_cvt_f32_ubyte1_e32 v143, v46
	v_cvt_f32_ubyte2_e32 v145, v46
	v_cvt_f32_ubyte3_e32 v147, v46
	v_cvt_f32_ubyte0_e32 v149, v47
	v_cvt_f32_ubyte1_e32 v151, v47
	v_cvt_f32_ubyte2_e32 v153, v47
	v_cvt_f32_ubyte3_e32 v155, v47
	s_lshl_b32 s30, s79, 12
	s_add_u32 s28, s26, s30
	s_addc_u32 s29, s27, 0
	global_load_dwordx2 v[46:47], v162, s[28:29]
	v_mul_f32_e32 v186, v124, v108
	v_mul_f32_e32 v187, v125, v108
	v_mul_f32_e32 v188, v140, v108
	v_mul_f32_e32 v189, v141, v108
	v_fmac_f32_e32 v186, v126, v109
	v_fmac_f32_e32 v187, v127, v109
	v_fmac_f32_e32 v188, v142, v109
	v_fmac_f32_e32 v189, v143, v109
	v_fmac_f32_e32 v186, v128, v110
	v_fmac_f32_e32 v187, v129, v110
	v_fmac_f32_e32 v188, v144, v110
	v_fmac_f32_e32 v189, v145, v110
	v_fmac_f32_e32 v186, v130, v111
	v_fmac_f32_e32 v187, v131, v111
	v_fmac_f32_e32 v188, v146, v111
	v_fmac_f32_e32 v189, v147, v111
	v_fmac_f32_e32 v186, v132, v112
	v_fmac_f32_e32 v187, v133, v112
	v_fmac_f32_e32 v188, v148, v112
	v_fmac_f32_e32 v189, v149, v112
	v_fmac_f32_e32 v186, v134, v113
	v_fmac_f32_e32 v187, v135, v113
	v_fmac_f32_e32 v188, v150, v113
	v_fmac_f32_e32 v189, v151, v113
	v_fmac_f32_e32 v186, v136, v114
	v_fmac_f32_e32 v187, v137, v114
	v_fmac_f32_e32 v188, v152, v114
	v_fmac_f32_e32 v189, v153, v114
	v_fmac_f32_e32 v186, v138, v115
	v_fmac_f32_e32 v187, v139, v115
	v_fmac_f32_e32 v188, v154, v115
	v_fmac_f32_e32 v189, v155, v115
	s_waitcnt vmcnt(34)
	v_cvt_f32_ubyte0_e32 v124, v48
	v_cvt_f32_ubyte1_e32 v126, v48
	v_cvt_f32_ubyte2_e32 v128, v48
	v_cvt_f32_ubyte3_e32 v130, v48
	v_cvt_f32_ubyte0_e32 v132, v49
	v_cvt_f32_ubyte1_e32 v134, v49
	v_cvt_f32_ubyte2_e32 v136, v49
	v_cvt_f32_ubyte3_e32 v138, v49
	s_lshl_b32 s30, s80, 12
	s_add_u32 s28, s26, s30
	s_addc_u32 s29, s27, 0
	global_load_dwordx2 v[48:49], v162, s[28:29]
	s_waitcnt vmcnt(34)
	v_cvt_f32_ubyte0_e32 v125, v50
	v_cvt_f32_ubyte1_e32 v127, v50
	v_cvt_f32_ubyte2_e32 v129, v50
	v_cvt_f32_ubyte3_e32 v131, v50
	v_cvt_f32_ubyte0_e32 v133, v51
	v_cvt_f32_ubyte1_e32 v135, v51
	v_cvt_f32_ubyte2_e32 v137, v51
	v_cvt_f32_ubyte3_e32 v139, v51
	s_lshl_b32 s30, s81, 12
	s_add_u32 s28, s26, s30
	s_addc_u32 s29, s27, 0
	global_load_dwordx2 v[50:51], v162, s[28:29]
	s_waitcnt vmcnt(34)
	v_cvt_f32_ubyte0_e32 v140, v52
	v_cvt_f32_ubyte1_e32 v142, v52
	v_cvt_f32_ubyte2_e32 v144, v52
	v_cvt_f32_ubyte3_e32 v146, v52
	v_cvt_f32_ubyte0_e32 v148, v53
	v_cvt_f32_ubyte1_e32 v150, v53
	v_cvt_f32_ubyte2_e32 v152, v53
	v_cvt_f32_ubyte3_e32 v154, v53
	s_lshl_b32 s30, s82, 12
	s_add_u32 s28, s26, s30
	s_addc_u32 s29, s27, 0
	global_load_dwordx2 v[52:53], v162, s[28:29]
	s_waitcnt vmcnt(34)
	v_cvt_f32_ubyte0_e32 v141, v54
	v_cvt_f32_ubyte1_e32 v143, v54
	v_cvt_f32_ubyte2_e32 v145, v54
	v_cvt_f32_ubyte3_e32 v147, v54
	v_cvt_f32_ubyte0_e32 v149, v55
	v_cvt_f32_ubyte1_e32 v151, v55
	v_cvt_f32_ubyte2_e32 v153, v55
	v_cvt_f32_ubyte3_e32 v155, v55
	s_lshl_b32 s30, s83, 12
	s_add_u32 s28, s26, s30
	s_addc_u32 s29, s27, 0
	global_load_dwordx2 v[54:55], v162, s[28:29]
	v_mul_f32_e32 v190, v124, v108
	v_mul_f32_e32 v191, v125, v108
	v_mul_f32_e32 v192, v140, v108
	v_mul_f32_e32 v193, v141, v108
	v_fmac_f32_e32 v190, v126, v109
	v_fmac_f32_e32 v191, v127, v109
	v_fmac_f32_e32 v192, v142, v109
	v_fmac_f32_e32 v193, v143, v109
	v_fmac_f32_e32 v190, v128, v110
	v_fmac_f32_e32 v191, v129, v110
	v_fmac_f32_e32 v192, v144, v110
	v_fmac_f32_e32 v193, v145, v110
	v_fmac_f32_e32 v190, v130, v111
	v_fmac_f32_e32 v191, v131, v111
	v_fmac_f32_e32 v192, v146, v111
	v_fmac_f32_e32 v193, v147, v111
	v_fmac_f32_e32 v190, v132, v112
	v_fmac_f32_e32 v191, v133, v112
	v_fmac_f32_e32 v192, v148, v112
	v_fmac_f32_e32 v193, v149, v112
	v_fmac_f32_e32 v190, v134, v113
	v_fmac_f32_e32 v191, v135, v113
	v_fmac_f32_e32 v192, v150, v113
	v_fmac_f32_e32 v193, v151, v113
	v_fmac_f32_e32 v190, v136, v114
	v_fmac_f32_e32 v191, v137, v114
	v_fmac_f32_e32 v192, v152, v114
	v_fmac_f32_e32 v193, v153, v114
	v_fmac_f32_e32 v190, v138, v115
	v_fmac_f32_e32 v191, v139, v115
	v_fmac_f32_e32 v192, v154, v115
	v_fmac_f32_e32 v193, v155, v115
	s_waitcnt vmcnt(34)
	v_cvt_f32_ubyte0_e32 v124, v56
	v_cvt_f32_ubyte1_e32 v126, v56
	v_cvt_f32_ubyte2_e32 v128, v56
	v_cvt_f32_ubyte3_e32 v130, v56
	v_cvt_f32_ubyte0_e32 v132, v57
	v_cvt_f32_ubyte1_e32 v134, v57
	v_cvt_f32_ubyte2_e32 v136, v57
	v_cvt_f32_ubyte3_e32 v138, v57
	s_waitcnt lgkmcnt(0)
	s_load_dwordx16 s[68:83], s[36:37], 0x100 glc
	s_lshl_b32 s30, s84, 12
	s_add_u32 s28, s26, s30
	s_addc_u32 s29, s27, 0
	global_load_dwordx2 v[56:57], v162, s[28:29]
	s_waitcnt vmcnt(34)
	v_cvt_f32_ubyte0_e32 v125, v58
	v_cvt_f32_ubyte1_e32 v127, v58
	v_cvt_f32_ubyte2_e32 v129, v58
	v_cvt_f32_ubyte3_e32 v131, v58
	v_cvt_f32_ubyte0_e32 v133, v59
	v_cvt_f32_ubyte1_e32 v135, v59
	v_cvt_f32_ubyte2_e32 v137, v59
	v_cvt_f32_ubyte3_e32 v139, v59
	s_lshl_b32 s30, s85, 12
	s_add_u32 s28, s26, s30
	s_addc_u32 s29, s27, 0
	global_load_dwordx2 v[58:59], v162, s[28:29]
	s_waitcnt vmcnt(34)
	v_cvt_f32_ubyte0_e32 v140, v60
	v_cvt_f32_ubyte1_e32 v142, v60
	v_cvt_f32_ubyte2_e32 v144, v60
	v_cvt_f32_ubyte3_e32 v146, v60
	v_cvt_f32_ubyte0_e32 v148, v61
	v_cvt_f32_ubyte1_e32 v150, v61
	v_cvt_f32_ubyte2_e32 v152, v61
	v_cvt_f32_ubyte3_e32 v154, v61
	s_lshl_b32 s30, s86, 12
	s_add_u32 s28, s26, s30
	s_addc_u32 s29, s27, 0
	global_load_dwordx2 v[60:61], v162, s[28:29]
	s_waitcnt vmcnt(34)
	v_cvt_f32_ubyte0_e32 v141, v62
	v_cvt_f32_ubyte1_e32 v143, v62
	v_cvt_f32_ubyte2_e32 v145, v62
	v_cvt_f32_ubyte3_e32 v147, v62
	v_cvt_f32_ubyte0_e32 v149, v63
	v_cvt_f32_ubyte1_e32 v151, v63
	v_cvt_f32_ubyte2_e32 v153, v63
	v_cvt_f32_ubyte3_e32 v155, v63
	s_lshl_b32 s30, s87, 12
	s_add_u32 s28, s26, s30
	s_addc_u32 s29, s27, 0
	global_load_dwordx2 v[62:63], v162, s[28:29]
	v_mul_f32_e32 v194, v124, v108
	v_mul_f32_e32 v195, v125, v108
	v_mul_f32_e32 v196, v140, v108
	v_mul_f32_e32 v197, v141, v108
	v_fmac_f32_e32 v194, v126, v109
	v_fmac_f32_e32 v195, v127, v109
	v_fmac_f32_e32 v196, v142, v109
	v_fmac_f32_e32 v197, v143, v109
	v_fmac_f32_e32 v194, v128, v110
	v_fmac_f32_e32 v195, v129, v110
	v_fmac_f32_e32 v196, v144, v110
	v_fmac_f32_e32 v197, v145, v110
	v_fmac_f32_e32 v194, v130, v111
	v_fmac_f32_e32 v195, v131, v111
	v_fmac_f32_e32 v196, v146, v111
	v_fmac_f32_e32 v197, v147, v111
	v_fmac_f32_e32 v194, v132, v112
	v_fmac_f32_e32 v195, v133, v112
	v_fmac_f32_e32 v196, v148, v112
	v_fmac_f32_e32 v197, v149, v112
	v_fmac_f32_e32 v194, v134, v113
	v_fmac_f32_e32 v195, v135, v113
	v_fmac_f32_e32 v196, v150, v113
	v_fmac_f32_e32 v197, v151, v113
	v_fmac_f32_e32 v194, v136, v114
	v_fmac_f32_e32 v195, v137, v114
	v_fmac_f32_e32 v196, v152, v114
	v_fmac_f32_e32 v197, v153, v114
	v_fmac_f32_e32 v194, v138, v115
	v_fmac_f32_e32 v195, v139, v115
	v_fmac_f32_e32 v196, v154, v115
	v_fmac_f32_e32 v197, v155, v115
	s_waitcnt vmcnt(34)
	v_cvt_f32_ubyte0_e32 v124, v64
	v_cvt_f32_ubyte1_e32 v126, v64
	v_cvt_f32_ubyte2_e32 v128, v64
	v_cvt_f32_ubyte3_e32 v130, v64
	v_cvt_f32_ubyte0_e32 v132, v65
	v_cvt_f32_ubyte1_e32 v134, v65
	v_cvt_f32_ubyte2_e32 v136, v65
	v_cvt_f32_ubyte3_e32 v138, v65
	s_lshl_b32 s30, s88, 12
	s_add_u32 s28, s26, s30
	s_addc_u32 s29, s27, 0
	global_load_dwordx2 v[64:65], v162, s[28:29]
	s_waitcnt vmcnt(34)
	v_cvt_f32_ubyte0_e32 v125, v66
	v_cvt_f32_ubyte1_e32 v127, v66
	v_cvt_f32_ubyte2_e32 v129, v66
	v_cvt_f32_ubyte3_e32 v131, v66
	v_cvt_f32_ubyte0_e32 v133, v67
	v_cvt_f32_ubyte1_e32 v135, v67
	v_cvt_f32_ubyte2_e32 v137, v67
	v_cvt_f32_ubyte3_e32 v139, v67
	s_lshl_b32 s30, s89, 12
	s_add_u32 s28, s26, s30
	s_addc_u32 s29, s27, 0
	global_load_dwordx2 v[66:67], v162, s[28:29]
	s_waitcnt vmcnt(34)
	v_cvt_f32_ubyte0_e32 v140, v68
	v_cvt_f32_ubyte1_e32 v142, v68
	v_cvt_f32_ubyte2_e32 v144, v68
	v_cvt_f32_ubyte3_e32 v146, v68
	v_cvt_f32_ubyte0_e32 v148, v69
	v_cvt_f32_ubyte1_e32 v150, v69
	v_cvt_f32_ubyte2_e32 v152, v69
	v_cvt_f32_ubyte3_e32 v154, v69
	s_lshl_b32 s30, s90, 12
	s_add_u32 s28, s26, s30
	s_addc_u32 s29, s27, 0
	global_load_dwordx2 v[68:69], v162, s[28:29]
	s_waitcnt vmcnt(34)
	v_cvt_f32_ubyte0_e32 v141, v70
	v_cvt_f32_ubyte1_e32 v143, v70
	v_cvt_f32_ubyte2_e32 v145, v70
	v_cvt_f32_ubyte3_e32 v147, v70
	v_cvt_f32_ubyte0_e32 v149, v71
	v_cvt_f32_ubyte1_e32 v151, v71
	v_cvt_f32_ubyte2_e32 v153, v71
	v_cvt_f32_ubyte3_e32 v155, v71
	s_lshl_b32 s30, s91, 12
	s_add_u32 s28, s26, s30
	s_addc_u32 s29, s27, 0
	global_load_dwordx2 v[70:71], v162, s[28:29]
	v_mul_f32_e32 v198, v124, v108
	v_mul_f32_e32 v199, v125, v108
	v_mul_f32_e32 v200, v140, v108
	v_mul_f32_e32 v201, v141, v108
	v_fmac_f32_e32 v198, v126, v109
	v_fmac_f32_e32 v199, v127, v109
	v_fmac_f32_e32 v200, v142, v109
	v_fmac_f32_e32 v201, v143, v109
	v_fmac_f32_e32 v198, v128, v110
	v_fmac_f32_e32 v199, v129, v110
	v_fmac_f32_e32 v200, v144, v110
	v_fmac_f32_e32 v201, v145, v110
	v_fmac_f32_e32 v198, v130, v111
	v_fmac_f32_e32 v199, v131, v111
	v_fmac_f32_e32 v200, v146, v111
	v_fmac_f32_e32 v201, v147, v111
	v_fmac_f32_e32 v198, v132, v112
	v_fmac_f32_e32 v199, v133, v112
	v_fmac_f32_e32 v200, v148, v112
	v_fmac_f32_e32 v201, v149, v112
	v_fmac_f32_e32 v198, v134, v113
	v_fmac_f32_e32 v199, v135, v113
	v_fmac_f32_e32 v200, v150, v113
	v_fmac_f32_e32 v201, v151, v113
	v_fmac_f32_e32 v198, v136, v114
	v_fmac_f32_e32 v199, v137, v114
	v_fmac_f32_e32 v200, v152, v114
	v_fmac_f32_e32 v201, v153, v114
	v_fmac_f32_e32 v198, v138, v115
	v_fmac_f32_e32 v199, v139, v115
	v_fmac_f32_e32 v200, v154, v115
	v_fmac_f32_e32 v201, v155, v115
	s_waitcnt vmcnt(34)
	v_cvt_f32_ubyte0_e32 v124, v72
	v_cvt_f32_ubyte1_e32 v126, v72
	v_cvt_f32_ubyte2_e32 v128, v72
	v_cvt_f32_ubyte3_e32 v130, v72
	v_cvt_f32_ubyte0_e32 v132, v73
	v_cvt_f32_ubyte1_e32 v134, v73
	v_cvt_f32_ubyte2_e32 v136, v73
	v_cvt_f32_ubyte3_e32 v138, v73
	s_lshl_b32 s30, s92, 12
	s_add_u32 s28, s26, s30
	s_addc_u32 s29, s27, 0
	global_load_dwordx2 v[72:73], v162, s[28:29]
	s_waitcnt vmcnt(34)
	v_cvt_f32_ubyte0_e32 v125, v74
	v_cvt_f32_ubyte1_e32 v127, v74
	v_cvt_f32_ubyte2_e32 v129, v74
	v_cvt_f32_ubyte3_e32 v131, v74
	v_cvt_f32_ubyte0_e32 v133, v75
	v_cvt_f32_ubyte1_e32 v135, v75
	v_cvt_f32_ubyte2_e32 v137, v75
	v_cvt_f32_ubyte3_e32 v139, v75
	s_lshl_b32 s30, s93, 12
	s_add_u32 s28, s26, s30
	s_addc_u32 s29, s27, 0
	global_load_dwordx2 v[74:75], v162, s[28:29]
	s_waitcnt vmcnt(34)
	v_cvt_f32_ubyte0_e32 v140, v76
	v_cvt_f32_ubyte1_e32 v142, v76
	v_cvt_f32_ubyte2_e32 v144, v76
	v_cvt_f32_ubyte3_e32 v146, v76
	v_cvt_f32_ubyte0_e32 v148, v77
	v_cvt_f32_ubyte1_e32 v150, v77
	v_cvt_f32_ubyte2_e32 v152, v77
	v_cvt_f32_ubyte3_e32 v154, v77
	s_lshl_b32 s30, s94, 12
	s_add_u32 s28, s26, s30
	s_addc_u32 s29, s27, 0
	global_load_dwordx2 v[76:77], v162, s[28:29]
	s_waitcnt vmcnt(34)
	v_cvt_f32_ubyte0_e32 v141, v78
	v_cvt_f32_ubyte1_e32 v143, v78
	v_cvt_f32_ubyte2_e32 v145, v78
	v_cvt_f32_ubyte3_e32 v147, v78
	v_cvt_f32_ubyte0_e32 v149, v79
	v_cvt_f32_ubyte1_e32 v151, v79
	v_cvt_f32_ubyte2_e32 v153, v79
	v_cvt_f32_ubyte3_e32 v155, v79
	s_lshl_b32 s30, s95, 12
	s_add_u32 s28, s26, s30
	s_addc_u32 s29, s27, 0
	global_load_dwordx2 v[78:79], v162, s[28:29]
	v_mul_f32_e32 v202, v124, v108
	v_mul_f32_e32 v203, v125, v108
	v_mul_f32_e32 v204, v140, v108
	v_mul_f32_e32 v205, v141, v108
	v_fmac_f32_e32 v202, v126, v109
	v_fmac_f32_e32 v203, v127, v109
	v_fmac_f32_e32 v204, v142, v109
	v_fmac_f32_e32 v205, v143, v109
	v_fmac_f32_e32 v202, v128, v110
	v_fmac_f32_e32 v203, v129, v110
	v_fmac_f32_e32 v204, v144, v110
	v_fmac_f32_e32 v205, v145, v110
	v_fmac_f32_e32 v202, v130, v111
	v_fmac_f32_e32 v203, v131, v111
	v_fmac_f32_e32 v204, v146, v111
	v_fmac_f32_e32 v205, v147, v111
	v_fmac_f32_e32 v202, v132, v112
	v_fmac_f32_e32 v203, v133, v112
	v_fmac_f32_e32 v204, v148, v112
	v_fmac_f32_e32 v205, v149, v112
	v_fmac_f32_e32 v202, v134, v113
	v_fmac_f32_e32 v203, v135, v113
	v_fmac_f32_e32 v204, v150, v113
	v_fmac_f32_e32 v205, v151, v113
	v_fmac_f32_e32 v202, v136, v114
	v_fmac_f32_e32 v203, v137, v114
	v_fmac_f32_e32 v204, v152, v114
	v_fmac_f32_e32 v205, v153, v114
	v_fmac_f32_e32 v202, v138, v115
	v_fmac_f32_e32 v203, v139, v115
	v_fmac_f32_e32 v204, v154, v115
	v_fmac_f32_e32 v205, v155, v115
	s_waitcnt vmcnt(34)
	v_cvt_f32_ubyte0_e32 v124, v80
	v_cvt_f32_ubyte1_e32 v126, v80
	v_cvt_f32_ubyte2_e32 v128, v80
	v_cvt_f32_ubyte3_e32 v130, v80
	v_cvt_f32_ubyte0_e32 v132, v81
	v_cvt_f32_ubyte1_e32 v134, v81
	v_cvt_f32_ubyte2_e32 v136, v81
	v_cvt_f32_ubyte3_e32 v138, v81
	s_lshl_b32 s30, s96, 12
	s_add_u32 s28, s26, s30
	s_addc_u32 s29, s27, 0
	global_load_dwordx2 v[80:81], v162, s[28:29]
	s_waitcnt vmcnt(34)
	v_cvt_f32_ubyte0_e32 v125, v82
	v_cvt_f32_ubyte1_e32 v127, v82
	v_cvt_f32_ubyte2_e32 v129, v82
	v_cvt_f32_ubyte3_e32 v131, v82
	v_cvt_f32_ubyte0_e32 v133, v83
	v_cvt_f32_ubyte1_e32 v135, v83
	v_cvt_f32_ubyte2_e32 v137, v83
	v_cvt_f32_ubyte3_e32 v139, v83
	s_lshl_b32 s30, s97, 12
	s_add_u32 s28, s26, s30
	s_addc_u32 s29, s27, 0
	global_load_dwordx2 v[82:83], v162, s[28:29]
	s_waitcnt vmcnt(34)
	v_cvt_f32_ubyte0_e32 v140, v84
	v_cvt_f32_ubyte1_e32 v142, v84
	v_cvt_f32_ubyte2_e32 v144, v84
	v_cvt_f32_ubyte3_e32 v146, v84
	v_cvt_f32_ubyte0_e32 v148, v85
	v_cvt_f32_ubyte1_e32 v150, v85
	v_cvt_f32_ubyte2_e32 v152, v85
	v_cvt_f32_ubyte3_e32 v154, v85
	s_lshl_b32 s30, s98, 12
	s_add_u32 s28, s26, s30
	s_addc_u32 s29, s27, 0
	global_load_dwordx2 v[84:85], v162, s[28:29]
	s_waitcnt vmcnt(34)
	v_cvt_f32_ubyte0_e32 v141, v86
	v_cvt_f32_ubyte1_e32 v143, v86
	v_cvt_f32_ubyte2_e32 v145, v86
	v_cvt_f32_ubyte3_e32 v147, v86
	v_cvt_f32_ubyte0_e32 v149, v87
	v_cvt_f32_ubyte1_e32 v151, v87
	v_cvt_f32_ubyte2_e32 v153, v87
	v_cvt_f32_ubyte3_e32 v155, v87
	s_lshl_b32 s30, s99, 12
	s_add_u32 s28, s26, s30
	s_addc_u32 s29, s27, 0
	global_load_dwordx2 v[86:87], v162, s[28:29]
	v_mul_f32_e32 v206, v124, v108
	v_mul_f32_e32 v207, v125, v108
	v_mul_f32_e32 v208, v140, v108
	v_mul_f32_e32 v209, v141, v108
	v_fmac_f32_e32 v206, v126, v109
	v_fmac_f32_e32 v207, v127, v109
	v_fmac_f32_e32 v208, v142, v109
	v_fmac_f32_e32 v209, v143, v109
	v_fmac_f32_e32 v206, v128, v110
	v_fmac_f32_e32 v207, v129, v110
	v_fmac_f32_e32 v208, v144, v110
	v_fmac_f32_e32 v209, v145, v110
	v_fmac_f32_e32 v206, v130, v111
	v_fmac_f32_e32 v207, v131, v111
	v_fmac_f32_e32 v208, v146, v111
	v_fmac_f32_e32 v209, v147, v111
	v_fmac_f32_e32 v206, v132, v112
	v_fmac_f32_e32 v207, v133, v112
	v_fmac_f32_e32 v208, v148, v112
	v_fmac_f32_e32 v209, v149, v112
	v_fmac_f32_e32 v206, v134, v113
	v_fmac_f32_e32 v207, v135, v113
	v_fmac_f32_e32 v208, v150, v113
	v_fmac_f32_e32 v209, v151, v113
	v_fmac_f32_e32 v206, v136, v114
	v_fmac_f32_e32 v207, v137, v114
	v_fmac_f32_e32 v208, v152, v114
	v_fmac_f32_e32 v209, v153, v114
	v_fmac_f32_e32 v206, v138, v115
	v_fmac_f32_e32 v207, v139, v115
	v_fmac_f32_e32 v208, v154, v115
	v_fmac_f32_e32 v209, v155, v115
	v_permlane32_swap_b32_e32 v178, v194
	v_permlane32_swap_b32_e32 v179, v195
	v_permlane32_swap_b32_e32 v180, v196
	v_permlane32_swap_b32_e32 v181, v197
	v_permlane32_swap_b32_e32 v182, v198
	v_permlane32_swap_b32_e32 v183, v199
	v_permlane32_swap_b32_e32 v184, v200
	v_permlane32_swap_b32_e32 v185, v201
	v_permlane32_swap_b32_e32 v186, v202
	v_permlane32_swap_b32_e32 v187, v203
	v_permlane32_swap_b32_e32 v188, v204
	v_permlane32_swap_b32_e32 v189, v205
	v_permlane32_swap_b32_e32 v190, v206
	v_permlane32_swap_b32_e32 v191, v207
	v_permlane32_swap_b32_e32 v192, v208
	v_permlane32_swap_b32_e32 v193, v209
	v_add_f32_e32 v178, v178, v194
	v_add_f32_e32 v179, v179, v195
	v_add_f32_e32 v180, v180, v196
	v_add_f32_e32 v181, v181, v197
	v_add_f32_e32 v182, v182, v198
	v_add_f32_e32 v183, v183, v199
	v_add_f32_e32 v184, v184, v200
	v_add_f32_e32 v185, v185, v201
	v_add_f32_e32 v186, v186, v202
	v_add_f32_e32 v187, v187, v203
	v_add_f32_e32 v188, v188, v204
	v_add_f32_e32 v189, v189, v205
	v_add_f32_e32 v190, v190, v206
	v_add_f32_e32 v191, v191, v207
	v_add_f32_e32 v192, v192, v208
	v_add_f32_e32 v193, v193, v209
	v_permlane16_swap_b32_e32 v178, v186
	v_permlane16_swap_b32_e32 v179, v187
	v_permlane16_swap_b32_e32 v180, v188
	v_permlane16_swap_b32_e32 v181, v189
	v_permlane16_swap_b32_e32 v182, v190
	v_permlane16_swap_b32_e32 v183, v191
	v_permlane16_swap_b32_e32 v184, v192
	v_permlane16_swap_b32_e32 v185, v193
	v_add_f32_e32 v178, v178, v186
	v_add_f32_e32 v179, v179, v187
	v_add_f32_e32 v180, v180, v188
	v_add_f32_e32 v181, v181, v189
	v_add_f32_e32 v182, v182, v190
	v_add_f32_e32 v183, v183, v191
	v_add_f32_e32 v184, v184, v192
	v_add_f32_e32 v185, v185, v193
	v_cndmask_b32_e64 v2, v178, v182, s[8:9]
	v_cndmask_b32_e64 v3, v179, v183, s[8:9]
	v_cndmask_b32_e64 v4, v180, v184, s[8:9]
	v_cndmask_b32_e64 v5, v181, v185, s[8:9]
	v_cndmask_b32_e64 v6, v182, v178, s[8:9]
	v_cndmask_b32_e64 v7, v183, v179, s[8:9]
	v_cndmask_b32_e64 v8, v184, v180, s[8:9]
	v_cndmask_b32_e64 v9, v185, v181, s[8:9]
	v_add_f32_dpp v6, v2, v6 row_ror:8 row_mask:0xf bank_mask:0xf
	v_add_f32_dpp v7, v3, v7 row_ror:8 row_mask:0xf bank_mask:0xf
	v_add_f32_dpp v8, v4, v8 row_ror:8 row_mask:0xf bank_mask:0xf
	v_add_f32_dpp v9, v5, v9 row_ror:8 row_mask:0xf bank_mask:0xf
	v_cndmask_b32_e64 v2, v6, v8, s[10:11]
	v_cndmask_b32_e64 v3, v7, v9, s[10:11]
	v_cndmask_b32_e64 v4, v8, v6, s[10:11]
	v_cndmask_b32_e64 v5, v9, v7, s[10:11]
	v_add_f32_dpp v4, v2, v4 row_half_mirror row_mask:0xf bank_mask:0xf
	v_add_f32_dpp v5, v3, v5 row_half_mirror row_mask:0xf bank_mask:0xf
	v_cndmask_b32_e64 v2, v4, v5, s[14:15]
	v_cndmask_b32_e64 v3, v5, v4, s[14:15]
	s_nop 0
	v_add_f32_dpp v3, v2, v3 quad_perm:[2,3,0,1] row_mask:0xf bank_mask:0xf
	s_nop 1
	v_add_f32_dpp v11, v3, v3 quad_perm:[1,0,3,2] row_mask:0xf bank_mask:0xf
	s_mov_b64 exec, s[2:3]
	global_store_dword v[22:23], v11, off
	s_mov_b64 exec, -1
	s_waitcnt vmcnt(32)
	v_cvt_f32_ubyte0_e32 v124, v24
	v_cvt_f32_ubyte1_e32 v126, v24
	v_cvt_f32_ubyte2_e32 v128, v24
	v_cvt_f32_ubyte3_e32 v130, v24
	v_cvt_f32_ubyte0_e32 v132, v25
	v_cvt_f32_ubyte1_e32 v134, v25
	v_cvt_f32_ubyte2_e32 v136, v25
	v_cvt_f32_ubyte3_e32 v138, v25
	s_waitcnt lgkmcnt(0)
	s_load_dwordx16 s[84:99], s[36:37], 0x140 glc
	s_lshl_b32 s30, s68, 12
	s_add_u32 s28, s26, s30
	s_addc_u32 s29, s27, 0
	global_load_dwordx2 v[24:25], v162, s[28:29]
	s_waitcnt vmcnt(32)
	v_cvt_f32_ubyte0_e32 v125, v26
	v_cvt_f32_ubyte1_e32 v127, v26
	v_cvt_f32_ubyte2_e32 v129, v26
	v_cvt_f32_ubyte3_e32 v131, v26
	v_cvt_f32_ubyte0_e32 v133, v27
	v_cvt_f32_ubyte1_e32 v135, v27
	v_cvt_f32_ubyte2_e32 v137, v27
	v_cvt_f32_ubyte3_e32 v139, v27
	s_lshl_b32 s30, s69, 12
	s_add_u32 s28, s26, s30
	s_addc_u32 s29, s27, 0
	global_load_dwordx2 v[26:27], v162, s[28:29]
	s_waitcnt vmcnt(32)
	v_cvt_f32_ubyte0_e32 v140, v28
	v_cvt_f32_ubyte1_e32 v142, v28
	v_cvt_f32_ubyte2_e32 v144, v28
	v_cvt_f32_ubyte3_e32 v146, v28
	v_cvt_f32_ubyte0_e32 v148, v29
	v_cvt_f32_ubyte1_e32 v150, v29
	v_cvt_f32_ubyte2_e32 v152, v29
	v_cvt_f32_ubyte3_e32 v154, v29
	s_lshl_b32 s30, s70, 12
	s_add_u32 s28, s26, s30
	s_addc_u32 s29, s27, 0
	global_load_dwordx2 v[28:29], v162, s[28:29]
	s_waitcnt vmcnt(32)
	v_cvt_f32_ubyte0_e32 v141, v30
	v_cvt_f32_ubyte1_e32 v143, v30
	v_cvt_f32_ubyte2_e32 v145, v30
	v_cvt_f32_ubyte3_e32 v147, v30
	v_cvt_f32_ubyte0_e32 v149, v31
	v_cvt_f32_ubyte1_e32 v151, v31
	v_cvt_f32_ubyte2_e32 v153, v31
	v_cvt_f32_ubyte3_e32 v155, v31
	s_lshl_b32 s30, s71, 12
	s_add_u32 s28, s26, s30
	s_addc_u32 s29, s27, 0
	global_load_dwordx2 v[30:31], v162, s[28:29]
	v_mul_f32_e32 v178, v124, v108
	v_mul_f32_e32 v179, v125, v108
	v_mul_f32_e32 v180, v140, v108
	v_mul_f32_e32 v181, v141, v108
	v_fmac_f32_e32 v178, v126, v109
	v_fmac_f32_e32 v179, v127, v109
	v_fmac_f32_e32 v180, v142, v109
	v_fmac_f32_e32 v181, v143, v109
	v_fmac_f32_e32 v178, v128, v110
	v_fmac_f32_e32 v179, v129, v110
	v_fmac_f32_e32 v180, v144, v110
	v_fmac_f32_e32 v181, v145, v110
	v_fmac_f32_e32 v178, v130, v111
	v_fmac_f32_e32 v179, v131, v111
	v_fmac_f32_e32 v180, v146, v111
	v_fmac_f32_e32 v181, v147, v111
	v_fmac_f32_e32 v178, v132, v112
	v_fmac_f32_e32 v179, v133, v112
	v_fmac_f32_e32 v180, v148, v112
	v_fmac_f32_e32 v181, v149, v112
	v_fmac_f32_e32 v178, v134, v113
	v_fmac_f32_e32 v179, v135, v113
	v_fmac_f32_e32 v180, v150, v113
	v_fmac_f32_e32 v181, v151, v113
	v_fmac_f32_e32 v178, v136, v114
	v_fmac_f32_e32 v179, v137, v114
	v_fmac_f32_e32 v180, v152, v114
	v_fmac_f32_e32 v181, v153, v114
	v_fmac_f32_e32 v178, v138, v115
	v_fmac_f32_e32 v179, v139, v115
	v_fmac_f32_e32 v180, v154, v115
	v_fmac_f32_e32 v181, v155, v115
	s_waitcnt vmcnt(32)
	v_cvt_f32_ubyte0_e32 v124, v32
	v_cvt_f32_ubyte1_e32 v126, v32
	v_cvt_f32_ubyte2_e32 v128, v32
	v_cvt_f32_ubyte3_e32 v130, v32
	v_cvt_f32_ubyte0_e32 v132, v33
	v_cvt_f32_ubyte1_e32 v134, v33
	v_cvt_f32_ubyte2_e32 v136, v33
	v_cvt_f32_ubyte3_e32 v138, v33
	s_lshl_b32 s30, s72, 12
	s_add_u32 s28, s26, s30
	s_addc_u32 s29, s27, 0
	global_load_dwordx2 v[32:33], v162, s[28:29]
	s_waitcnt vmcnt(32)
	v_cvt_f32_ubyte0_e32 v125, v34
	v_cvt_f32_ubyte1_e32 v127, v34
	v_cvt_f32_ubyte2_e32 v129, v34
	v_cvt_f32_ubyte3_e32 v131, v34
	v_cvt_f32_ubyte0_e32 v133, v35
	v_cvt_f32_ubyte1_e32 v135, v35
	v_cvt_f32_ubyte2_e32 v137, v35
	v_cvt_f32_ubyte3_e32 v139, v35
	s_lshl_b32 s30, s73, 12
	s_add_u32 s28, s26, s30
	s_addc_u32 s29, s27, 0
	global_load_dwordx2 v[34:35], v162, s[28:29]
	s_waitcnt vmcnt(32)
	v_cvt_f32_ubyte0_e32 v140, v36
	v_cvt_f32_ubyte1_e32 v142, v36
	v_cvt_f32_ubyte2_e32 v144, v36
	v_cvt_f32_ubyte3_e32 v146, v36
	v_cvt_f32_ubyte0_e32 v148, v37
	v_cvt_f32_ubyte1_e32 v150, v37
	v_cvt_f32_ubyte2_e32 v152, v37
	v_cvt_f32_ubyte3_e32 v154, v37
	s_lshl_b32 s30, s74, 12
	s_add_u32 s28, s26, s30
	s_addc_u32 s29, s27, 0
	global_load_dwordx2 v[36:37], v162, s[28:29]
	s_waitcnt vmcnt(32)
	v_cvt_f32_ubyte0_e32 v141, v38
	v_cvt_f32_ubyte1_e32 v143, v38
	v_cvt_f32_ubyte2_e32 v145, v38
	v_cvt_f32_ubyte3_e32 v147, v38
	v_cvt_f32_ubyte0_e32 v149, v39
	v_cvt_f32_ubyte1_e32 v151, v39
	v_cvt_f32_ubyte2_e32 v153, v39
	v_cvt_f32_ubyte3_e32 v155, v39
	s_lshl_b32 s30, s75, 12
	s_add_u32 s28, s26, s30
	s_addc_u32 s29, s27, 0
	global_load_dwordx2 v[38:39], v162, s[28:29]
	v_mul_f32_e32 v182, v124, v108
	v_mul_f32_e32 v183, v125, v108
	v_mul_f32_e32 v184, v140, v108
	v_mul_f32_e32 v185, v141, v108
	v_fmac_f32_e32 v182, v126, v109
	v_fmac_f32_e32 v183, v127, v109
	v_fmac_f32_e32 v184, v142, v109
	v_fmac_f32_e32 v185, v143, v109
	v_fmac_f32_e32 v182, v128, v110
	v_fmac_f32_e32 v183, v129, v110
	v_fmac_f32_e32 v184, v144, v110
	v_fmac_f32_e32 v185, v145, v110
	v_fmac_f32_e32 v182, v130, v111
	v_fmac_f32_e32 v183, v131, v111
	v_fmac_f32_e32 v184, v146, v111
	v_fmac_f32_e32 v185, v147, v111
	v_fmac_f32_e32 v182, v132, v112
	v_fmac_f32_e32 v183, v133, v112
	v_fmac_f32_e32 v184, v148, v112
	v_fmac_f32_e32 v185, v149, v112
	v_fmac_f32_e32 v182, v134, v113
	v_fmac_f32_e32 v183, v135, v113
	v_fmac_f32_e32 v184, v150, v113
	v_fmac_f32_e32 v185, v151, v113
	v_fmac_f32_e32 v182, v136, v114
	v_fmac_f32_e32 v183, v137, v114
	v_fmac_f32_e32 v184, v152, v114
	v_fmac_f32_e32 v185, v153, v114
	v_fmac_f32_e32 v182, v138, v115
	v_fmac_f32_e32 v183, v139, v115
	v_fmac_f32_e32 v184, v154, v115
	v_fmac_f32_e32 v185, v155, v115
	s_waitcnt vmcnt(32)
	v_cvt_f32_ubyte0_e32 v124, v40
	v_cvt_f32_ubyte1_e32 v126, v40
	v_cvt_f32_ubyte2_e32 v128, v40
	v_cvt_f32_ubyte3_e32 v130, v40
	v_cvt_f32_ubyte0_e32 v132, v41
	v_cvt_f32_ubyte1_e32 v134, v41
	v_cvt_f32_ubyte2_e32 v136, v41
	v_cvt_f32_ubyte3_e32 v138, v41
	s_lshl_b32 s30, s76, 12
	s_add_u32 s28, s26, s30
	s_addc_u32 s29, s27, 0
	global_load_dwordx2 v[40:41], v162, s[28:29]
	s_waitcnt vmcnt(32)
	v_cvt_f32_ubyte0_e32 v125, v42
	v_cvt_f32_ubyte1_e32 v127, v42
	v_cvt_f32_ubyte2_e32 v129, v42
	v_cvt_f32_ubyte3_e32 v131, v42
	v_cvt_f32_ubyte0_e32 v133, v43
	v_cvt_f32_ubyte1_e32 v135, v43
	v_cvt_f32_ubyte2_e32 v137, v43
	v_cvt_f32_ubyte3_e32 v139, v43
	s_lshl_b32 s30, s77, 12
	s_add_u32 s28, s26, s30
	s_addc_u32 s29, s27, 0
	global_load_dwordx2 v[42:43], v162, s[28:29]
	s_waitcnt vmcnt(32)
	v_cvt_f32_ubyte0_e32 v140, v44
	v_cvt_f32_ubyte1_e32 v142, v44
	v_cvt_f32_ubyte2_e32 v144, v44
	v_cvt_f32_ubyte3_e32 v146, v44
	v_cvt_f32_ubyte0_e32 v148, v45
	v_cvt_f32_ubyte1_e32 v150, v45
	v_cvt_f32_ubyte2_e32 v152, v45
	v_cvt_f32_ubyte3_e32 v154, v45
	s_lshl_b32 s30, s78, 12
	s_add_u32 s28, s26, s30
	s_addc_u32 s29, s27, 0
	global_load_dwordx2 v[44:45], v162, s[28:29]
	s_waitcnt vmcnt(32)
	v_cvt_f32_ubyte0_e32 v141, v46
	v_cvt_f32_ubyte1_e32 v143, v46
	v_cvt_f32_ubyte2_e32 v145, v46
	v_cvt_f32_ubyte3_e32 v147, v46
	v_cvt_f32_ubyte0_e32 v149, v47
	v_cvt_f32_ubyte1_e32 v151, v47
	v_cvt_f32_ubyte2_e32 v153, v47
	v_cvt_f32_ubyte3_e32 v155, v47
	s_lshl_b32 s30, s79, 12
	s_add_u32 s28, s26, s30
	s_addc_u32 s29, s27, 0
	global_load_dwordx2 v[46:47], v162, s[28:29]
	v_mul_f32_e32 v186, v124, v108
	v_mul_f32_e32 v187, v125, v108
	v_mul_f32_e32 v188, v140, v108
	v_mul_f32_e32 v189, v141, v108
	v_fmac_f32_e32 v186, v126, v109
	v_fmac_f32_e32 v187, v127, v109
	v_fmac_f32_e32 v188, v142, v109
	v_fmac_f32_e32 v189, v143, v109
	v_fmac_f32_e32 v186, v128, v110
	v_fmac_f32_e32 v187, v129, v110
	v_fmac_f32_e32 v188, v144, v110
	v_fmac_f32_e32 v189, v145, v110
	v_fmac_f32_e32 v186, v130, v111
	v_fmac_f32_e32 v187, v131, v111
	v_fmac_f32_e32 v188, v146, v111
	v_fmac_f32_e32 v189, v147, v111
	v_fmac_f32_e32 v186, v132, v112
	v_fmac_f32_e32 v187, v133, v112
	v_fmac_f32_e32 v188, v148, v112
	v_fmac_f32_e32 v189, v149, v112
	v_fmac_f32_e32 v186, v134, v113
	v_fmac_f32_e32 v187, v135, v113
	v_fmac_f32_e32 v188, v150, v113
	v_fmac_f32_e32 v189, v151, v113
	v_fmac_f32_e32 v186, v136, v114
	v_fmac_f32_e32 v187, v137, v114
	v_fmac_f32_e32 v188, v152, v114
	v_fmac_f32_e32 v189, v153, v114
	v_fmac_f32_e32 v186, v138, v115
	v_fmac_f32_e32 v187, v139, v115
	v_fmac_f32_e32 v188, v154, v115
	v_fmac_f32_e32 v189, v155, v115
	s_waitcnt vmcnt(32)
	v_cvt_f32_ubyte0_e32 v124, v48
	v_cvt_f32_ubyte1_e32 v126, v48
	v_cvt_f32_ubyte2_e32 v128, v48
	v_cvt_f32_ubyte3_e32 v130, v48
	v_cvt_f32_ubyte0_e32 v132, v49
	v_cvt_f32_ubyte1_e32 v134, v49
	v_cvt_f32_ubyte2_e32 v136, v49
	v_cvt_f32_ubyte3_e32 v138, v49
	s_lshl_b32 s30, s80, 12
	s_add_u32 s28, s26, s30
	s_addc_u32 s29, s27, 0
	global_load_dwordx2 v[48:49], v162, s[28:29]
	s_waitcnt vmcnt(32)
	v_cvt_f32_ubyte0_e32 v125, v50
	v_cvt_f32_ubyte1_e32 v127, v50
	v_cvt_f32_ubyte2_e32 v129, v50
	v_cvt_f32_ubyte3_e32 v131, v50
	v_cvt_f32_ubyte0_e32 v133, v51
	v_cvt_f32_ubyte1_e32 v135, v51
	v_cvt_f32_ubyte2_e32 v137, v51
	v_cvt_f32_ubyte3_e32 v139, v51
	s_lshl_b32 s30, s81, 12
	s_add_u32 s28, s26, s30
	s_addc_u32 s29, s27, 0
	global_load_dwordx2 v[50:51], v162, s[28:29]
	s_waitcnt vmcnt(32)
	v_cvt_f32_ubyte0_e32 v140, v52
	v_cvt_f32_ubyte1_e32 v142, v52
	v_cvt_f32_ubyte2_e32 v144, v52
	v_cvt_f32_ubyte3_e32 v146, v52
	v_cvt_f32_ubyte0_e32 v148, v53
	v_cvt_f32_ubyte1_e32 v150, v53
	v_cvt_f32_ubyte2_e32 v152, v53
	v_cvt_f32_ubyte3_e32 v154, v53
	s_lshl_b32 s30, s82, 12
	s_add_u32 s28, s26, s30
	s_addc_u32 s29, s27, 0
	global_load_dwordx2 v[52:53], v162, s[28:29]
	s_waitcnt vmcnt(32)
	v_cvt_f32_ubyte0_e32 v141, v54
	v_cvt_f32_ubyte1_e32 v143, v54
	v_cvt_f32_ubyte2_e32 v145, v54
	v_cvt_f32_ubyte3_e32 v147, v54
	v_cvt_f32_ubyte0_e32 v149, v55
	v_cvt_f32_ubyte1_e32 v151, v55
	v_cvt_f32_ubyte2_e32 v153, v55
	v_cvt_f32_ubyte3_e32 v155, v55
	s_lshl_b32 s30, s83, 12
	s_add_u32 s28, s26, s30
	s_addc_u32 s29, s27, 0
	global_load_dwordx2 v[54:55], v162, s[28:29]
	v_mul_f32_e32 v190, v124, v108
	v_mul_f32_e32 v191, v125, v108
	v_mul_f32_e32 v192, v140, v108
	v_mul_f32_e32 v193, v141, v108
	v_fmac_f32_e32 v190, v126, v109
	v_fmac_f32_e32 v191, v127, v109
	v_fmac_f32_e32 v192, v142, v109
	v_fmac_f32_e32 v193, v143, v109
	v_fmac_f32_e32 v190, v128, v110
	v_fmac_f32_e32 v191, v129, v110
	v_fmac_f32_e32 v192, v144, v110
	v_fmac_f32_e32 v193, v145, v110
	v_fmac_f32_e32 v190, v130, v111
	v_fmac_f32_e32 v191, v131, v111
	v_fmac_f32_e32 v192, v146, v111
	v_fmac_f32_e32 v193, v147, v111
	v_fmac_f32_e32 v190, v132, v112
	v_fmac_f32_e32 v191, v133, v112
	v_fmac_f32_e32 v192, v148, v112
	v_fmac_f32_e32 v193, v149, v112
	v_fmac_f32_e32 v190, v134, v113
	v_fmac_f32_e32 v191, v135, v113
	v_fmac_f32_e32 v192, v150, v113
	v_fmac_f32_e32 v193, v151, v113
	v_fmac_f32_e32 v190, v136, v114
	v_fmac_f32_e32 v191, v137, v114
	v_fmac_f32_e32 v192, v152, v114
	v_fmac_f32_e32 v193, v153, v114
	v_fmac_f32_e32 v190, v138, v115
	v_fmac_f32_e32 v191, v139, v115
	v_fmac_f32_e32 v192, v154, v115
	v_fmac_f32_e32 v193, v155, v115
	s_waitcnt vmcnt(32)
	v_cvt_f32_ubyte0_e32 v124, v56
	v_cvt_f32_ubyte1_e32 v126, v56
	v_cvt_f32_ubyte2_e32 v128, v56
	v_cvt_f32_ubyte3_e32 v130, v56
	v_cvt_f32_ubyte0_e32 v132, v57
	v_cvt_f32_ubyte1_e32 v134, v57
	v_cvt_f32_ubyte2_e32 v136, v57
	v_cvt_f32_ubyte3_e32 v138, v57
	s_waitcnt lgkmcnt(0)
	s_load_dwordx16 s[68:83], s[36:37], 0x180 glc
	s_lshl_b32 s30, s84, 12
	s_add_u32 s28, s26, s30
	s_addc_u32 s29, s27, 0
	global_load_dwordx2 v[56:57], v162, s[28:29]
	s_waitcnt vmcnt(32)
	v_cvt_f32_ubyte0_e32 v125, v58
	v_cvt_f32_ubyte1_e32 v127, v58
	v_cvt_f32_ubyte2_e32 v129, v58
	v_cvt_f32_ubyte3_e32 v131, v58
	v_cvt_f32_ubyte0_e32 v133, v59
	v_cvt_f32_ubyte1_e32 v135, v59
	v_cvt_f32_ubyte2_e32 v137, v59
	v_cvt_f32_ubyte3_e32 v139, v59
	s_lshl_b32 s30, s85, 12
	s_add_u32 s28, s26, s30
	s_addc_u32 s29, s27, 0
	global_load_dwordx2 v[58:59], v162, s[28:29]
	s_waitcnt vmcnt(32)
	v_cvt_f32_ubyte0_e32 v140, v60
	v_cvt_f32_ubyte1_e32 v142, v60
	v_cvt_f32_ubyte2_e32 v144, v60
	v_cvt_f32_ubyte3_e32 v146, v60
	v_cvt_f32_ubyte0_e32 v148, v61
	v_cvt_f32_ubyte1_e32 v150, v61
	v_cvt_f32_ubyte2_e32 v152, v61
	v_cvt_f32_ubyte3_e32 v154, v61
	s_lshl_b32 s30, s86, 12
	s_add_u32 s28, s26, s30
	s_addc_u32 s29, s27, 0
	global_load_dwordx2 v[60:61], v162, s[28:29]
	s_waitcnt vmcnt(32)
	v_cvt_f32_ubyte0_e32 v141, v62
	v_cvt_f32_ubyte1_e32 v143, v62
	v_cvt_f32_ubyte2_e32 v145, v62
	v_cvt_f32_ubyte3_e32 v147, v62
	v_cvt_f32_ubyte0_e32 v149, v63
	v_cvt_f32_ubyte1_e32 v151, v63
	v_cvt_f32_ubyte2_e32 v153, v63
	v_cvt_f32_ubyte3_e32 v155, v63
	s_lshl_b32 s30, s87, 12
	s_add_u32 s28, s26, s30
	s_addc_u32 s29, s27, 0
	global_load_dwordx2 v[62:63], v162, s[28:29]
	v_mul_f32_e32 v194, v124, v108
	v_mul_f32_e32 v195, v125, v108
	v_mul_f32_e32 v196, v140, v108
	v_mul_f32_e32 v197, v141, v108
	v_fmac_f32_e32 v194, v126, v109
	v_fmac_f32_e32 v195, v127, v109
	v_fmac_f32_e32 v196, v142, v109
	v_fmac_f32_e32 v197, v143, v109
	v_fmac_f32_e32 v194, v128, v110
	v_fmac_f32_e32 v195, v129, v110
	v_fmac_f32_e32 v196, v144, v110
	v_fmac_f32_e32 v197, v145, v110
	v_fmac_f32_e32 v194, v130, v111
	v_fmac_f32_e32 v195, v131, v111
	v_fmac_f32_e32 v196, v146, v111
	v_fmac_f32_e32 v197, v147, v111
	v_fmac_f32_e32 v194, v132, v112
	v_fmac_f32_e32 v195, v133, v112
	v_fmac_f32_e32 v196, v148, v112
	v_fmac_f32_e32 v197, v149, v112
	v_fmac_f32_e32 v194, v134, v113
	v_fmac_f32_e32 v195, v135, v113
	v_fmac_f32_e32 v196, v150, v113
	v_fmac_f32_e32 v197, v151, v113
	v_fmac_f32_e32 v194, v136, v114
	v_fmac_f32_e32 v195, v137, v114
	v_fmac_f32_e32 v196, v152, v114
	v_fmac_f32_e32 v197, v153, v114
	v_fmac_f32_e32 v194, v138, v115
	v_fmac_f32_e32 v195, v139, v115
	v_fmac_f32_e32 v196, v154, v115
	v_fmac_f32_e32 v197, v155, v115
	s_waitcnt vmcnt(32)
	v_cvt_f32_ubyte0_e32 v124, v64
	v_cvt_f32_ubyte1_e32 v126, v64
	v_cvt_f32_ubyte2_e32 v128, v64
	v_cvt_f32_ubyte3_e32 v130, v64
	v_cvt_f32_ubyte0_e32 v132, v65
	v_cvt_f32_ubyte1_e32 v134, v65
	v_cvt_f32_ubyte2_e32 v136, v65
	v_cvt_f32_ubyte3_e32 v138, v65
	s_lshl_b32 s30, s88, 12
	s_add_u32 s28, s26, s30
	s_addc_u32 s29, s27, 0
	global_load_dwordx2 v[64:65], v162, s[28:29]
	s_waitcnt vmcnt(32)
	v_cvt_f32_ubyte0_e32 v125, v66
	v_cvt_f32_ubyte1_e32 v127, v66
	v_cvt_f32_ubyte2_e32 v129, v66
	v_cvt_f32_ubyte3_e32 v131, v66
	v_cvt_f32_ubyte0_e32 v133, v67
	v_cvt_f32_ubyte1_e32 v135, v67
	v_cvt_f32_ubyte2_e32 v137, v67
	v_cvt_f32_ubyte3_e32 v139, v67
	s_lshl_b32 s30, s89, 12
	s_add_u32 s28, s26, s30
	s_addc_u32 s29, s27, 0
	global_load_dwordx2 v[66:67], v162, s[28:29]
	s_waitcnt vmcnt(32)
	v_cvt_f32_ubyte0_e32 v140, v68
	v_cvt_f32_ubyte1_e32 v142, v68
	v_cvt_f32_ubyte2_e32 v144, v68
	v_cvt_f32_ubyte3_e32 v146, v68
	v_cvt_f32_ubyte0_e32 v148, v69
	v_cvt_f32_ubyte1_e32 v150, v69
	v_cvt_f32_ubyte2_e32 v152, v69
	v_cvt_f32_ubyte3_e32 v154, v69
	s_lshl_b32 s30, s90, 12
	s_add_u32 s28, s26, s30
	s_addc_u32 s29, s27, 0
	global_load_dwordx2 v[68:69], v162, s[28:29]
	s_waitcnt vmcnt(32)
	v_cvt_f32_ubyte0_e32 v141, v70
	v_cvt_f32_ubyte1_e32 v143, v70
	v_cvt_f32_ubyte2_e32 v145, v70
	v_cvt_f32_ubyte3_e32 v147, v70
	v_cvt_f32_ubyte0_e32 v149, v71
	v_cvt_f32_ubyte1_e32 v151, v71
	v_cvt_f32_ubyte2_e32 v153, v71
	v_cvt_f32_ubyte3_e32 v155, v71
	s_lshl_b32 s30, s91, 12
	s_add_u32 s28, s26, s30
	s_addc_u32 s29, s27, 0
	global_load_dwordx2 v[70:71], v162, s[28:29]
	v_mul_f32_e32 v198, v124, v108
	v_mul_f32_e32 v199, v125, v108
	v_mul_f32_e32 v200, v140, v108
	v_mul_f32_e32 v201, v141, v108
	v_fmac_f32_e32 v198, v126, v109
	v_fmac_f32_e32 v199, v127, v109
	v_fmac_f32_e32 v200, v142, v109
	v_fmac_f32_e32 v201, v143, v109
	v_fmac_f32_e32 v198, v128, v110
	v_fmac_f32_e32 v199, v129, v110
	v_fmac_f32_e32 v200, v144, v110
	v_fmac_f32_e32 v201, v145, v110
	v_fmac_f32_e32 v198, v130, v111
	v_fmac_f32_e32 v199, v131, v111
	v_fmac_f32_e32 v200, v146, v111
	v_fmac_f32_e32 v201, v147, v111
	v_fmac_f32_e32 v198, v132, v112
	v_fmac_f32_e32 v199, v133, v112
	v_fmac_f32_e32 v200, v148, v112
	v_fmac_f32_e32 v201, v149, v112
	v_fmac_f32_e32 v198, v134, v113
	v_fmac_f32_e32 v199, v135, v113
	v_fmac_f32_e32 v200, v150, v113
	v_fmac_f32_e32 v201, v151, v113
	v_fmac_f32_e32 v198, v136, v114
	v_fmac_f32_e32 v199, v137, v114
	v_fmac_f32_e32 v200, v152, v114
	v_fmac_f32_e32 v201, v153, v114
	v_fmac_f32_e32 v198, v138, v115
	v_fmac_f32_e32 v199, v139, v115
	v_fmac_f32_e32 v200, v154, v115
	v_fmac_f32_e32 v201, v155, v115
	s_waitcnt vmcnt(32)
	v_cvt_f32_ubyte0_e32 v124, v72
	v_cvt_f32_ubyte1_e32 v126, v72
	v_cvt_f32_ubyte2_e32 v128, v72
	v_cvt_f32_ubyte3_e32 v130, v72
	v_cvt_f32_ubyte0_e32 v132, v73
	v_cvt_f32_ubyte1_e32 v134, v73
	v_cvt_f32_ubyte2_e32 v136, v73
	v_cvt_f32_ubyte3_e32 v138, v73
	s_lshl_b32 s30, s92, 12
	s_add_u32 s28, s26, s30
	s_addc_u32 s29, s27, 0
	global_load_dwordx2 v[72:73], v162, s[28:29]
	s_waitcnt vmcnt(32)
	v_cvt_f32_ubyte0_e32 v125, v74
	v_cvt_f32_ubyte1_e32 v127, v74
	v_cvt_f32_ubyte2_e32 v129, v74
	v_cvt_f32_ubyte3_e32 v131, v74
	v_cvt_f32_ubyte0_e32 v133, v75
	v_cvt_f32_ubyte1_e32 v135, v75
	v_cvt_f32_ubyte2_e32 v137, v75
	v_cvt_f32_ubyte3_e32 v139, v75
	s_lshl_b32 s30, s93, 12
	s_add_u32 s28, s26, s30
	s_addc_u32 s29, s27, 0
	global_load_dwordx2 v[74:75], v162, s[28:29]
	s_waitcnt vmcnt(32)
	v_cvt_f32_ubyte0_e32 v140, v76
	v_cvt_f32_ubyte1_e32 v142, v76
	v_cvt_f32_ubyte2_e32 v144, v76
	v_cvt_f32_ubyte3_e32 v146, v76
	v_cvt_f32_ubyte0_e32 v148, v77
	v_cvt_f32_ubyte1_e32 v150, v77
	v_cvt_f32_ubyte2_e32 v152, v77
	v_cvt_f32_ubyte3_e32 v154, v77
	s_lshl_b32 s30, s94, 12
	s_add_u32 s28, s26, s30
	s_addc_u32 s29, s27, 0
	global_load_dwordx2 v[76:77], v162, s[28:29]
	s_waitcnt vmcnt(32)
	v_cvt_f32_ubyte0_e32 v141, v78
	v_cvt_f32_ubyte1_e32 v143, v78
	v_cvt_f32_ubyte2_e32 v145, v78
	v_cvt_f32_ubyte3_e32 v147, v78
	v_cvt_f32_ubyte0_e32 v149, v79
	v_cvt_f32_ubyte1_e32 v151, v79
	v_cvt_f32_ubyte2_e32 v153, v79
	v_cvt_f32_ubyte3_e32 v155, v79
	s_lshl_b32 s30, s95, 12
	s_add_u32 s28, s26, s30
	s_addc_u32 s29, s27, 0
	global_load_dwordx2 v[78:79], v162, s[28:29]
	v_mul_f32_e32 v202, v124, v108
	v_mul_f32_e32 v203, v125, v108
	v_mul_f32_e32 v204, v140, v108
	v_mul_f32_e32 v205, v141, v108
	v_fmac_f32_e32 v202, v126, v109
	v_fmac_f32_e32 v203, v127, v109
	v_fmac_f32_e32 v204, v142, v109
	v_fmac_f32_e32 v205, v143, v109
	v_fmac_f32_e32 v202, v128, v110
	v_fmac_f32_e32 v203, v129, v110
	v_fmac_f32_e32 v204, v144, v110
	v_fmac_f32_e32 v205, v145, v110
	v_fmac_f32_e32 v202, v130, v111
	v_fmac_f32_e32 v203, v131, v111
	v_fmac_f32_e32 v204, v146, v111
	v_fmac_f32_e32 v205, v147, v111
	v_fmac_f32_e32 v202, v132, v112
	v_fmac_f32_e32 v203, v133, v112
	v_fmac_f32_e32 v204, v148, v112
	v_fmac_f32_e32 v205, v149, v112
	v_fmac_f32_e32 v202, v134, v113
	v_fmac_f32_e32 v203, v135, v113
	v_fmac_f32_e32 v204, v150, v113
	v_fmac_f32_e32 v205, v151, v113
	v_fmac_f32_e32 v202, v136, v114
	v_fmac_f32_e32 v203, v137, v114
	v_fmac_f32_e32 v204, v152, v114
	v_fmac_f32_e32 v205, v153, v114
	v_fmac_f32_e32 v202, v138, v115
	v_fmac_f32_e32 v203, v139, v115
	v_fmac_f32_e32 v204, v154, v115
	v_fmac_f32_e32 v205, v155, v115
	s_waitcnt vmcnt(32)
	v_cvt_f32_ubyte0_e32 v124, v80
	v_cvt_f32_ubyte1_e32 v126, v80
	v_cvt_f32_ubyte2_e32 v128, v80
	v_cvt_f32_ubyte3_e32 v130, v80
	v_cvt_f32_ubyte0_e32 v132, v81
	v_cvt_f32_ubyte1_e32 v134, v81
	v_cvt_f32_ubyte2_e32 v136, v81
	v_cvt_f32_ubyte3_e32 v138, v81
	s_lshl_b32 s30, s96, 12
	s_add_u32 s28, s26, s30
	s_addc_u32 s29, s27, 0
	global_load_dwordx2 v[80:81], v162, s[28:29]
	s_waitcnt vmcnt(32)
	v_cvt_f32_ubyte0_e32 v125, v82
	v_cvt_f32_ubyte1_e32 v127, v82
	v_cvt_f32_ubyte2_e32 v129, v82
	v_cvt_f32_ubyte3_e32 v131, v82
	v_cvt_f32_ubyte0_e32 v133, v83
	v_cvt_f32_ubyte1_e32 v135, v83
	v_cvt_f32_ubyte2_e32 v137, v83
	v_cvt_f32_ubyte3_e32 v139, v83
	s_lshl_b32 s30, s97, 12
	s_add_u32 s28, s26, s30
	s_addc_u32 s29, s27, 0
	global_load_dwordx2 v[82:83], v162, s[28:29]
	s_waitcnt vmcnt(32)
	v_cvt_f32_ubyte0_e32 v140, v84
	v_cvt_f32_ubyte1_e32 v142, v84
	v_cvt_f32_ubyte2_e32 v144, v84
	v_cvt_f32_ubyte3_e32 v146, v84
	v_cvt_f32_ubyte0_e32 v148, v85
	v_cvt_f32_ubyte1_e32 v150, v85
	v_cvt_f32_ubyte2_e32 v152, v85
	v_cvt_f32_ubyte3_e32 v154, v85
	s_lshl_b32 s30, s98, 12
	s_add_u32 s28, s26, s30
	s_addc_u32 s29, s27, 0
	global_load_dwordx2 v[84:85], v162, s[28:29]
	s_waitcnt vmcnt(32)
	v_cvt_f32_ubyte0_e32 v141, v86
	v_cvt_f32_ubyte1_e32 v143, v86
	v_cvt_f32_ubyte2_e32 v145, v86
	v_cvt_f32_ubyte3_e32 v147, v86
	v_cvt_f32_ubyte0_e32 v149, v87
	v_cvt_f32_ubyte1_e32 v151, v87
	v_cvt_f32_ubyte2_e32 v153, v87
	v_cvt_f32_ubyte3_e32 v155, v87
	s_lshl_b32 s30, s99, 12
	s_add_u32 s28, s26, s30
	s_addc_u32 s29, s27, 0
	global_load_dwordx2 v[86:87], v162, s[28:29]
	v_mul_f32_e32 v206, v124, v108
	v_mul_f32_e32 v207, v125, v108
	v_mul_f32_e32 v208, v140, v108
	v_mul_f32_e32 v209, v141, v108
	v_fmac_f32_e32 v206, v126, v109
	v_fmac_f32_e32 v207, v127, v109
	v_fmac_f32_e32 v208, v142, v109
	v_fmac_f32_e32 v209, v143, v109
	v_fmac_f32_e32 v206, v128, v110
	v_fmac_f32_e32 v207, v129, v110
	v_fmac_f32_e32 v208, v144, v110
	v_fmac_f32_e32 v209, v145, v110
	v_fmac_f32_e32 v206, v130, v111
	v_fmac_f32_e32 v207, v131, v111
	v_fmac_f32_e32 v208, v146, v111
	v_fmac_f32_e32 v209, v147, v111
	v_fmac_f32_e32 v206, v132, v112
	v_fmac_f32_e32 v207, v133, v112
	v_fmac_f32_e32 v208, v148, v112
	v_fmac_f32_e32 v209, v149, v112
	v_fmac_f32_e32 v206, v134, v113
	v_fmac_f32_e32 v207, v135, v113
	v_fmac_f32_e32 v208, v150, v113
	v_fmac_f32_e32 v209, v151, v113
	v_fmac_f32_e32 v206, v136, v114
	v_fmac_f32_e32 v207, v137, v114
	v_fmac_f32_e32 v208, v152, v114
	v_fmac_f32_e32 v209, v153, v114
	v_fmac_f32_e32 v206, v138, v115
	v_fmac_f32_e32 v207, v139, v115
	v_fmac_f32_e32 v208, v154, v115
	v_fmac_f32_e32 v209, v155, v115
	v_permlane32_swap_b32_e32 v178, v194
	v_permlane32_swap_b32_e32 v179, v195
	v_permlane32_swap_b32_e32 v180, v196
	v_permlane32_swap_b32_e32 v181, v197
	v_permlane32_swap_b32_e32 v182, v198
	v_permlane32_swap_b32_e32 v183, v199
	v_permlane32_swap_b32_e32 v184, v200
	v_permlane32_swap_b32_e32 v185, v201
	v_permlane32_swap_b32_e32 v186, v202
	v_permlane32_swap_b32_e32 v187, v203
	v_permlane32_swap_b32_e32 v188, v204
	v_permlane32_swap_b32_e32 v189, v205
	v_permlane32_swap_b32_e32 v190, v206
	v_permlane32_swap_b32_e32 v191, v207
	v_permlane32_swap_b32_e32 v192, v208
	v_permlane32_swap_b32_e32 v193, v209
	v_add_f32_e32 v178, v178, v194
	v_add_f32_e32 v179, v179, v195
	v_add_f32_e32 v180, v180, v196
	v_add_f32_e32 v181, v181, v197
	v_add_f32_e32 v182, v182, v198
	v_add_f32_e32 v183, v183, v199
	v_add_f32_e32 v184, v184, v200
	v_add_f32_e32 v185, v185, v201
	v_add_f32_e32 v186, v186, v202
	v_add_f32_e32 v187, v187, v203
	v_add_f32_e32 v188, v188, v204
	v_add_f32_e32 v189, v189, v205
	v_add_f32_e32 v190, v190, v206
	v_add_f32_e32 v191, v191, v207
	v_add_f32_e32 v192, v192, v208
	v_add_f32_e32 v193, v193, v209
	v_permlane16_swap_b32_e32 v178, v186
	v_permlane16_swap_b32_e32 v179, v187
	v_permlane16_swap_b32_e32 v180, v188
	v_permlane16_swap_b32_e32 v181, v189
	v_permlane16_swap_b32_e32 v182, v190
	v_permlane16_swap_b32_e32 v183, v191
	v_permlane16_swap_b32_e32 v184, v192
	v_permlane16_swap_b32_e32 v185, v193
	v_add_f32_e32 v178, v178, v186
	v_add_f32_e32 v179, v179, v187
	v_add_f32_e32 v180, v180, v188
	v_add_f32_e32 v181, v181, v189
	v_add_f32_e32 v182, v182, v190
	v_add_f32_e32 v183, v183, v191
	v_add_f32_e32 v184, v184, v192
	v_add_f32_e32 v185, v185, v193
	v_cndmask_b32_e64 v2, v178, v182, s[8:9]
	v_cndmask_b32_e64 v3, v179, v183, s[8:9]
	v_cndmask_b32_e64 v4, v180, v184, s[8:9]
	v_cndmask_b32_e64 v5, v181, v185, s[8:9]
	v_cndmask_b32_e64 v6, v182, v178, s[8:9]
	v_cndmask_b32_e64 v7, v183, v179, s[8:9]
	v_cndmask_b32_e64 v8, v184, v180, s[8:9]
	v_cndmask_b32_e64 v9, v185, v181, s[8:9]
	v_add_f32_dpp v6, v2, v6 row_ror:8 row_mask:0xf bank_mask:0xf
	v_add_f32_dpp v7, v3, v7 row_ror:8 row_mask:0xf bank_mask:0xf
	v_add_f32_dpp v8, v4, v8 row_ror:8 row_mask:0xf bank_mask:0xf
	v_add_f32_dpp v9, v5, v9 row_ror:8 row_mask:0xf bank_mask:0xf
	v_cndmask_b32_e64 v2, v6, v8, s[10:11]
	v_cndmask_b32_e64 v3, v7, v9, s[10:11]
	v_cndmask_b32_e64 v4, v8, v6, s[10:11]
	v_cndmask_b32_e64 v5, v9, v7, s[10:11]
	v_add_f32_dpp v4, v2, v4 row_half_mirror row_mask:0xf bank_mask:0xf
	v_add_f32_dpp v5, v3, v5 row_half_mirror row_mask:0xf bank_mask:0xf
	v_cndmask_b32_e64 v2, v4, v5, s[14:15]
	v_cndmask_b32_e64 v3, v5, v4, s[14:15]
	s_nop 0
	v_add_f32_dpp v3, v2, v3 quad_perm:[2,3,0,1] row_mask:0xf bank_mask:0xf
	s_nop 1
	v_add_f32_dpp v11, v3, v3 quad_perm:[1,0,3,2] row_mask:0xf bank_mask:0xf
	s_mov_b64 exec, s[2:3]
	global_store_dword v[22:23], v11, off offset:128
	s_mov_b64 exec, -1
	s_waitcnt vmcnt(32)
	v_cvt_f32_ubyte0_e32 v124, v24
	v_cvt_f32_ubyte1_e32 v126, v24
	v_cvt_f32_ubyte2_e32 v128, v24
	v_cvt_f32_ubyte3_e32 v130, v24
	v_cvt_f32_ubyte0_e32 v132, v25
	v_cvt_f32_ubyte1_e32 v134, v25
	v_cvt_f32_ubyte2_e32 v136, v25
	v_cvt_f32_ubyte3_e32 v138, v25
	s_waitcnt lgkmcnt(0)
	s_load_dwordx16 s[84:99], s[36:37], 0x1c0 glc
	s_lshl_b32 s30, s68, 12
	s_add_u32 s28, s26, s30
	s_addc_u32 s29, s27, 0
	global_load_dwordx2 v[24:25], v162, s[28:29]
	s_waitcnt vmcnt(32)
	v_cvt_f32_ubyte0_e32 v125, v26
	v_cvt_f32_ubyte1_e32 v127, v26
	v_cvt_f32_ubyte2_e32 v129, v26
	v_cvt_f32_ubyte3_e32 v131, v26
	v_cvt_f32_ubyte0_e32 v133, v27
	v_cvt_f32_ubyte1_e32 v135, v27
	v_cvt_f32_ubyte2_e32 v137, v27
	v_cvt_f32_ubyte3_e32 v139, v27
	s_lshl_b32 s30, s69, 12
	s_add_u32 s28, s26, s30
	s_addc_u32 s29, s27, 0
	global_load_dwordx2 v[26:27], v162, s[28:29]
	s_waitcnt vmcnt(32)
	v_cvt_f32_ubyte0_e32 v140, v28
	v_cvt_f32_ubyte1_e32 v142, v28
	v_cvt_f32_ubyte2_e32 v144, v28
	v_cvt_f32_ubyte3_e32 v146, v28
	v_cvt_f32_ubyte0_e32 v148, v29
	v_cvt_f32_ubyte1_e32 v150, v29
	v_cvt_f32_ubyte2_e32 v152, v29
	v_cvt_f32_ubyte3_e32 v154, v29
	s_lshl_b32 s30, s70, 12
	s_add_u32 s28, s26, s30
	s_addc_u32 s29, s27, 0
	global_load_dwordx2 v[28:29], v162, s[28:29]
	s_waitcnt vmcnt(32)
	v_cvt_f32_ubyte0_e32 v141, v30
	v_cvt_f32_ubyte1_e32 v143, v30
	v_cvt_f32_ubyte2_e32 v145, v30
	v_cvt_f32_ubyte3_e32 v147, v30
	v_cvt_f32_ubyte0_e32 v149, v31
	v_cvt_f32_ubyte1_e32 v151, v31
	v_cvt_f32_ubyte2_e32 v153, v31
	v_cvt_f32_ubyte3_e32 v155, v31
	s_lshl_b32 s30, s71, 12
	s_add_u32 s28, s26, s30
	s_addc_u32 s29, s27, 0
	global_load_dwordx2 v[30:31], v162, s[28:29]
	v_mul_f32_e32 v178, v124, v108
	v_mul_f32_e32 v179, v125, v108
	v_mul_f32_e32 v180, v140, v108
	v_mul_f32_e32 v181, v141, v108
	v_fmac_f32_e32 v178, v126, v109
	v_fmac_f32_e32 v179, v127, v109
	v_fmac_f32_e32 v180, v142, v109
	v_fmac_f32_e32 v181, v143, v109
	v_fmac_f32_e32 v178, v128, v110
	v_fmac_f32_e32 v179, v129, v110
	v_fmac_f32_e32 v180, v144, v110
	v_fmac_f32_e32 v181, v145, v110
	v_fmac_f32_e32 v178, v130, v111
	v_fmac_f32_e32 v179, v131, v111
	v_fmac_f32_e32 v180, v146, v111
	v_fmac_f32_e32 v181, v147, v111
	v_fmac_f32_e32 v178, v132, v112
	v_fmac_f32_e32 v179, v133, v112
	v_fmac_f32_e32 v180, v148, v112
	v_fmac_f32_e32 v181, v149, v112
	v_fmac_f32_e32 v178, v134, v113
	v_fmac_f32_e32 v179, v135, v113
	v_fmac_f32_e32 v180, v150, v113
	v_fmac_f32_e32 v181, v151, v113
	v_fmac_f32_e32 v178, v136, v114
	v_fmac_f32_e32 v179, v137, v114
	v_fmac_f32_e32 v180, v152, v114
	v_fmac_f32_e32 v181, v153, v114
	v_fmac_f32_e32 v178, v138, v115
	v_fmac_f32_e32 v179, v139, v115
	v_fmac_f32_e32 v180, v154, v115
	v_fmac_f32_e32 v181, v155, v115
	s_waitcnt vmcnt(32)
	v_cvt_f32_ubyte0_e32 v124, v32
	v_cvt_f32_ubyte1_e32 v126, v32
	v_cvt_f32_ubyte2_e32 v128, v32
	v_cvt_f32_ubyte3_e32 v130, v32
	v_cvt_f32_ubyte0_e32 v132, v33
	v_cvt_f32_ubyte1_e32 v134, v33
	v_cvt_f32_ubyte2_e32 v136, v33
	v_cvt_f32_ubyte3_e32 v138, v33
	s_lshl_b32 s30, s72, 12
	s_add_u32 s28, s26, s30
	s_addc_u32 s29, s27, 0
	global_load_dwordx2 v[32:33], v162, s[28:29]
	s_waitcnt vmcnt(32)
	v_cvt_f32_ubyte0_e32 v125, v34
	v_cvt_f32_ubyte1_e32 v127, v34
	v_cvt_f32_ubyte2_e32 v129, v34
	v_cvt_f32_ubyte3_e32 v131, v34
	v_cvt_f32_ubyte0_e32 v133, v35
	v_cvt_f32_ubyte1_e32 v135, v35
	v_cvt_f32_ubyte2_e32 v137, v35
	v_cvt_f32_ubyte3_e32 v139, v35
	s_lshl_b32 s30, s73, 12
	s_add_u32 s28, s26, s30
	s_addc_u32 s29, s27, 0
	global_load_dwordx2 v[34:35], v162, s[28:29]
	s_waitcnt vmcnt(32)
	v_cvt_f32_ubyte0_e32 v140, v36
	v_cvt_f32_ubyte1_e32 v142, v36
	v_cvt_f32_ubyte2_e32 v144, v36
	v_cvt_f32_ubyte3_e32 v146, v36
	v_cvt_f32_ubyte0_e32 v148, v37
	v_cvt_f32_ubyte1_e32 v150, v37
	v_cvt_f32_ubyte2_e32 v152, v37
	v_cvt_f32_ubyte3_e32 v154, v37
	s_lshl_b32 s30, s74, 12
	s_add_u32 s28, s26, s30
	s_addc_u32 s29, s27, 0
	global_load_dwordx2 v[36:37], v162, s[28:29]
	s_waitcnt vmcnt(32)
	v_cvt_f32_ubyte0_e32 v141, v38
	v_cvt_f32_ubyte1_e32 v143, v38
	v_cvt_f32_ubyte2_e32 v145, v38
	v_cvt_f32_ubyte3_e32 v147, v38
	v_cvt_f32_ubyte0_e32 v149, v39
	v_cvt_f32_ubyte1_e32 v151, v39
	v_cvt_f32_ubyte2_e32 v153, v39
	v_cvt_f32_ubyte3_e32 v155, v39
	s_lshl_b32 s30, s75, 12
	s_add_u32 s28, s26, s30
	s_addc_u32 s29, s27, 0
	global_load_dwordx2 v[38:39], v162, s[28:29]
	v_mul_f32_e32 v182, v124, v108
	v_mul_f32_e32 v183, v125, v108
	v_mul_f32_e32 v184, v140, v108
	v_mul_f32_e32 v185, v141, v108
	v_fmac_f32_e32 v182, v126, v109
	v_fmac_f32_e32 v183, v127, v109
	v_fmac_f32_e32 v184, v142, v109
	v_fmac_f32_e32 v185, v143, v109
	v_fmac_f32_e32 v182, v128, v110
	v_fmac_f32_e32 v183, v129, v110
	v_fmac_f32_e32 v184, v144, v110
	v_fmac_f32_e32 v185, v145, v110
	v_fmac_f32_e32 v182, v130, v111
	v_fmac_f32_e32 v183, v131, v111
	v_fmac_f32_e32 v184, v146, v111
	v_fmac_f32_e32 v185, v147, v111
	v_fmac_f32_e32 v182, v132, v112
	v_fmac_f32_e32 v183, v133, v112
	v_fmac_f32_e32 v184, v148, v112
	v_fmac_f32_e32 v185, v149, v112
	v_fmac_f32_e32 v182, v134, v113
	v_fmac_f32_e32 v183, v135, v113
	v_fmac_f32_e32 v184, v150, v113
	v_fmac_f32_e32 v185, v151, v113
	v_fmac_f32_e32 v182, v136, v114
	v_fmac_f32_e32 v183, v137, v114
	v_fmac_f32_e32 v184, v152, v114
	v_fmac_f32_e32 v185, v153, v114
	v_fmac_f32_e32 v182, v138, v115
	v_fmac_f32_e32 v183, v139, v115
	v_fmac_f32_e32 v184, v154, v115
	v_fmac_f32_e32 v185, v155, v115
	s_waitcnt vmcnt(32)
	v_cvt_f32_ubyte0_e32 v124, v40
	v_cvt_f32_ubyte1_e32 v126, v40
	v_cvt_f32_ubyte2_e32 v128, v40
	v_cvt_f32_ubyte3_e32 v130, v40
	v_cvt_f32_ubyte0_e32 v132, v41
	v_cvt_f32_ubyte1_e32 v134, v41
	v_cvt_f32_ubyte2_e32 v136, v41
	v_cvt_f32_ubyte3_e32 v138, v41
	s_lshl_b32 s30, s76, 12
	s_add_u32 s28, s26, s30
	s_addc_u32 s29, s27, 0
	global_load_dwordx2 v[40:41], v162, s[28:29]
	s_waitcnt vmcnt(32)
	v_cvt_f32_ubyte0_e32 v125, v42
	v_cvt_f32_ubyte1_e32 v127, v42
	v_cvt_f32_ubyte2_e32 v129, v42
	v_cvt_f32_ubyte3_e32 v131, v42
	v_cvt_f32_ubyte0_e32 v133, v43
	v_cvt_f32_ubyte1_e32 v135, v43
	v_cvt_f32_ubyte2_e32 v137, v43
	v_cvt_f32_ubyte3_e32 v139, v43
	s_lshl_b32 s30, s77, 12
	s_add_u32 s28, s26, s30
	s_addc_u32 s29, s27, 0
	global_load_dwordx2 v[42:43], v162, s[28:29]
	s_waitcnt vmcnt(32)
	v_cvt_f32_ubyte0_e32 v140, v44
	v_cvt_f32_ubyte1_e32 v142, v44
	v_cvt_f32_ubyte2_e32 v144, v44
	v_cvt_f32_ubyte3_e32 v146, v44
	v_cvt_f32_ubyte0_e32 v148, v45
	v_cvt_f32_ubyte1_e32 v150, v45
	v_cvt_f32_ubyte2_e32 v152, v45
	v_cvt_f32_ubyte3_e32 v154, v45
	s_lshl_b32 s30, s78, 12
	s_add_u32 s28, s26, s30
	s_addc_u32 s29, s27, 0
	global_load_dwordx2 v[44:45], v162, s[28:29]
	s_waitcnt vmcnt(32)
	v_cvt_f32_ubyte0_e32 v141, v46
	v_cvt_f32_ubyte1_e32 v143, v46
	v_cvt_f32_ubyte2_e32 v145, v46
	v_cvt_f32_ubyte3_e32 v147, v46
	v_cvt_f32_ubyte0_e32 v149, v47
	v_cvt_f32_ubyte1_e32 v151, v47
	v_cvt_f32_ubyte2_e32 v153, v47
	v_cvt_f32_ubyte3_e32 v155, v47
	s_lshl_b32 s30, s79, 12
	s_add_u32 s28, s26, s30
	s_addc_u32 s29, s27, 0
	global_load_dwordx2 v[46:47], v162, s[28:29]
	v_mul_f32_e32 v186, v124, v108
	v_mul_f32_e32 v187, v125, v108
	v_mul_f32_e32 v188, v140, v108
	v_mul_f32_e32 v189, v141, v108
	v_fmac_f32_e32 v186, v126, v109
	v_fmac_f32_e32 v187, v127, v109
	v_fmac_f32_e32 v188, v142, v109
	v_fmac_f32_e32 v189, v143, v109
	v_fmac_f32_e32 v186, v128, v110
	v_fmac_f32_e32 v187, v129, v110
	v_fmac_f32_e32 v188, v144, v110
	v_fmac_f32_e32 v189, v145, v110
	v_fmac_f32_e32 v186, v130, v111
	v_fmac_f32_e32 v187, v131, v111
	v_fmac_f32_e32 v188, v146, v111
	v_fmac_f32_e32 v189, v147, v111
	v_fmac_f32_e32 v186, v132, v112
	v_fmac_f32_e32 v187, v133, v112
	v_fmac_f32_e32 v188, v148, v112
	v_fmac_f32_e32 v189, v149, v112
	v_fmac_f32_e32 v186, v134, v113
	v_fmac_f32_e32 v187, v135, v113
	v_fmac_f32_e32 v188, v150, v113
	v_fmac_f32_e32 v189, v151, v113
	v_fmac_f32_e32 v186, v136, v114
	v_fmac_f32_e32 v187, v137, v114
	v_fmac_f32_e32 v188, v152, v114
	v_fmac_f32_e32 v189, v153, v114
	v_fmac_f32_e32 v186, v138, v115
	v_fmac_f32_e32 v187, v139, v115
	v_fmac_f32_e32 v188, v154, v115
	v_fmac_f32_e32 v189, v155, v115
	s_waitcnt vmcnt(32)
	v_cvt_f32_ubyte0_e32 v124, v48
	v_cvt_f32_ubyte1_e32 v126, v48
	v_cvt_f32_ubyte2_e32 v128, v48
	v_cvt_f32_ubyte3_e32 v130, v48
	v_cvt_f32_ubyte0_e32 v132, v49
	v_cvt_f32_ubyte1_e32 v134, v49
	v_cvt_f32_ubyte2_e32 v136, v49
	v_cvt_f32_ubyte3_e32 v138, v49
	s_lshl_b32 s30, s80, 12
	s_add_u32 s28, s26, s30
	s_addc_u32 s29, s27, 0
	global_load_dwordx2 v[48:49], v162, s[28:29]
	s_waitcnt vmcnt(32)
	v_cvt_f32_ubyte0_e32 v125, v50
	v_cvt_f32_ubyte1_e32 v127, v50
	v_cvt_f32_ubyte2_e32 v129, v50
	v_cvt_f32_ubyte3_e32 v131, v50
	v_cvt_f32_ubyte0_e32 v133, v51
	v_cvt_f32_ubyte1_e32 v135, v51
	v_cvt_f32_ubyte2_e32 v137, v51
	v_cvt_f32_ubyte3_e32 v139, v51
	s_lshl_b32 s30, s81, 12
	s_add_u32 s28, s26, s30
	s_addc_u32 s29, s27, 0
	global_load_dwordx2 v[50:51], v162, s[28:29]
	s_waitcnt vmcnt(32)
	v_cvt_f32_ubyte0_e32 v140, v52
	v_cvt_f32_ubyte1_e32 v142, v52
	v_cvt_f32_ubyte2_e32 v144, v52
	v_cvt_f32_ubyte3_e32 v146, v52
	v_cvt_f32_ubyte0_e32 v148, v53
	v_cvt_f32_ubyte1_e32 v150, v53
	v_cvt_f32_ubyte2_e32 v152, v53
	v_cvt_f32_ubyte3_e32 v154, v53
	s_lshl_b32 s30, s82, 12
	s_add_u32 s28, s26, s30
	s_addc_u32 s29, s27, 0
	global_load_dwordx2 v[52:53], v162, s[28:29]
	s_waitcnt vmcnt(32)
	v_cvt_f32_ubyte0_e32 v141, v54
	v_cvt_f32_ubyte1_e32 v143, v54
	v_cvt_f32_ubyte2_e32 v145, v54
	v_cvt_f32_ubyte3_e32 v147, v54
	v_cvt_f32_ubyte0_e32 v149, v55
	v_cvt_f32_ubyte1_e32 v151, v55
	v_cvt_f32_ubyte2_e32 v153, v55
	v_cvt_f32_ubyte3_e32 v155, v55
	s_lshl_b32 s30, s83, 12
	s_add_u32 s28, s26, s30
	s_addc_u32 s29, s27, 0
	global_load_dwordx2 v[54:55], v162, s[28:29]
	v_mul_f32_e32 v190, v124, v108
	v_mul_f32_e32 v191, v125, v108
	v_mul_f32_e32 v192, v140, v108
	v_mul_f32_e32 v193, v141, v108
	v_fmac_f32_e32 v190, v126, v109
	v_fmac_f32_e32 v191, v127, v109
	v_fmac_f32_e32 v192, v142, v109
	v_fmac_f32_e32 v193, v143, v109
	v_fmac_f32_e32 v190, v128, v110
	v_fmac_f32_e32 v191, v129, v110
	v_fmac_f32_e32 v192, v144, v110
	v_fmac_f32_e32 v193, v145, v110
	v_fmac_f32_e32 v190, v130, v111
	v_fmac_f32_e32 v191, v131, v111
	v_fmac_f32_e32 v192, v146, v111
	v_fmac_f32_e32 v193, v147, v111
	v_fmac_f32_e32 v190, v132, v112
	v_fmac_f32_e32 v191, v133, v112
	v_fmac_f32_e32 v192, v148, v112
	v_fmac_f32_e32 v193, v149, v112
	v_fmac_f32_e32 v190, v134, v113
	v_fmac_f32_e32 v191, v135, v113
	v_fmac_f32_e32 v192, v150, v113
	v_fmac_f32_e32 v193, v151, v113
	v_fmac_f32_e32 v190, v136, v114
	v_fmac_f32_e32 v191, v137, v114
	v_fmac_f32_e32 v192, v152, v114
	v_fmac_f32_e32 v193, v153, v114
	v_fmac_f32_e32 v190, v138, v115
	v_fmac_f32_e32 v191, v139, v115
	v_fmac_f32_e32 v192, v154, v115
	v_fmac_f32_e32 v193, v155, v115
	s_waitcnt vmcnt(32)
	v_cvt_f32_ubyte0_e32 v124, v56
	v_cvt_f32_ubyte1_e32 v126, v56
	v_cvt_f32_ubyte2_e32 v128, v56
	v_cvt_f32_ubyte3_e32 v130, v56
	v_cvt_f32_ubyte0_e32 v132, v57
	v_cvt_f32_ubyte1_e32 v134, v57
	v_cvt_f32_ubyte2_e32 v136, v57
	v_cvt_f32_ubyte3_e32 v138, v57
	s_waitcnt lgkmcnt(0)
	s_load_dwordx16 s[68:83], s[38:39], 0x0 glc
	s_lshl_b32 s30, s84, 12
	s_add_u32 s28, s26, s30
	s_addc_u32 s29, s27, 0
	global_load_dwordx2 v[56:57], v162, s[28:29]
	s_waitcnt vmcnt(32)
	v_cvt_f32_ubyte0_e32 v125, v58
	v_cvt_f32_ubyte1_e32 v127, v58
	v_cvt_f32_ubyte2_e32 v129, v58
	v_cvt_f32_ubyte3_e32 v131, v58
	v_cvt_f32_ubyte0_e32 v133, v59
	v_cvt_f32_ubyte1_e32 v135, v59
	v_cvt_f32_ubyte2_e32 v137, v59
	v_cvt_f32_ubyte3_e32 v139, v59
	s_lshl_b32 s30, s85, 12
	s_add_u32 s28, s26, s30
	s_addc_u32 s29, s27, 0
	global_load_dwordx2 v[58:59], v162, s[28:29]
	s_waitcnt vmcnt(32)
	v_cvt_f32_ubyte0_e32 v140, v60
	v_cvt_f32_ubyte1_e32 v142, v60
	v_cvt_f32_ubyte2_e32 v144, v60
	v_cvt_f32_ubyte3_e32 v146, v60
	v_cvt_f32_ubyte0_e32 v148, v61
	v_cvt_f32_ubyte1_e32 v150, v61
	v_cvt_f32_ubyte2_e32 v152, v61
	v_cvt_f32_ubyte3_e32 v154, v61
	s_lshl_b32 s30, s86, 12
	s_add_u32 s28, s26, s30
	s_addc_u32 s29, s27, 0
	global_load_dwordx2 v[60:61], v162, s[28:29]
	s_waitcnt vmcnt(32)
	v_cvt_f32_ubyte0_e32 v141, v62
	v_cvt_f32_ubyte1_e32 v143, v62
	v_cvt_f32_ubyte2_e32 v145, v62
	v_cvt_f32_ubyte3_e32 v147, v62
	v_cvt_f32_ubyte0_e32 v149, v63
	v_cvt_f32_ubyte1_e32 v151, v63
	v_cvt_f32_ubyte2_e32 v153, v63
	v_cvt_f32_ubyte3_e32 v155, v63
	s_lshl_b32 s30, s87, 12
	s_add_u32 s28, s26, s30
	s_addc_u32 s29, s27, 0
	global_load_dwordx2 v[62:63], v162, s[28:29]
	v_mul_f32_e32 v194, v124, v108
	v_mul_f32_e32 v195, v125, v108
	v_mul_f32_e32 v196, v140, v108
	v_mul_f32_e32 v197, v141, v108
	v_fmac_f32_e32 v194, v126, v109
	v_fmac_f32_e32 v195, v127, v109
	v_fmac_f32_e32 v196, v142, v109
	v_fmac_f32_e32 v197, v143, v109
	v_fmac_f32_e32 v194, v128, v110
	v_fmac_f32_e32 v195, v129, v110
	v_fmac_f32_e32 v196, v144, v110
	v_fmac_f32_e32 v197, v145, v110
	v_fmac_f32_e32 v194, v130, v111
	v_fmac_f32_e32 v195, v131, v111
	v_fmac_f32_e32 v196, v146, v111
	v_fmac_f32_e32 v197, v147, v111
	v_fmac_f32_e32 v194, v132, v112
	v_fmac_f32_e32 v195, v133, v112
	v_fmac_f32_e32 v196, v148, v112
	v_fmac_f32_e32 v197, v149, v112
	v_fmac_f32_e32 v194, v134, v113
	v_fmac_f32_e32 v195, v135, v113
	v_fmac_f32_e32 v196, v150, v113
	v_fmac_f32_e32 v197, v151, v113
	v_fmac_f32_e32 v194, v136, v114
	v_fmac_f32_e32 v195, v137, v114
	v_fmac_f32_e32 v196, v152, v114
	v_fmac_f32_e32 v197, v153, v114
	v_fmac_f32_e32 v194, v138, v115
	v_fmac_f32_e32 v195, v139, v115
	v_fmac_f32_e32 v196, v154, v115
	v_fmac_f32_e32 v197, v155, v115
	s_waitcnt vmcnt(32)
	v_cvt_f32_ubyte0_e32 v124, v64
	v_cvt_f32_ubyte1_e32 v126, v64
	v_cvt_f32_ubyte2_e32 v128, v64
	v_cvt_f32_ubyte3_e32 v130, v64
	v_cvt_f32_ubyte0_e32 v132, v65
	v_cvt_f32_ubyte1_e32 v134, v65
	v_cvt_f32_ubyte2_e32 v136, v65
	v_cvt_f32_ubyte3_e32 v138, v65
	s_lshl_b32 s30, s88, 12
	s_add_u32 s28, s26, s30
	s_addc_u32 s29, s27, 0
	global_load_dwordx2 v[64:65], v162, s[28:29]
	s_waitcnt vmcnt(32)
	v_cvt_f32_ubyte0_e32 v125, v66
	v_cvt_f32_ubyte1_e32 v127, v66
	v_cvt_f32_ubyte2_e32 v129, v66
	v_cvt_f32_ubyte3_e32 v131, v66
	v_cvt_f32_ubyte0_e32 v133, v67
	v_cvt_f32_ubyte1_e32 v135, v67
	v_cvt_f32_ubyte2_e32 v137, v67
	v_cvt_f32_ubyte3_e32 v139, v67
	s_lshl_b32 s30, s89, 12
	s_add_u32 s28, s26, s30
	s_addc_u32 s29, s27, 0
	global_load_dwordx2 v[66:67], v162, s[28:29]
	s_waitcnt vmcnt(32)
	v_cvt_f32_ubyte0_e32 v140, v68
	v_cvt_f32_ubyte1_e32 v142, v68
	v_cvt_f32_ubyte2_e32 v144, v68
	v_cvt_f32_ubyte3_e32 v146, v68
	v_cvt_f32_ubyte0_e32 v148, v69
	v_cvt_f32_ubyte1_e32 v150, v69
	v_cvt_f32_ubyte2_e32 v152, v69
	v_cvt_f32_ubyte3_e32 v154, v69
	s_lshl_b32 s30, s90, 12
	s_add_u32 s28, s26, s30
	s_addc_u32 s29, s27, 0
	global_load_dwordx2 v[68:69], v162, s[28:29]
	s_waitcnt vmcnt(32)
	v_cvt_f32_ubyte0_e32 v141, v70
	v_cvt_f32_ubyte1_e32 v143, v70
	v_cvt_f32_ubyte2_e32 v145, v70
	v_cvt_f32_ubyte3_e32 v147, v70
	v_cvt_f32_ubyte0_e32 v149, v71
	v_cvt_f32_ubyte1_e32 v151, v71
	v_cvt_f32_ubyte2_e32 v153, v71
	v_cvt_f32_ubyte3_e32 v155, v71
	s_lshl_b32 s30, s91, 12
	s_add_u32 s28, s26, s30
	s_addc_u32 s29, s27, 0
	global_load_dwordx2 v[70:71], v162, s[28:29]
	v_mul_f32_e32 v198, v124, v108
	v_mul_f32_e32 v199, v125, v108
	v_mul_f32_e32 v200, v140, v108
	v_mul_f32_e32 v201, v141, v108
	v_fmac_f32_e32 v198, v126, v109
	v_fmac_f32_e32 v199, v127, v109
	v_fmac_f32_e32 v200, v142, v109
	v_fmac_f32_e32 v201, v143, v109
	v_fmac_f32_e32 v198, v128, v110
	v_fmac_f32_e32 v199, v129, v110
	v_fmac_f32_e32 v200, v144, v110
	v_fmac_f32_e32 v201, v145, v110
	v_fmac_f32_e32 v198, v130, v111
	v_fmac_f32_e32 v199, v131, v111
	v_fmac_f32_e32 v200, v146, v111
	v_fmac_f32_e32 v201, v147, v111
	v_fmac_f32_e32 v198, v132, v112
	v_fmac_f32_e32 v199, v133, v112
	v_fmac_f32_e32 v200, v148, v112
	v_fmac_f32_e32 v201, v149, v112
	v_fmac_f32_e32 v198, v134, v113
	v_fmac_f32_e32 v199, v135, v113
	v_fmac_f32_e32 v200, v150, v113
	v_fmac_f32_e32 v201, v151, v113
	v_fmac_f32_e32 v198, v136, v114
	v_fmac_f32_e32 v199, v137, v114
	v_fmac_f32_e32 v200, v152, v114
	v_fmac_f32_e32 v201, v153, v114
	v_fmac_f32_e32 v198, v138, v115
	v_fmac_f32_e32 v199, v139, v115
	v_fmac_f32_e32 v200, v154, v115
	v_fmac_f32_e32 v201, v155, v115
	s_waitcnt vmcnt(32)
	v_cvt_f32_ubyte0_e32 v124, v72
	v_cvt_f32_ubyte1_e32 v126, v72
	v_cvt_f32_ubyte2_e32 v128, v72
	v_cvt_f32_ubyte3_e32 v130, v72
	v_cvt_f32_ubyte0_e32 v132, v73
	v_cvt_f32_ubyte1_e32 v134, v73
	v_cvt_f32_ubyte2_e32 v136, v73
	v_cvt_f32_ubyte3_e32 v138, v73
	s_lshl_b32 s30, s92, 12
	s_add_u32 s28, s26, s30
	s_addc_u32 s29, s27, 0
	global_load_dwordx2 v[72:73], v162, s[28:29]
	s_waitcnt vmcnt(32)
	v_cvt_f32_ubyte0_e32 v125, v74
	v_cvt_f32_ubyte1_e32 v127, v74
	v_cvt_f32_ubyte2_e32 v129, v74
	v_cvt_f32_ubyte3_e32 v131, v74
	v_cvt_f32_ubyte0_e32 v133, v75
	v_cvt_f32_ubyte1_e32 v135, v75
	v_cvt_f32_ubyte2_e32 v137, v75
	v_cvt_f32_ubyte3_e32 v139, v75
	s_lshl_b32 s30, s93, 12
	s_add_u32 s28, s26, s30
	s_addc_u32 s29, s27, 0
	global_load_dwordx2 v[74:75], v162, s[28:29]
	s_waitcnt vmcnt(32)
	v_cvt_f32_ubyte0_e32 v140, v76
	v_cvt_f32_ubyte1_e32 v142, v76
	v_cvt_f32_ubyte2_e32 v144, v76
	v_cvt_f32_ubyte3_e32 v146, v76
	v_cvt_f32_ubyte0_e32 v148, v77
	v_cvt_f32_ubyte1_e32 v150, v77
	v_cvt_f32_ubyte2_e32 v152, v77
	v_cvt_f32_ubyte3_e32 v154, v77
	s_lshl_b32 s30, s94, 12
	s_add_u32 s28, s26, s30
	s_addc_u32 s29, s27, 0
	global_load_dwordx2 v[76:77], v162, s[28:29]
	s_waitcnt vmcnt(32)
	v_cvt_f32_ubyte0_e32 v141, v78
	v_cvt_f32_ubyte1_e32 v143, v78
	v_cvt_f32_ubyte2_e32 v145, v78
	v_cvt_f32_ubyte3_e32 v147, v78
	v_cvt_f32_ubyte0_e32 v149, v79
	v_cvt_f32_ubyte1_e32 v151, v79
	v_cvt_f32_ubyte2_e32 v153, v79
	v_cvt_f32_ubyte3_e32 v155, v79
	s_lshl_b32 s30, s95, 12
	s_add_u32 s28, s26, s30
	s_addc_u32 s29, s27, 0
	global_load_dwordx2 v[78:79], v162, s[28:29]
	v_mul_f32_e32 v202, v124, v108
	v_mul_f32_e32 v203, v125, v108
	v_mul_f32_e32 v204, v140, v108
	v_mul_f32_e32 v205, v141, v108
	v_fmac_f32_e32 v202, v126, v109
	v_fmac_f32_e32 v203, v127, v109
	v_fmac_f32_e32 v204, v142, v109
	v_fmac_f32_e32 v205, v143, v109
	v_fmac_f32_e32 v202, v128, v110
	v_fmac_f32_e32 v203, v129, v110
	v_fmac_f32_e32 v204, v144, v110
	v_fmac_f32_e32 v205, v145, v110
	v_fmac_f32_e32 v202, v130, v111
	v_fmac_f32_e32 v203, v131, v111
	v_fmac_f32_e32 v204, v146, v111
	v_fmac_f32_e32 v205, v147, v111
	v_fmac_f32_e32 v202, v132, v112
	v_fmac_f32_e32 v203, v133, v112
	v_fmac_f32_e32 v204, v148, v112
	v_fmac_f32_e32 v205, v149, v112
	v_fmac_f32_e32 v202, v134, v113
	v_fmac_f32_e32 v203, v135, v113
	v_fmac_f32_e32 v204, v150, v113
	v_fmac_f32_e32 v205, v151, v113
	v_fmac_f32_e32 v202, v136, v114
	v_fmac_f32_e32 v203, v137, v114
	v_fmac_f32_e32 v204, v152, v114
	v_fmac_f32_e32 v205, v153, v114
	v_fmac_f32_e32 v202, v138, v115
	v_fmac_f32_e32 v203, v139, v115
	v_fmac_f32_e32 v204, v154, v115
	v_fmac_f32_e32 v205, v155, v115
	s_waitcnt vmcnt(32)
	v_cvt_f32_ubyte0_e32 v124, v80
	v_cvt_f32_ubyte1_e32 v126, v80
	v_cvt_f32_ubyte2_e32 v128, v80
	v_cvt_f32_ubyte3_e32 v130, v80
	v_cvt_f32_ubyte0_e32 v132, v81
	v_cvt_f32_ubyte1_e32 v134, v81
	v_cvt_f32_ubyte2_e32 v136, v81
	v_cvt_f32_ubyte3_e32 v138, v81
	s_lshl_b32 s30, s96, 12
	s_add_u32 s28, s26, s30
	s_addc_u32 s29, s27, 0
	global_load_dwordx2 v[80:81], v162, s[28:29]
	s_waitcnt vmcnt(32)
	v_cvt_f32_ubyte0_e32 v125, v82
	v_cvt_f32_ubyte1_e32 v127, v82
	v_cvt_f32_ubyte2_e32 v129, v82
	v_cvt_f32_ubyte3_e32 v131, v82
	v_cvt_f32_ubyte0_e32 v133, v83
	v_cvt_f32_ubyte1_e32 v135, v83
	v_cvt_f32_ubyte2_e32 v137, v83
	v_cvt_f32_ubyte3_e32 v139, v83
	s_lshl_b32 s30, s97, 12
	s_add_u32 s28, s26, s30
	s_addc_u32 s29, s27, 0
	global_load_dwordx2 v[82:83], v162, s[28:29]
	s_waitcnt vmcnt(32)
	v_cvt_f32_ubyte0_e32 v140, v84
	v_cvt_f32_ubyte1_e32 v142, v84
	v_cvt_f32_ubyte2_e32 v144, v84
	v_cvt_f32_ubyte3_e32 v146, v84
	v_cvt_f32_ubyte0_e32 v148, v85
	v_cvt_f32_ubyte1_e32 v150, v85
	v_cvt_f32_ubyte2_e32 v152, v85
	v_cvt_f32_ubyte3_e32 v154, v85
	s_lshl_b32 s30, s98, 12
	s_add_u32 s28, s26, s30
	s_addc_u32 s29, s27, 0
	global_load_dwordx2 v[84:85], v162, s[28:29]
	s_waitcnt vmcnt(32)
	v_cvt_f32_ubyte0_e32 v141, v86
	v_cvt_f32_ubyte1_e32 v143, v86
	v_cvt_f32_ubyte2_e32 v145, v86
	v_cvt_f32_ubyte3_e32 v147, v86
	v_cvt_f32_ubyte0_e32 v149, v87
	v_cvt_f32_ubyte1_e32 v151, v87
	v_cvt_f32_ubyte2_e32 v153, v87
	v_cvt_f32_ubyte3_e32 v155, v87
	s_lshl_b32 s30, s99, 12
	s_add_u32 s28, s26, s30
	s_addc_u32 s29, s27, 0
	global_load_dwordx2 v[86:87], v162, s[28:29]
	v_mul_f32_e32 v206, v124, v108
	v_mul_f32_e32 v207, v125, v108
	v_mul_f32_e32 v208, v140, v108
	v_mul_f32_e32 v209, v141, v108
	v_fmac_f32_e32 v206, v126, v109
	v_fmac_f32_e32 v207, v127, v109
	v_fmac_f32_e32 v208, v142, v109
	v_fmac_f32_e32 v209, v143, v109
	v_fmac_f32_e32 v206, v128, v110
	v_fmac_f32_e32 v207, v129, v110
	v_fmac_f32_e32 v208, v144, v110
	v_fmac_f32_e32 v209, v145, v110
	v_fmac_f32_e32 v206, v130, v111
	v_fmac_f32_e32 v207, v131, v111
	v_fmac_f32_e32 v208, v146, v111
	v_fmac_f32_e32 v209, v147, v111
	v_fmac_f32_e32 v206, v132, v112
	v_fmac_f32_e32 v207, v133, v112
	v_fmac_f32_e32 v208, v148, v112
	v_fmac_f32_e32 v209, v149, v112
	v_fmac_f32_e32 v206, v134, v113
	v_fmac_f32_e32 v207, v135, v113
	v_fmac_f32_e32 v208, v150, v113
	v_fmac_f32_e32 v209, v151, v113
	v_fmac_f32_e32 v206, v136, v114
	v_fmac_f32_e32 v207, v137, v114
	v_fmac_f32_e32 v208, v152, v114
	v_fmac_f32_e32 v209, v153, v114
	v_fmac_f32_e32 v206, v138, v115
	v_fmac_f32_e32 v207, v139, v115
	v_fmac_f32_e32 v208, v154, v115
	v_fmac_f32_e32 v209, v155, v115
	v_permlane32_swap_b32_e32 v178, v194
	v_permlane32_swap_b32_e32 v179, v195
	v_permlane32_swap_b32_e32 v180, v196
	v_permlane32_swap_b32_e32 v181, v197
	v_permlane32_swap_b32_e32 v182, v198
	v_permlane32_swap_b32_e32 v183, v199
	v_permlane32_swap_b32_e32 v184, v200
	v_permlane32_swap_b32_e32 v185, v201
	v_permlane32_swap_b32_e32 v186, v202
	v_permlane32_swap_b32_e32 v187, v203
	v_permlane32_swap_b32_e32 v188, v204
	v_permlane32_swap_b32_e32 v189, v205
	v_permlane32_swap_b32_e32 v190, v206
	v_permlane32_swap_b32_e32 v191, v207
	v_permlane32_swap_b32_e32 v192, v208
	v_permlane32_swap_b32_e32 v193, v209
	v_add_f32_e32 v178, v178, v194
	v_add_f32_e32 v179, v179, v195
	v_add_f32_e32 v180, v180, v196
	v_add_f32_e32 v181, v181, v197
	v_add_f32_e32 v182, v182, v198
	v_add_f32_e32 v183, v183, v199
	v_add_f32_e32 v184, v184, v200
	v_add_f32_e32 v185, v185, v201
	v_add_f32_e32 v186, v186, v202
	v_add_f32_e32 v187, v187, v203
	v_add_f32_e32 v188, v188, v204
	v_add_f32_e32 v189, v189, v205
	v_add_f32_e32 v190, v190, v206
	v_add_f32_e32 v191, v191, v207
	v_add_f32_e32 v192, v192, v208
	v_add_f32_e32 v193, v193, v209
	v_permlane16_swap_b32_e32 v178, v186
	v_permlane16_swap_b32_e32 v179, v187
	v_permlane16_swap_b32_e32 v180, v188
	v_permlane16_swap_b32_e32 v181, v189
	v_permlane16_swap_b32_e32 v182, v190
	v_permlane16_swap_b32_e32 v183, v191
	v_permlane16_swap_b32_e32 v184, v192
	v_permlane16_swap_b32_e32 v185, v193
	v_add_f32_e32 v178, v178, v186
	v_add_f32_e32 v179, v179, v187
	v_add_f32_e32 v180, v180, v188
	v_add_f32_e32 v181, v181, v189
	v_add_f32_e32 v182, v182, v190
	v_add_f32_e32 v183, v183, v191
	v_add_f32_e32 v184, v184, v192
	v_add_f32_e32 v185, v185, v193
	v_cndmask_b32_e64 v2, v178, v182, s[8:9]
	v_cndmask_b32_e64 v3, v179, v183, s[8:9]
	v_cndmask_b32_e64 v4, v180, v184, s[8:9]
	v_cndmask_b32_e64 v5, v181, v185, s[8:9]
	v_cndmask_b32_e64 v6, v182, v178, s[8:9]
	v_cndmask_b32_e64 v7, v183, v179, s[8:9]
	v_cndmask_b32_e64 v8, v184, v180, s[8:9]
	v_cndmask_b32_e64 v9, v185, v181, s[8:9]
	v_add_f32_dpp v6, v2, v6 row_ror:8 row_mask:0xf bank_mask:0xf
	v_add_f32_dpp v7, v3, v7 row_ror:8 row_mask:0xf bank_mask:0xf
	v_add_f32_dpp v8, v4, v8 row_ror:8 row_mask:0xf bank_mask:0xf
	v_add_f32_dpp v9, v5, v9 row_ror:8 row_mask:0xf bank_mask:0xf
	v_cndmask_b32_e64 v2, v6, v8, s[10:11]
	v_cndmask_b32_e64 v3, v7, v9, s[10:11]
	v_cndmask_b32_e64 v4, v8, v6, s[10:11]
	v_cndmask_b32_e64 v5, v9, v7, s[10:11]
	v_add_f32_dpp v4, v2, v4 row_half_mirror row_mask:0xf bank_mask:0xf
	v_add_f32_dpp v5, v3, v5 row_half_mirror row_mask:0xf bank_mask:0xf
	v_cndmask_b32_e64 v2, v4, v5, s[14:15]
	v_cndmask_b32_e64 v3, v5, v4, s[14:15]
	s_nop 0
	v_add_f32_dpp v3, v2, v3 quad_perm:[2,3,0,1] row_mask:0xf bank_mask:0xf
	s_nop 1
	v_add_f32_dpp v11, v3, v3 quad_perm:[1,0,3,2] row_mask:0xf bank_mask:0xf
	s_mov_b64 exec, s[2:3]
	global_store_dword v[22:23], v11, off offset:256
	s_mov_b64 exec, -1
	s_waitcnt vmcnt(32)
	v_cvt_f32_ubyte0_e32 v124, v24
	v_cvt_f32_ubyte1_e32 v126, v24
	v_cvt_f32_ubyte2_e32 v128, v24
	v_cvt_f32_ubyte3_e32 v130, v24
	v_cvt_f32_ubyte0_e32 v132, v25
	v_cvt_f32_ubyte1_e32 v134, v25
	v_cvt_f32_ubyte2_e32 v136, v25
	v_cvt_f32_ubyte3_e32 v138, v25
	s_waitcnt vmcnt(31)
	v_cvt_f32_ubyte0_e32 v125, v26
	v_cvt_f32_ubyte1_e32 v127, v26
	v_cvt_f32_ubyte2_e32 v129, v26
	v_cvt_f32_ubyte3_e32 v131, v26
	v_cvt_f32_ubyte0_e32 v133, v27
	v_cvt_f32_ubyte1_e32 v135, v27
	v_cvt_f32_ubyte2_e32 v137, v27
	v_cvt_f32_ubyte3_e32 v139, v27
	s_waitcnt vmcnt(30)
	v_cvt_f32_ubyte0_e32 v140, v28
	v_cvt_f32_ubyte1_e32 v142, v28
	v_cvt_f32_ubyte2_e32 v144, v28
	v_cvt_f32_ubyte3_e32 v146, v28
	v_cvt_f32_ubyte0_e32 v148, v29
	v_cvt_f32_ubyte1_e32 v150, v29
	v_cvt_f32_ubyte2_e32 v152, v29
	v_cvt_f32_ubyte3_e32 v154, v29
	s_waitcnt vmcnt(29)
	v_cvt_f32_ubyte0_e32 v141, v30
	v_cvt_f32_ubyte1_e32 v143, v30
	v_cvt_f32_ubyte2_e32 v145, v30
	v_cvt_f32_ubyte3_e32 v147, v30
	v_cvt_f32_ubyte0_e32 v149, v31
	v_cvt_f32_ubyte1_e32 v151, v31
	v_cvt_f32_ubyte2_e32 v153, v31
	v_cvt_f32_ubyte3_e32 v155, v31
	v_mul_f32_e32 v178, v124, v108
	v_mul_f32_e32 v179, v125, v108
	v_mul_f32_e32 v180, v140, v108
	v_mul_f32_e32 v181, v141, v108
	v_fmac_f32_e32 v178, v126, v109
	v_fmac_f32_e32 v179, v127, v109
	v_fmac_f32_e32 v180, v142, v109
	v_fmac_f32_e32 v181, v143, v109
	v_fmac_f32_e32 v178, v128, v110
	v_fmac_f32_e32 v179, v129, v110
	v_fmac_f32_e32 v180, v144, v110
	v_fmac_f32_e32 v181, v145, v110
	v_fmac_f32_e32 v178, v130, v111
	v_fmac_f32_e32 v179, v131, v111
	v_fmac_f32_e32 v180, v146, v111
	v_fmac_f32_e32 v181, v147, v111
	v_fmac_f32_e32 v178, v132, v112
	v_fmac_f32_e32 v179, v133, v112
	v_fmac_f32_e32 v180, v148, v112
	v_fmac_f32_e32 v181, v149, v112
	v_fmac_f32_e32 v178, v134, v113
	v_fmac_f32_e32 v179, v135, v113
	v_fmac_f32_e32 v180, v150, v113
	v_fmac_f32_e32 v181, v151, v113
	v_fmac_f32_e32 v178, v136, v114
	v_fmac_f32_e32 v179, v137, v114
	v_fmac_f32_e32 v180, v152, v114
	v_fmac_f32_e32 v181, v153, v114
	v_fmac_f32_e32 v178, v138, v115
	v_fmac_f32_e32 v179, v139, v115
	v_fmac_f32_e32 v180, v154, v115
	v_fmac_f32_e32 v181, v155, v115
	s_waitcnt vmcnt(28)
	v_cvt_f32_ubyte0_e32 v124, v32
	v_cvt_f32_ubyte1_e32 v126, v32
	v_cvt_f32_ubyte2_e32 v128, v32
	v_cvt_f32_ubyte3_e32 v130, v32
	v_cvt_f32_ubyte0_e32 v132, v33
	v_cvt_f32_ubyte1_e32 v134, v33
	v_cvt_f32_ubyte2_e32 v136, v33
	v_cvt_f32_ubyte3_e32 v138, v33
	s_waitcnt vmcnt(27)
	v_cvt_f32_ubyte0_e32 v125, v34
	v_cvt_f32_ubyte1_e32 v127, v34
	v_cvt_f32_ubyte2_e32 v129, v34
	v_cvt_f32_ubyte3_e32 v131, v34
	v_cvt_f32_ubyte0_e32 v133, v35
	v_cvt_f32_ubyte1_e32 v135, v35
	v_cvt_f32_ubyte2_e32 v137, v35
	v_cvt_f32_ubyte3_e32 v139, v35
	s_waitcnt vmcnt(26)
	v_cvt_f32_ubyte0_e32 v140, v36
	v_cvt_f32_ubyte1_e32 v142, v36
	v_cvt_f32_ubyte2_e32 v144, v36
	v_cvt_f32_ubyte3_e32 v146, v36
	v_cvt_f32_ubyte0_e32 v148, v37
	v_cvt_f32_ubyte1_e32 v150, v37
	v_cvt_f32_ubyte2_e32 v152, v37
	v_cvt_f32_ubyte3_e32 v154, v37
	s_waitcnt vmcnt(25)
	v_cvt_f32_ubyte0_e32 v141, v38
	v_cvt_f32_ubyte1_e32 v143, v38
	v_cvt_f32_ubyte2_e32 v145, v38
	v_cvt_f32_ubyte3_e32 v147, v38
	v_cvt_f32_ubyte0_e32 v149, v39
	v_cvt_f32_ubyte1_e32 v151, v39
	v_cvt_f32_ubyte2_e32 v153, v39
	v_cvt_f32_ubyte3_e32 v155, v39
	v_mul_f32_e32 v182, v124, v108
	v_mul_f32_e32 v183, v125, v108
	v_mul_f32_e32 v184, v140, v108
	v_mul_f32_e32 v185, v141, v108
	v_fmac_f32_e32 v182, v126, v109
	v_fmac_f32_e32 v183, v127, v109
	v_fmac_f32_e32 v184, v142, v109
	v_fmac_f32_e32 v185, v143, v109
	v_fmac_f32_e32 v182, v128, v110
	v_fmac_f32_e32 v183, v129, v110
	v_fmac_f32_e32 v184, v144, v110
	v_fmac_f32_e32 v185, v145, v110
	v_fmac_f32_e32 v182, v130, v111
	v_fmac_f32_e32 v183, v131, v111
	v_fmac_f32_e32 v184, v146, v111
	v_fmac_f32_e32 v185, v147, v111
	v_fmac_f32_e32 v182, v132, v112
	v_fmac_f32_e32 v183, v133, v112
	v_fmac_f32_e32 v184, v148, v112
	v_fmac_f32_e32 v185, v149, v112
	v_fmac_f32_e32 v182, v134, v113
	v_fmac_f32_e32 v183, v135, v113
	v_fmac_f32_e32 v184, v150, v113
	v_fmac_f32_e32 v185, v151, v113
	v_fmac_f32_e32 v182, v136, v114
	v_fmac_f32_e32 v183, v137, v114
	v_fmac_f32_e32 v184, v152, v114
	v_fmac_f32_e32 v185, v153, v114
	v_fmac_f32_e32 v182, v138, v115
	v_fmac_f32_e32 v183, v139, v115
	v_fmac_f32_e32 v184, v154, v115
	v_fmac_f32_e32 v185, v155, v115
	s_waitcnt vmcnt(24)
	v_cvt_f32_ubyte0_e32 v124, v40
	v_cvt_f32_ubyte1_e32 v126, v40
	v_cvt_f32_ubyte2_e32 v128, v40
	v_cvt_f32_ubyte3_e32 v130, v40
	v_cvt_f32_ubyte0_e32 v132, v41
	v_cvt_f32_ubyte1_e32 v134, v41
	v_cvt_f32_ubyte2_e32 v136, v41
	v_cvt_f32_ubyte3_e32 v138, v41
	s_waitcnt vmcnt(23)
	v_cvt_f32_ubyte0_e32 v125, v42
	v_cvt_f32_ubyte1_e32 v127, v42
	v_cvt_f32_ubyte2_e32 v129, v42
	v_cvt_f32_ubyte3_e32 v131, v42
	v_cvt_f32_ubyte0_e32 v133, v43
	v_cvt_f32_ubyte1_e32 v135, v43
	v_cvt_f32_ubyte2_e32 v137, v43
	v_cvt_f32_ubyte3_e32 v139, v43
	s_waitcnt vmcnt(22)
	v_cvt_f32_ubyte0_e32 v140, v44
	v_cvt_f32_ubyte1_e32 v142, v44
	v_cvt_f32_ubyte2_e32 v144, v44
	v_cvt_f32_ubyte3_e32 v146, v44
	v_cvt_f32_ubyte0_e32 v148, v45
	v_cvt_f32_ubyte1_e32 v150, v45
	v_cvt_f32_ubyte2_e32 v152, v45
	v_cvt_f32_ubyte3_e32 v154, v45
	s_waitcnt vmcnt(21)
	v_cvt_f32_ubyte0_e32 v141, v46
	v_cvt_f32_ubyte1_e32 v143, v46
	v_cvt_f32_ubyte2_e32 v145, v46
	v_cvt_f32_ubyte3_e32 v147, v46
	v_cvt_f32_ubyte0_e32 v149, v47
	v_cvt_f32_ubyte1_e32 v151, v47
	v_cvt_f32_ubyte2_e32 v153, v47
	v_cvt_f32_ubyte3_e32 v155, v47
	v_mul_f32_e32 v186, v124, v108
	v_mul_f32_e32 v187, v125, v108
	v_mul_f32_e32 v188, v140, v108
	v_mul_f32_e32 v189, v141, v108
	v_fmac_f32_e32 v186, v126, v109
	v_fmac_f32_e32 v187, v127, v109
	v_fmac_f32_e32 v188, v142, v109
	v_fmac_f32_e32 v189, v143, v109
	v_fmac_f32_e32 v186, v128, v110
	v_fmac_f32_e32 v187, v129, v110
	v_fmac_f32_e32 v188, v144, v110
	v_fmac_f32_e32 v189, v145, v110
	v_fmac_f32_e32 v186, v130, v111
	v_fmac_f32_e32 v187, v131, v111
	v_fmac_f32_e32 v188, v146, v111
	v_fmac_f32_e32 v189, v147, v111
	v_fmac_f32_e32 v186, v132, v112
	v_fmac_f32_e32 v187, v133, v112
	v_fmac_f32_e32 v188, v148, v112
	v_fmac_f32_e32 v189, v149, v112
	v_fmac_f32_e32 v186, v134, v113
	v_fmac_f32_e32 v187, v135, v113
	v_fmac_f32_e32 v188, v150, v113
	v_fmac_f32_e32 v189, v151, v113
	v_fmac_f32_e32 v186, v136, v114
	v_fmac_f32_e32 v187, v137, v114
	v_fmac_f32_e32 v188, v152, v114
	v_fmac_f32_e32 v189, v153, v114
	v_fmac_f32_e32 v186, v138, v115
	v_fmac_f32_e32 v187, v139, v115
	v_fmac_f32_e32 v188, v154, v115
	v_fmac_f32_e32 v189, v155, v115
	s_waitcnt vmcnt(20)
	v_cvt_f32_ubyte0_e32 v124, v48
	v_cvt_f32_ubyte1_e32 v126, v48
	v_cvt_f32_ubyte2_e32 v128, v48
	v_cvt_f32_ubyte3_e32 v130, v48
	v_cvt_f32_ubyte0_e32 v132, v49
	v_cvt_f32_ubyte1_e32 v134, v49
	v_cvt_f32_ubyte2_e32 v136, v49
	v_cvt_f32_ubyte3_e32 v138, v49
	s_waitcnt vmcnt(19)
	v_cvt_f32_ubyte0_e32 v125, v50
	v_cvt_f32_ubyte1_e32 v127, v50
	v_cvt_f32_ubyte2_e32 v129, v50
	v_cvt_f32_ubyte3_e32 v131, v50
	v_cvt_f32_ubyte0_e32 v133, v51
	v_cvt_f32_ubyte1_e32 v135, v51
	v_cvt_f32_ubyte2_e32 v137, v51
	v_cvt_f32_ubyte3_e32 v139, v51
	s_waitcnt vmcnt(18)
	v_cvt_f32_ubyte0_e32 v140, v52
	v_cvt_f32_ubyte1_e32 v142, v52
	v_cvt_f32_ubyte2_e32 v144, v52
	v_cvt_f32_ubyte3_e32 v146, v52
	v_cvt_f32_ubyte0_e32 v148, v53
	v_cvt_f32_ubyte1_e32 v150, v53
	v_cvt_f32_ubyte2_e32 v152, v53
	v_cvt_f32_ubyte3_e32 v154, v53
	s_waitcnt vmcnt(17)
	v_cvt_f32_ubyte0_e32 v141, v54
	v_cvt_f32_ubyte1_e32 v143, v54
	v_cvt_f32_ubyte2_e32 v145, v54
	v_cvt_f32_ubyte3_e32 v147, v54
	v_cvt_f32_ubyte0_e32 v149, v55
	v_cvt_f32_ubyte1_e32 v151, v55
	v_cvt_f32_ubyte2_e32 v153, v55
	v_cvt_f32_ubyte3_e32 v155, v55
	v_mul_f32_e32 v190, v124, v108
	v_mul_f32_e32 v191, v125, v108
	v_mul_f32_e32 v192, v140, v108
	v_mul_f32_e32 v193, v141, v108
	v_fmac_f32_e32 v190, v126, v109
	v_fmac_f32_e32 v191, v127, v109
	v_fmac_f32_e32 v192, v142, v109
	v_fmac_f32_e32 v193, v143, v109
	v_fmac_f32_e32 v190, v128, v110
	v_fmac_f32_e32 v191, v129, v110
	v_fmac_f32_e32 v192, v144, v110
	v_fmac_f32_e32 v193, v145, v110
	v_fmac_f32_e32 v190, v130, v111
	v_fmac_f32_e32 v191, v131, v111
	v_fmac_f32_e32 v192, v146, v111
	v_fmac_f32_e32 v193, v147, v111
	v_fmac_f32_e32 v190, v132, v112
	v_fmac_f32_e32 v191, v133, v112
	v_fmac_f32_e32 v192, v148, v112
	v_fmac_f32_e32 v193, v149, v112
	v_fmac_f32_e32 v190, v134, v113
	v_fmac_f32_e32 v191, v135, v113
	v_fmac_f32_e32 v192, v150, v113
	v_fmac_f32_e32 v193, v151, v113
	v_fmac_f32_e32 v190, v136, v114
	v_fmac_f32_e32 v191, v137, v114
	v_fmac_f32_e32 v192, v152, v114
	v_fmac_f32_e32 v193, v153, v114
	v_fmac_f32_e32 v190, v138, v115
	v_fmac_f32_e32 v191, v139, v115
	v_fmac_f32_e32 v192, v154, v115
	v_fmac_f32_e32 v193, v155, v115
	s_waitcnt vmcnt(16)
	v_cvt_f32_ubyte0_e32 v124, v56
	v_cvt_f32_ubyte1_e32 v126, v56
	v_cvt_f32_ubyte2_e32 v128, v56
	v_cvt_f32_ubyte3_e32 v130, v56
	v_cvt_f32_ubyte0_e32 v132, v57
	v_cvt_f32_ubyte1_e32 v134, v57
	v_cvt_f32_ubyte2_e32 v136, v57
	v_cvt_f32_ubyte3_e32 v138, v57
	s_waitcnt vmcnt(15)
	v_cvt_f32_ubyte0_e32 v125, v58
	v_cvt_f32_ubyte1_e32 v127, v58
	v_cvt_f32_ubyte2_e32 v129, v58
	v_cvt_f32_ubyte3_e32 v131, v58
	v_cvt_f32_ubyte0_e32 v133, v59
	v_cvt_f32_ubyte1_e32 v135, v59
	v_cvt_f32_ubyte2_e32 v137, v59
	v_cvt_f32_ubyte3_e32 v139, v59
	s_waitcnt vmcnt(14)
	v_cvt_f32_ubyte0_e32 v140, v60
	v_cvt_f32_ubyte1_e32 v142, v60
	v_cvt_f32_ubyte2_e32 v144, v60
	v_cvt_f32_ubyte3_e32 v146, v60
	v_cvt_f32_ubyte0_e32 v148, v61
	v_cvt_f32_ubyte1_e32 v150, v61
	v_cvt_f32_ubyte2_e32 v152, v61
	v_cvt_f32_ubyte3_e32 v154, v61
	s_waitcnt vmcnt(13)
	v_cvt_f32_ubyte0_e32 v141, v62
	v_cvt_f32_ubyte1_e32 v143, v62
	v_cvt_f32_ubyte2_e32 v145, v62
	v_cvt_f32_ubyte3_e32 v147, v62
	v_cvt_f32_ubyte0_e32 v149, v63
	v_cvt_f32_ubyte1_e32 v151, v63
	v_cvt_f32_ubyte2_e32 v153, v63
	v_cvt_f32_ubyte3_e32 v155, v63
	v_mul_f32_e32 v194, v124, v108
	v_mul_f32_e32 v195, v125, v108
	v_mul_f32_e32 v196, v140, v108
	v_mul_f32_e32 v197, v141, v108
	v_fmac_f32_e32 v194, v126, v109
	v_fmac_f32_e32 v195, v127, v109
	v_fmac_f32_e32 v196, v142, v109
	v_fmac_f32_e32 v197, v143, v109
	v_fmac_f32_e32 v194, v128, v110
	v_fmac_f32_e32 v195, v129, v110
	v_fmac_f32_e32 v196, v144, v110
	v_fmac_f32_e32 v197, v145, v110
	v_fmac_f32_e32 v194, v130, v111
	v_fmac_f32_e32 v195, v131, v111
	v_fmac_f32_e32 v196, v146, v111
	v_fmac_f32_e32 v197, v147, v111
	v_fmac_f32_e32 v194, v132, v112
	v_fmac_f32_e32 v195, v133, v112
	v_fmac_f32_e32 v196, v148, v112
	v_fmac_f32_e32 v197, v149, v112
	v_fmac_f32_e32 v194, v134, v113
	v_fmac_f32_e32 v195, v135, v113
	v_fmac_f32_e32 v196, v150, v113
	v_fmac_f32_e32 v197, v151, v113
	v_fmac_f32_e32 v194, v136, v114
	v_fmac_f32_e32 v195, v137, v114
	v_fmac_f32_e32 v196, v152, v114
	v_fmac_f32_e32 v197, v153, v114
	v_fmac_f32_e32 v194, v138, v115
	v_fmac_f32_e32 v195, v139, v115
	v_fmac_f32_e32 v196, v154, v115
	v_fmac_f32_e32 v197, v155, v115
	s_waitcnt vmcnt(12)
	v_cvt_f32_ubyte0_e32 v124, v64
	v_cvt_f32_ubyte1_e32 v126, v64
	v_cvt_f32_ubyte2_e32 v128, v64
	v_cvt_f32_ubyte3_e32 v130, v64
	v_cvt_f32_ubyte0_e32 v132, v65
	v_cvt_f32_ubyte1_e32 v134, v65
	v_cvt_f32_ubyte2_e32 v136, v65
	v_cvt_f32_ubyte3_e32 v138, v65
	s_waitcnt vmcnt(11)
	v_cvt_f32_ubyte0_e32 v125, v66
	v_cvt_f32_ubyte1_e32 v127, v66
	v_cvt_f32_ubyte2_e32 v129, v66
	v_cvt_f32_ubyte3_e32 v131, v66
	v_cvt_f32_ubyte0_e32 v133, v67
	v_cvt_f32_ubyte1_e32 v135, v67
	v_cvt_f32_ubyte2_e32 v137, v67
	v_cvt_f32_ubyte3_e32 v139, v67
	s_waitcnt vmcnt(10)
	v_cvt_f32_ubyte0_e32 v140, v68
	v_cvt_f32_ubyte1_e32 v142, v68
	v_cvt_f32_ubyte2_e32 v144, v68
	v_cvt_f32_ubyte3_e32 v146, v68
	v_cvt_f32_ubyte0_e32 v148, v69
	v_cvt_f32_ubyte1_e32 v150, v69
	v_cvt_f32_ubyte2_e32 v152, v69
	v_cvt_f32_ubyte3_e32 v154, v69
	s_waitcnt vmcnt(9)
	v_cvt_f32_ubyte0_e32 v141, v70
	v_cvt_f32_ubyte1_e32 v143, v70
	v_cvt_f32_ubyte2_e32 v145, v70
	v_cvt_f32_ubyte3_e32 v147, v70
	v_cvt_f32_ubyte0_e32 v149, v71
	v_cvt_f32_ubyte1_e32 v151, v71
	v_cvt_f32_ubyte2_e32 v153, v71
	v_cvt_f32_ubyte3_e32 v155, v71
	v_mul_f32_e32 v198, v124, v108
	v_mul_f32_e32 v199, v125, v108
	v_mul_f32_e32 v200, v140, v108
	v_mul_f32_e32 v201, v141, v108
	v_fmac_f32_e32 v198, v126, v109
	v_fmac_f32_e32 v199, v127, v109
	v_fmac_f32_e32 v200, v142, v109
	v_fmac_f32_e32 v201, v143, v109
	v_fmac_f32_e32 v198, v128, v110
	v_fmac_f32_e32 v199, v129, v110
	v_fmac_f32_e32 v200, v144, v110
	v_fmac_f32_e32 v201, v145, v110
	v_fmac_f32_e32 v198, v130, v111
	v_fmac_f32_e32 v199, v131, v111
	v_fmac_f32_e32 v200, v146, v111
	v_fmac_f32_e32 v201, v147, v111
	v_fmac_f32_e32 v198, v132, v112
	v_fmac_f32_e32 v199, v133, v112
	v_fmac_f32_e32 v200, v148, v112
	v_fmac_f32_e32 v201, v149, v112
	v_fmac_f32_e32 v198, v134, v113
	v_fmac_f32_e32 v199, v135, v113
	v_fmac_f32_e32 v200, v150, v113
	v_fmac_f32_e32 v201, v151, v113
	v_fmac_f32_e32 v198, v136, v114
	v_fmac_f32_e32 v199, v137, v114
	v_fmac_f32_e32 v200, v152, v114
	v_fmac_f32_e32 v201, v153, v114
	v_fmac_f32_e32 v198, v138, v115
	v_fmac_f32_e32 v199, v139, v115
	v_fmac_f32_e32 v200, v154, v115
	v_fmac_f32_e32 v201, v155, v115
	s_waitcnt vmcnt(8)
	v_cvt_f32_ubyte0_e32 v124, v72
	v_cvt_f32_ubyte1_e32 v126, v72
	v_cvt_f32_ubyte2_e32 v128, v72
	v_cvt_f32_ubyte3_e32 v130, v72
	v_cvt_f32_ubyte0_e32 v132, v73
	v_cvt_f32_ubyte1_e32 v134, v73
	v_cvt_f32_ubyte2_e32 v136, v73
	v_cvt_f32_ubyte3_e32 v138, v73
	s_waitcnt vmcnt(7)
	v_cvt_f32_ubyte0_e32 v125, v74
	v_cvt_f32_ubyte1_e32 v127, v74
	v_cvt_f32_ubyte2_e32 v129, v74
	v_cvt_f32_ubyte3_e32 v131, v74
	v_cvt_f32_ubyte0_e32 v133, v75
	v_cvt_f32_ubyte1_e32 v135, v75
	v_cvt_f32_ubyte2_e32 v137, v75
	v_cvt_f32_ubyte3_e32 v139, v75
	s_waitcnt vmcnt(6)
	v_cvt_f32_ubyte0_e32 v140, v76
	v_cvt_f32_ubyte1_e32 v142, v76
	v_cvt_f32_ubyte2_e32 v144, v76
	v_cvt_f32_ubyte3_e32 v146, v76
	v_cvt_f32_ubyte0_e32 v148, v77
	v_cvt_f32_ubyte1_e32 v150, v77
	v_cvt_f32_ubyte2_e32 v152, v77
	v_cvt_f32_ubyte3_e32 v154, v77
	s_waitcnt vmcnt(5)
	v_cvt_f32_ubyte0_e32 v141, v78
	v_cvt_f32_ubyte1_e32 v143, v78
	v_cvt_f32_ubyte2_e32 v145, v78
	v_cvt_f32_ubyte3_e32 v147, v78
	v_cvt_f32_ubyte0_e32 v149, v79
	v_cvt_f32_ubyte1_e32 v151, v79
	v_cvt_f32_ubyte2_e32 v153, v79
	v_cvt_f32_ubyte3_e32 v155, v79
	v_mul_f32_e32 v202, v124, v108
	v_mul_f32_e32 v203, v125, v108
	v_mul_f32_e32 v204, v140, v108
	v_mul_f32_e32 v205, v141, v108
	v_fmac_f32_e32 v202, v126, v109
	v_fmac_f32_e32 v203, v127, v109
	v_fmac_f32_e32 v204, v142, v109
	v_fmac_f32_e32 v205, v143, v109
	v_fmac_f32_e32 v202, v128, v110
	v_fmac_f32_e32 v203, v129, v110
	v_fmac_f32_e32 v204, v144, v110
	v_fmac_f32_e32 v205, v145, v110
	v_fmac_f32_e32 v202, v130, v111
	v_fmac_f32_e32 v203, v131, v111
	v_fmac_f32_e32 v204, v146, v111
	v_fmac_f32_e32 v205, v147, v111
	v_fmac_f32_e32 v202, v132, v112
	v_fmac_f32_e32 v203, v133, v112
	v_fmac_f32_e32 v204, v148, v112
	v_fmac_f32_e32 v205, v149, v112
	v_fmac_f32_e32 v202, v134, v113
	v_fmac_f32_e32 v203, v135, v113
	v_fmac_f32_e32 v204, v150, v113
	v_fmac_f32_e32 v205, v151, v113
	v_fmac_f32_e32 v202, v136, v114
	v_fmac_f32_e32 v203, v137, v114
	v_fmac_f32_e32 v204, v152, v114
	v_fmac_f32_e32 v205, v153, v114
	v_fmac_f32_e32 v202, v138, v115
	v_fmac_f32_e32 v203, v139, v115
	v_fmac_f32_e32 v204, v154, v115
	v_fmac_f32_e32 v205, v155, v115
	s_waitcnt vmcnt(4)
	v_cvt_f32_ubyte0_e32 v124, v80
	v_cvt_f32_ubyte1_e32 v126, v80
	v_cvt_f32_ubyte2_e32 v128, v80
	v_cvt_f32_ubyte3_e32 v130, v80
	v_cvt_f32_ubyte0_e32 v132, v81
	v_cvt_f32_ubyte1_e32 v134, v81
	v_cvt_f32_ubyte2_e32 v136, v81
	v_cvt_f32_ubyte3_e32 v138, v81
	s_waitcnt vmcnt(3)
	v_cvt_f32_ubyte0_e32 v125, v82
	v_cvt_f32_ubyte1_e32 v127, v82
	v_cvt_f32_ubyte2_e32 v129, v82
	v_cvt_f32_ubyte3_e32 v131, v82
	v_cvt_f32_ubyte0_e32 v133, v83
	v_cvt_f32_ubyte1_e32 v135, v83
	v_cvt_f32_ubyte2_e32 v137, v83
	v_cvt_f32_ubyte3_e32 v139, v83
	s_waitcnt vmcnt(2)
	v_cvt_f32_ubyte0_e32 v140, v84
	v_cvt_f32_ubyte1_e32 v142, v84
	v_cvt_f32_ubyte2_e32 v144, v84
	v_cvt_f32_ubyte3_e32 v146, v84
	v_cvt_f32_ubyte0_e32 v148, v85
	v_cvt_f32_ubyte1_e32 v150, v85
	v_cvt_f32_ubyte2_e32 v152, v85
	v_cvt_f32_ubyte3_e32 v154, v85
	s_waitcnt vmcnt(1)
	v_cvt_f32_ubyte0_e32 v141, v86
	v_cvt_f32_ubyte1_e32 v143, v86
	v_cvt_f32_ubyte2_e32 v145, v86
	v_cvt_f32_ubyte3_e32 v147, v86
	v_cvt_f32_ubyte0_e32 v149, v87
	v_cvt_f32_ubyte1_e32 v151, v87
	v_cvt_f32_ubyte2_e32 v153, v87
	v_cvt_f32_ubyte3_e32 v155, v87
	v_mul_f32_e32 v206, v124, v108
	v_mul_f32_e32 v207, v125, v108
	v_mul_f32_e32 v208, v140, v108
	v_mul_f32_e32 v209, v141, v108
	v_fmac_f32_e32 v206, v126, v109
	v_fmac_f32_e32 v207, v127, v109
	v_fmac_f32_e32 v208, v142, v109
	v_fmac_f32_e32 v209, v143, v109
	v_fmac_f32_e32 v206, v128, v110
	v_fmac_f32_e32 v207, v129, v110
	v_fmac_f32_e32 v208, v144, v110
	v_fmac_f32_e32 v209, v145, v110
	v_fmac_f32_e32 v206, v130, v111
	v_fmac_f32_e32 v207, v131, v111
	v_fmac_f32_e32 v208, v146, v111
	v_fmac_f32_e32 v209, v147, v111
	v_fmac_f32_e32 v206, v132, v112
	v_fmac_f32_e32 v207, v133, v112
	v_fmac_f32_e32 v208, v148, v112
	v_fmac_f32_e32 v209, v149, v112
	v_fmac_f32_e32 v206, v134, v113
	v_fmac_f32_e32 v207, v135, v113
	v_fmac_f32_e32 v208, v150, v113
	v_fmac_f32_e32 v209, v151, v113
	v_fmac_f32_e32 v206, v136, v114
	v_fmac_f32_e32 v207, v137, v114
	v_fmac_f32_e32 v208, v152, v114
	v_fmac_f32_e32 v209, v153, v114
	v_fmac_f32_e32 v206, v138, v115
	v_fmac_f32_e32 v207, v139, v115
	v_fmac_f32_e32 v208, v154, v115
	v_fmac_f32_e32 v209, v155, v115
	s_waitcnt lgkmcnt(0)
	s_load_dwordx16 s[84:99], s[38:39], 0x40 glc
	s_lshl_b32 s30, s68, 12
	s_add_u32 s28, s26, s30
	s_addc_u32 s29, s27, 0
	global_load_dwordx2 v[24:25], v162, s[28:29]
	s_lshl_b32 s30, s69, 12
	s_add_u32 s28, s26, s30
	s_addc_u32 s29, s27, 0
	global_load_dwordx2 v[26:27], v162, s[28:29]
	s_lshl_b32 s30, s70, 12
	s_add_u32 s28, s26, s30
	s_addc_u32 s29, s27, 0
	global_load_dwordx2 v[28:29], v162, s[28:29]
	s_lshl_b32 s30, s71, 12
	s_add_u32 s28, s26, s30
	s_addc_u32 s29, s27, 0
	global_load_dwordx2 v[30:31], v162, s[28:29]
	s_lshl_b32 s30, s72, 12
	s_add_u32 s28, s26, s30
	s_addc_u32 s29, s27, 0
	global_load_dwordx2 v[32:33], v162, s[28:29]
	s_lshl_b32 s30, s73, 12
	s_add_u32 s28, s26, s30
	s_addc_u32 s29, s27, 0
	global_load_dwordx2 v[34:35], v162, s[28:29]
	s_lshl_b32 s30, s74, 12
	s_add_u32 s28, s26, s30
	s_addc_u32 s29, s27, 0
	global_load_dwordx2 v[36:37], v162, s[28:29]
	s_lshl_b32 s30, s75, 12
	s_add_u32 s28, s26, s30
	s_addc_u32 s29, s27, 0
	global_load_dwordx2 v[38:39], v162, s[28:29]
	s_lshl_b32 s30, s76, 12
	s_add_u32 s28, s26, s30
	s_addc_u32 s29, s27, 0
	global_load_dwordx2 v[40:41], v162, s[28:29]
	s_lshl_b32 s30, s77, 12
	s_add_u32 s28, s26, s30
	s_addc_u32 s29, s27, 0
	global_load_dwordx2 v[42:43], v162, s[28:29]
	s_lshl_b32 s30, s78, 12
	s_add_u32 s28, s26, s30
	s_addc_u32 s29, s27, 0
	global_load_dwordx2 v[44:45], v162, s[28:29]
	s_lshl_b32 s30, s79, 12
	s_add_u32 s28, s26, s30
	s_addc_u32 s29, s27, 0
	global_load_dwordx2 v[46:47], v162, s[28:29]
	s_lshl_b32 s30, s80, 12
	s_add_u32 s28, s26, s30
	s_addc_u32 s29, s27, 0
	global_load_dwordx2 v[48:49], v162, s[28:29]
	s_lshl_b32 s30, s81, 12
	s_add_u32 s28, s26, s30
	s_addc_u32 s29, s27, 0
	global_load_dwordx2 v[50:51], v162, s[28:29]
	s_lshl_b32 s30, s82, 12
	s_add_u32 s28, s26, s30
	s_addc_u32 s29, s27, 0
	global_load_dwordx2 v[52:53], v162, s[28:29]
	s_lshl_b32 s30, s83, 12
	s_add_u32 s28, s26, s30
	s_addc_u32 s29, s27, 0
	global_load_dwordx2 v[54:55], v162, s[28:29]
	s_waitcnt lgkmcnt(0)
	s_load_dwordx16 s[68:83], s[38:39], 0x80 glc
	s_lshl_b32 s30, s84, 12
	s_add_u32 s28, s26, s30
	s_addc_u32 s29, s27, 0
	global_load_dwordx2 v[56:57], v162, s[28:29]
	s_lshl_b32 s30, s85, 12
	s_add_u32 s28, s26, s30
	s_addc_u32 s29, s27, 0
	global_load_dwordx2 v[58:59], v162, s[28:29]
	s_lshl_b32 s30, s86, 12
	s_add_u32 s28, s26, s30
	s_addc_u32 s29, s27, 0
	global_load_dwordx2 v[60:61], v162, s[28:29]
	s_lshl_b32 s30, s87, 12
	s_add_u32 s28, s26, s30
	s_addc_u32 s29, s27, 0
	global_load_dwordx2 v[62:63], v162, s[28:29]
	s_lshl_b32 s30, s88, 12
	s_add_u32 s28, s26, s30
	s_addc_u32 s29, s27, 0
	global_load_dwordx2 v[64:65], v162, s[28:29]
	s_lshl_b32 s30, s89, 12
	s_add_u32 s28, s26, s30
	s_addc_u32 s29, s27, 0
	global_load_dwordx2 v[66:67], v162, s[28:29]
	s_lshl_b32 s30, s90, 12
	s_add_u32 s28, s26, s30
	s_addc_u32 s29, s27, 0
	global_load_dwordx2 v[68:69], v162, s[28:29]
	s_lshl_b32 s30, s91, 12
	s_add_u32 s28, s26, s30
	s_addc_u32 s29, s27, 0
	global_load_dwordx2 v[70:71], v162, s[28:29]
	s_lshl_b32 s30, s92, 12
	s_add_u32 s28, s26, s30
	s_addc_u32 s29, s27, 0
	global_load_dwordx2 v[72:73], v162, s[28:29]
	s_lshl_b32 s30, s93, 12
	s_add_u32 s28, s26, s30
	s_addc_u32 s29, s27, 0
	global_load_dwordx2 v[74:75], v162, s[28:29]
	s_lshl_b32 s30, s94, 12
	s_add_u32 s28, s26, s30
	s_addc_u32 s29, s27, 0
	global_load_dwordx2 v[76:77], v162, s[28:29]
	s_lshl_b32 s30, s95, 12
	s_add_u32 s28, s26, s30
	s_addc_u32 s29, s27, 0
	global_load_dwordx2 v[78:79], v162, s[28:29]
	s_lshl_b32 s30, s96, 12
	s_add_u32 s28, s26, s30
	s_addc_u32 s29, s27, 0
	global_load_dwordx2 v[80:81], v162, s[28:29]
	s_lshl_b32 s30, s97, 12
	s_add_u32 s28, s26, s30
	s_addc_u32 s29, s27, 0
	global_load_dwordx2 v[82:83], v162, s[28:29]
	s_lshl_b32 s30, s98, 12
	s_add_u32 s28, s26, s30
	s_addc_u32 s29, s27, 0
	global_load_dwordx2 v[84:85], v162, s[28:29]
	s_lshl_b32 s30, s99, 12
	s_add_u32 s28, s26, s30
	s_addc_u32 s29, s27, 0
	global_load_dwordx2 v[86:87], v162, s[28:29]
	v_permlane32_swap_b32_e32 v178, v194
	v_permlane32_swap_b32_e32 v179, v195
	v_permlane32_swap_b32_e32 v180, v196
	v_permlane32_swap_b32_e32 v181, v197
	v_permlane32_swap_b32_e32 v182, v198
	v_permlane32_swap_b32_e32 v183, v199
	v_permlane32_swap_b32_e32 v184, v200
	v_permlane32_swap_b32_e32 v185, v201
	v_permlane32_swap_b32_e32 v186, v202
	v_permlane32_swap_b32_e32 v187, v203
	v_permlane32_swap_b32_e32 v188, v204
	v_permlane32_swap_b32_e32 v189, v205
	v_permlane32_swap_b32_e32 v190, v206
	v_permlane32_swap_b32_e32 v191, v207
	v_permlane32_swap_b32_e32 v192, v208
	v_permlane32_swap_b32_e32 v193, v209
	v_add_f32_e32 v178, v178, v194
	v_add_f32_e32 v179, v179, v195
	v_add_f32_e32 v180, v180, v196
	v_add_f32_e32 v181, v181, v197
	v_add_f32_e32 v182, v182, v198
	v_add_f32_e32 v183, v183, v199
	v_add_f32_e32 v184, v184, v200
	v_add_f32_e32 v185, v185, v201
	v_add_f32_e32 v186, v186, v202
	v_add_f32_e32 v187, v187, v203
	v_add_f32_e32 v188, v188, v204
	v_add_f32_e32 v189, v189, v205
	v_add_f32_e32 v190, v190, v206
	v_add_f32_e32 v191, v191, v207
	v_add_f32_e32 v192, v192, v208
	v_add_f32_e32 v193, v193, v209
	v_permlane16_swap_b32_e32 v178, v186
	v_permlane16_swap_b32_e32 v179, v187
	v_permlane16_swap_b32_e32 v180, v188
	v_permlane16_swap_b32_e32 v181, v189
	v_permlane16_swap_b32_e32 v182, v190
	v_permlane16_swap_b32_e32 v183, v191
	v_permlane16_swap_b32_e32 v184, v192
	v_permlane16_swap_b32_e32 v185, v193
	v_add_f32_e32 v178, v178, v186
	v_add_f32_e32 v179, v179, v187
	v_add_f32_e32 v180, v180, v188
	v_add_f32_e32 v181, v181, v189
	v_add_f32_e32 v182, v182, v190
	v_add_f32_e32 v183, v183, v191
	v_add_f32_e32 v184, v184, v192
	v_add_f32_e32 v185, v185, v193
	v_cndmask_b32_e64 v2, v178, v182, s[8:9]
	v_cndmask_b32_e64 v3, v179, v183, s[8:9]
	v_cndmask_b32_e64 v4, v180, v184, s[8:9]
	v_cndmask_b32_e64 v5, v181, v185, s[8:9]
	v_cndmask_b32_e64 v6, v182, v178, s[8:9]
	v_cndmask_b32_e64 v7, v183, v179, s[8:9]
	v_cndmask_b32_e64 v8, v184, v180, s[8:9]
	v_cndmask_b32_e64 v9, v185, v181, s[8:9]
	v_add_f32_dpp v6, v2, v6 row_ror:8 row_mask:0xf bank_mask:0xf
	v_add_f32_dpp v7, v3, v7 row_ror:8 row_mask:0xf bank_mask:0xf
	v_add_f32_dpp v8, v4, v8 row_ror:8 row_mask:0xf bank_mask:0xf
	v_add_f32_dpp v9, v5, v9 row_ror:8 row_mask:0xf bank_mask:0xf
	v_cndmask_b32_e64 v2, v6, v8, s[10:11]
	v_cndmask_b32_e64 v3, v7, v9, s[10:11]
	v_cndmask_b32_e64 v4, v8, v6, s[10:11]
	v_cndmask_b32_e64 v5, v9, v7, s[10:11]
	v_add_f32_dpp v4, v2, v4 row_half_mirror row_mask:0xf bank_mask:0xf
	v_add_f32_dpp v5, v3, v5 row_half_mirror row_mask:0xf bank_mask:0xf
	v_cndmask_b32_e64 v2, v4, v5, s[14:15]
	v_cndmask_b32_e64 v3, v5, v4, s[14:15]
	s_nop 0
	v_add_f32_dpp v3, v2, v3 quad_perm:[2,3,0,1] row_mask:0xf bank_mask:0xf
	s_nop 1
	v_add_f32_dpp v11, v3, v3 quad_perm:[1,0,3,2] row_mask:0xf bank_mask:0xf
	s_mov_b64 exec, s[2:3]
	global_store_dword v[22:23], v11, off offset:384
	s_mov_b64 exec, -1
	s_add_i32 s16, s16, 1
	s_cmp_lt_i32 s16, s17
	s_cbranch_scc1 .Lpa_tok
	s_waitcnt vmcnt(0)
	s_waitcnt vmcnt(0)
	v_cmp_eq_u32_e32 vcc, 0, v0
	s_waitcnt vmcnt(0) lgkmcnt(0)
	s_barrier
	s_and_saveexec_b64 s[2:3], vcc
	s_cbranch_execz .Lgbb_1444
	v_readlane_b32 s4, v237, 5
	s_waitcnt vmcnt(0) expcnt(0) lgkmcnt(0)
	s_nop 0
	v_mov_b32_e32 v1, s4
	ds_read_b32 v3, v1
	ds_read_b32 v1, v1 offset:4
	s_waitcnt lgkmcnt(1)
	v_cmp_ne_u32_e32 vcc, 0, v3
	s_branch .Lgbb_1412
	v_readlane_b32 s4, v237, 2
	v_readlane_b32 s5, v237, 3
	s_load_dwordx2 s[8:9], s[6:7], 0x4
	s_lshl_b64 s[4:5], s[4:5], 2
	v_readlane_b32 s6, v237, 0
	s_add_u32 s4, s6, s4
	v_readlane_b32 s6, v237, 1
	s_addc_u32 s5, s6, s5
	s_add_u32 s6, s4, 0x1000
	s_addc_u32 s7, s5, 0
	s_waitcnt lgkmcnt(0)
	s_mul_i32 s20, s8, s38
	s_add_u32 s8, s4, 0x1100
	s_mul_i32 s20, s20, s9
	s_addc_u32 s9, s5, 0
	s_add_u32 s10, s4, 0x1200
	s_addc_u32 s11, s5, 0
	s_add_u32 s12, s4, 0x1300
	s_addc_u32 s13, s5, 0
	s_mov_b32 s21, 1
	v_mov_b32_e32 v17, 0
	s_branch .Lgbb_1400

.Lgbb_1444:
	s_or_b64 exec, exec, s[2:3]
	s_waitcnt lgkmcnt(0)
	s_barrier
	s_mov_b64 exec, -1
	v_and_b32_e32 v1, 63, v0
	v_readfirstlane_b32 s16, v0
	s_load_dwordx2 s[12:13], s[0:1], 0xc0
	s_lshr_b32 s16, s16, 6
	s_and_b32 s18, s33, 7
	s_lshr_b32 s19, s33, 3
	s_lshl_b32 s19, s19, 8
	s_lshl_b32 s16, s16, 5
	s_add_i32 s16, s16, s19
	s_add_i32 s17, s16, 32
	s_add_i32 s24, s17, -1
	s_lshl_b32 s19, s18, 9
	v_lshl_add_u32 v162, v1, 3, s19
	v_mov_b32_e32 v163, 0
	s_mov_b32 s31, 0
	v_mov_b32_e32 v4, v1
	v_mov_b32_e32 v5, 0
	s_mov_b32 s101, 0
	s_mov_b32 s100, 0x400000
	s_mov_b32 s41, 0x378e98ab
	s_mov_b32 s42, 0x3b7cd369
	s_mov_b32 s43, 0xbcc618b2
	s_mov_b32 s44, 0x3dda74e4
	s_mov_b32 s45, 0x3f228afd
	s_mov_b32 s46, 0x3e03c728
	s_mov_b32 s47, 0xbfb8aa3b
	s_mov_b32 s48, 0x42ce8ed0
	s_mov_b32 s49, 0xc2b17218
	s_mov_b32 s50, 0x7fffffff
	v_mov_b32_e32 v97, 0x43000000
	v_mov_b32_e32 v250, 0x3ba10414
	v_mov_b32_e32 v251, 0xb9c68948
	v_mov_b32_e32 v252, 0x7f800000
	s_load_dwordx2 s[4:5], s[0:1], 0xb8
	s_waitcnt lgkmcnt(0)
	s_add_u32 s26, s12, 0x17c00000
	s_addc_u32 s27, s13, 0
	s_add_u32 s20, s12, 0x100000
	s_addc_u32 s21, s13, 0
	v_lshl_add_u64 v[172:173], v[162:163], 1, s[20:21]
	s_add_u32 s20, s12, 0x4da00000
	s_addc_u32 s21, s13, 0
	v_lshl_add_u64 v[174:175], v[4:5], 2, s[20:21]
	s_add_u32 s20, s12, 0x4de00000
	s_addc_u32 s21, s13, 0
	v_lshl_add_u64 v[176:177], v[4:5], 2, s[20:21]
	s_add_u32 s20, s12, 0x23c00000
	s_addc_u32 s21, s13, 0
	v_lshl_add_u64 v[210:211], v[4:5], 2, s[20:21]
	s_add_u32 s20, s12, 0x25c00000
	s_addc_u32 s21, s13, 0
	v_and_b32_e32 v6, 7, v1
	v_mov_b32_e32 v7, 0
	v_lshlrev_b32_e32 v6, 20, v6
	v_lshl_add_u64 v[212:213], v[6:7], 0, s[20:21]
	v_lshl_add_u64 v[214:215], v[162:163], 2, s[4:5]
	s_add_u32 s66, s12, 0x1fe00000
	s_addc_u32 s67, s13, 0
	s_add_u32 s64, s12, 0x38d80000
	s_addc_u32 s65, s13, 0
	s_add_u32 s60, s12, 0x38d90000
	s_addc_u32 s61, s13, 0
	s_lshl_b32 s19, s18, 20
	s_add_u32 s62, s12, 0x26c00000
	s_addc_u32 s63, s13, 0
	s_add_u32 s62, s62, s19
	s_addc_u32 s63, s63, 0
	v_mov_b32_e32 v19, 0
	s_mov_b32 s2, 0x55555555
	s_mov_b32 s3, 0x55555555
	s_lshl_b32 s30, s16, 13
	v_lshl_add_u64 v[160:161], v[172:173], 0, s[30:31]
	global_load_dwordx4 v[116:119], v[160:161], off
	s_lshl_b32 s30, s16, 9
	v_lshl_add_u64 v[160:161], v[174:175], 0, s[30:31]
	global_load_dword v122, v[160:161], off
	global_load_dword v123, v[160:161], off offset:256
	v_lshl_add_u64 v[160:161], v[176:177], 0, s[30:31]
	global_load_dword v216, v[160:161], off
	global_load_dword v217, v[160:161], off offset:256
	v_lshl_add_u64 v[160:161], v[210:211], 0, s[30:31]
	global_load_dword v218, v[160:161], off
	global_load_dword v226, v[160:161], off offset:256
	v_lshl_add_u64 v[160:161], v[160:161], 0, s[100:101]
	global_load_dword v219, v[160:161], off
	global_load_dword v227, v[160:161], off offset:256
	v_lshl_add_u64 v[160:161], v[160:161], 0, s[100:101]
	global_load_dword v220, v[160:161], off
	global_load_dword v228, v[160:161], off offset:256
	v_lshl_add_u64 v[160:161], v[160:161], 0, s[100:101]
	global_load_dword v221, v[160:161], off
	global_load_dword v229, v[160:161], off offset:256
	v_lshl_add_u64 v[160:161], v[160:161], 0, s[100:101]
	global_load_dword v222, v[160:161], off
	global_load_dword v230, v[160:161], off offset:256
	v_lshl_add_u64 v[160:161], v[160:161], 0, s[100:101]
	global_load_dword v223, v[160:161], off
	global_load_dword v231, v[160:161], off offset:256
	v_lshl_add_u64 v[160:161], v[160:161], 0, s[100:101]
	global_load_dword v224, v[160:161], off
	global_load_dword v232, v[160:161], off offset:256
	v_lshl_add_u64 v[160:161], v[160:161], 0, s[100:101]
	global_load_dword v225, v[160:161], off
	global_load_dword v233, v[160:161], off offset:256
	s_lshl_b32 s30, s16, 7
	v_lshl_add_u64 v[160:161], v[212:213], 0, s[30:31]
	global_load_dword v234, v[160:161], off
	s_lshl_b32 s30, s16, 2
	s_add_u32 s28, s66, s30
	s_addc_u32 s29, s67, 0
	global_load_dword v235, v19, s[28:29]
	s_waitcnt vmcnt(0)
	v_lshlrev_b32_e32 v16, 2, v122
	v_lshlrev_b32_e32 v17, 2, v123
	global_load_dword v238, v16, s[64:65]
	global_load_dword v240, v16, s[60:61]
	global_load_dword v239, v17, s[64:65]
	global_load_dword v241, v17, s[60:61]
	s_waitcnt vmcnt(0)
	s_add_u32 s22, s12, 0x4da00000
	s_addc_u32 s23, s13, 0
	s_lshl_b32 s30, s16, 9
	s_add_u32 s36, s22, s30
	s_addc_u32 s37, s23, 0
	s_load_dwordx16 s[68:83], s[36:37], 0x0 glc
	s_load_dwordx16 s[84:99], s[36:37], 0x40 glc
	s_waitcnt lgkmcnt(0)
	s_lshl_b32 s30, s68, 12
	s_add_u32 s28, s26, s30
	s_addc_u32 s29, s27, 0
	global_load_dwordx2 v[24:25], v162, s[28:29]
	s_lshl_b32 s30, s69, 12
	s_add_u32 s28, s26, s30
	s_addc_u32 s29, s27, 0
	global_load_dwordx2 v[26:27], v162, s[28:29]
	s_lshl_b32 s30, s70, 12
	s_add_u32 s28, s26, s30
	s_addc_u32 s29, s27, 0
	global_load_dwordx2 v[28:29], v162, s[28:29]
	s_lshl_b32 s30, s71, 12
	s_add_u32 s28, s26, s30
	s_addc_u32 s29, s27, 0
	global_load_dwordx2 v[30:31], v162, s[28:29]
	s_lshl_b32 s30, s72, 12
	s_add_u32 s28, s26, s30
	s_addc_u32 s29, s27, 0
	global_load_dwordx2 v[32:33], v162, s[28:29]
	s_lshl_b32 s30, s73, 12
	s_add_u32 s28, s26, s30
	s_addc_u32 s29, s27, 0
	global_load_dwordx2 v[34:35], v162, s[28:29]
	s_lshl_b32 s30, s74, 12
	s_add_u32 s28, s26, s30
	s_addc_u32 s29, s27, 0
	global_load_dwordx2 v[36:37], v162, s[28:29]
	s_lshl_b32 s30, s75, 12
	s_add_u32 s28, s26, s30
	s_addc_u32 s29, s27, 0
	global_load_dwordx2 v[38:39], v162, s[28:29]
	s_lshl_b32 s30, s76, 12
	s_add_u32 s28, s26, s30
	s_addc_u32 s29, s27, 0
	global_load_dwordx2 v[40:41], v162, s[28:29]
	s_lshl_b32 s30, s77, 12
	s_add_u32 s28, s26, s30
	s_addc_u32 s29, s27, 0
	global_load_dwordx2 v[42:43], v162, s[28:29]
	s_lshl_b32 s30, s78, 12
	s_add_u32 s28, s26, s30
	s_addc_u32 s29, s27, 0
	global_load_dwordx2 v[44:45], v162, s[28:29]
	s_lshl_b32 s30, s79, 12
	s_add_u32 s28, s26, s30
	s_addc_u32 s29, s27, 0
	global_load_dwordx2 v[46:47], v162, s[28:29]
	s_lshl_b32 s30, s80, 12
	s_add_u32 s28, s26, s30
	s_addc_u32 s29, s27, 0
	global_load_dwordx2 v[48:49], v162, s[28:29]
	s_lshl_b32 s30, s81, 12
	s_add_u32 s28, s26, s30
	s_addc_u32 s29, s27, 0
	global_load_dwordx2 v[50:51], v162, s[28:29]
	s_lshl_b32 s30, s82, 12
	s_add_u32 s28, s26, s30
	s_addc_u32 s29, s27, 0
	global_load_dwordx2 v[52:53], v162, s[28:29]
	s_lshl_b32 s30, s83, 12
	s_add_u32 s28, s26, s30
	s_addc_u32 s29, s27, 0
	global_load_dwordx2 v[54:55], v162, s[28:29]
	s_lshl_b32 s30, s84, 12
	s_add_u32 s28, s26, s30
	s_addc_u32 s29, s27, 0
	global_load_dwordx2 v[56:57], v162, s[28:29]
	s_lshl_b32 s30, s85, 12
	s_add_u32 s28, s26, s30
	s_addc_u32 s29, s27, 0
	global_load_dwordx2 v[58:59], v162, s[28:29]
	s_lshl_b32 s30, s86, 12
	s_add_u32 s28, s26, s30
	s_addc_u32 s29, s27, 0
	global_load_dwordx2 v[60:61], v162, s[28:29]
	s_lshl_b32 s30, s87, 12
	s_add_u32 s28, s26, s30
	s_addc_u32 s29, s27, 0
	global_load_dwordx2 v[62:63], v162, s[28:29]
	s_lshl_b32 s30, s88, 12
	s_add_u32 s28, s26, s30
	s_addc_u32 s29, s27, 0
	global_load_dwordx2 v[64:65], v162, s[28:29]
	s_lshl_b32 s30, s89, 12
	s_add_u32 s28, s26, s30
	s_addc_u32 s29, s27, 0
	global_load_dwordx2 v[66:67], v162, s[28:29]
	s_lshl_b32 s30, s90, 12
	s_add_u32 s28, s26, s30
	s_addc_u32 s29, s27, 0
	global_load_dwordx2 v[68:69], v162, s[28:29]
	s_lshl_b32 s30, s91, 12
	s_add_u32 s28, s26, s30
	s_addc_u32 s29, s27, 0
	global_load_dwordx2 v[70:71], v162, s[28:29]
	s_lshl_b32 s30, s92, 12
	s_add_u32 s28, s26, s30
	s_addc_u32 s29, s27, 0
	global_load_dwordx2 v[72:73], v162, s[28:29]
	s_lshl_b32 s30, s93, 12
	s_add_u32 s28, s26, s30
	s_addc_u32 s29, s27, 0
	global_load_dwordx2 v[74:75], v162, s[28:29]
	s_lshl_b32 s30, s94, 12
	s_add_u32 s28, s26, s30
	s_addc_u32 s29, s27, 0
	global_load_dwordx2 v[76:77], v162, s[28:29]
	s_lshl_b32 s30, s95, 12
	s_add_u32 s28, s26, s30
	s_addc_u32 s29, s27, 0
	global_load_dwordx2 v[78:79], v162, s[28:29]
	s_lshl_b32 s30, s96, 12
	s_add_u32 s28, s26, s30
	s_addc_u32 s29, s27, 0
	global_load_dwordx2 v[80:81], v162, s[28:29]
	s_lshl_b32 s30, s97, 12
	s_add_u32 s28, s26, s30
	s_addc_u32 s29, s27, 0
	global_load_dwordx2 v[82:83], v162, s[28:29]
	s_lshl_b32 s30, s98, 12
	s_add_u32 s28, s26, s30
	s_addc_u32 s29, s27, 0
	global_load_dwordx2 v[84:85], v162, s[28:29]
	s_lshl_b32 s30, s99, 12
	s_add_u32 s28, s26, s30
	s_addc_u32 s29, s27, 0
	global_load_dwordx2 v[86:87], v162, s[28:29]
	s_load_dwordx16 s[68:83], s[36:37], 0x80 glc

.Lerfa1_1476:
	s_andn2_saveexec_b64 s[34:35], s[34:35]
	v_mul_f32_e32 v12, v11, v11
	v_fmamk_f32 v13, v12, 0xba1345e1, v250
	v_fmaak_f32 v13, v12, v13, 0xbcdac9b8
	v_fmaak_f32 v13, v12, v13, 0x3de703be
	v_fmaak_f32 v13, v12, v13, 0xbec09330
	v_fmaak_f32 v12, v12, v13, 0x3e0375d0
	v_fma_f32 v12, |v11|, v12, |v11|
	s_or_b64 exec, exec, s[34:35]
	v_bfi_b32 v11, s50, v12, v11
	v_mul_f32_e32 v10, 0.5, v10
	v_add_f32_e32 v11, 1.0, v11
	v_mul_f32_e32 v10, v10, v11
	v_mul_f32_e32 v10, v164, v10
	v_mul_f32_e32 v10, v249, v10
	v_mov_b32_e32 v247, v10
	v_add_f32_e32 v16, v246, v247
	s_nop 1
	v_add_f32_dpp v17, v16, v16 quad_perm:[1,0,3,2] row_mask:0xf bank_mask:0xf
	s_nop 1
	v_add_f32_dpp v16, v17, v17 quad_perm:[2,3,0,1] row_mask:0xf bank_mask:0xf
	s_nop 1
	v_add_f32_dpp v17, v16, v16 row_half_mirror row_mask:0xf bank_mask:0xf
	s_nop 1
	v_add_f32_dpp v16, v17, v17 row_ror:8 row_mask:0xf bank_mask:0xf
	v_mov_b32_e32 v17, v16
	s_nop 1
	v_permlane16_swap_b32_e32 v16, v17
	v_add_f32_e32 v16, v16, v17
	v_mov_b32_e32 v17, v16
	s_nop 1
	v_permlane32_swap_b32_e32 v16, v17
	v_add_f32_e32 v16, v16, v17
	v_mul_f32_e32 v248, 0xc3000000, v16
	v_mov_b32_e32 v242, v116
	v_mov_b32_e32 v243, v117
	v_mov_b32_e32 v244, v118
	v_mov_b32_e32 v245, v119
	v_mov_b32_e32 v120, v122
	v_mov_b32_e32 v121, v123
	s_lshl_b32 s30, s16, 14
	v_lshl_add_u64 v[20:21], v[214:215], 0, s[30:31]
	s_add_i32 s18, s16, 1
	s_min_i32 s18, s18, s24
	s_lshl_b32 s30, s16, 9
	s_add_u32 s36, s22, s30
	s_addc_u32 s37, s23, 0
	s_lshl_b32 s30, s18, 9
	s_add_u32 s38, s22, s30
	s_addc_u32 s39, s23, 0
	s_lshl_b32 s30, s18, 13
	v_lshl_add_u64 v[160:161], v[172:173], 0, s[30:31]
	global_load_dwordx4 v[116:119], v[160:161], off
	s_lshl_b32 s30, s18, 9
	v_lshl_add_u64 v[160:161], v[174:175], 0, s[30:31]
	global_load_dword v122, v[160:161], off
	global_load_dword v123, v[160:161], off offset:256
	v_lshl_add_u64 v[160:161], v[176:177], 0, s[30:31]
	global_load_dword v216, v[160:161], off
	global_load_dword v217, v[160:161], off offset:256
	v_lshl_add_u64 v[160:161], v[210:211], 0, s[30:31]
	global_load_dword v218, v[160:161], off
	global_load_dword v226, v[160:161], off offset:256
	v_lshl_add_u64 v[160:161], v[160:161], 0, s[100:101]
	global_load_dword v219, v[160:161], off
	global_load_dword v227, v[160:161], off offset:256
	v_lshl_add_u64 v[160:161], v[160:161], 0, s[100:101]
	global_load_dword v220, v[160:161], off
	global_load_dword v228, v[160:161], off offset:256
	v_lshl_add_u64 v[160:161], v[160:161], 0, s[100:101]
	global_load_dword v221, v[160:161], off
	global_load_dword v229, v[160:161], off offset:256
	v_lshl_add_u64 v[160:161], v[160:161], 0, s[100:101]
	global_load_dword v222, v[160:161], off
	global_load_dword v230, v[160:161], off offset:256
	v_lshl_add_u64 v[160:161], v[160:161], 0, s[100:101]
	global_load_dword v223, v[160:161], off
	global_load_dword v231, v[160:161], off offset:256
	v_lshl_add_u64 v[160:161], v[160:161], 0, s[100:101]
	global_load_dword v224, v[160:161], off
	global_load_dword v232, v[160:161], off offset:256
	v_lshl_add_u64 v[160:161], v[160:161], 0, s[100:101]
	global_load_dword v225, v[160:161], off
	global_load_dword v233, v[160:161], off offset:256
	s_lshl_b32 s30, s18, 7
	v_lshl_add_u64 v[160:161], v[212:213], 0, s[30:31]
	global_load_dword v234, v[160:161], off
	s_lshl_b32 s30, s18, 2
	s_add_u32 s28, s66, s30
	s_addc_u32 s29, s67, 0
	global_load_dword v235, v19, s[28:29]
	v_mov_b32_e32 v178, 0
	v_mov_b32_e32 v179, 0
	v_mov_b32_e32 v180, 0
	v_mov_b32_e32 v181, 0
	v_mov_b32_e32 v182, 0
	v_mov_b32_e32 v183, 0
	v_mov_b32_e32 v184, 0
	v_mov_b32_e32 v185, 0
	s_waitcnt vmcnt(54)
	v_readlane_b32 s25, v246, 0
	v_cvt_f32_ubyte0_e32 v124, v24
	v_cvt_f32_ubyte1_e32 v125, v24
	v_cvt_f32_ubyte2_e32 v126, v24
	v_cvt_f32_ubyte3_e32 v127, v24
	v_cvt_f32_ubyte0_e32 v128, v25
	v_cvt_f32_ubyte1_e32 v129, v25
	v_cvt_f32_ubyte2_e32 v130, v25
	v_cvt_f32_ubyte3_e32 v131, v25
	s_waitcnt lgkmcnt(0)
	s_load_dwordx16 s[84:99], s[36:37], 0xc0 glc
	s_lshl_b32 s30, s68, 12
	s_add_u32 s28, s26, s30
	s_addc_u32 s29, s27, 0
	global_load_dwordx2 v[24:25], v162, s[28:29]
	v_fmac_f32_e32 v178, s25, v124
	v_fmac_f32_e32 v179, s25, v125
	v_fmac_f32_e32 v180, s25, v126
	v_fmac_f32_e32 v181, s25, v127
	v_fmac_f32_e32 v182, s25, v128
	v_fmac_f32_e32 v183, s25, v129
	v_fmac_f32_e32 v184, s25, v130
	v_fmac_f32_e32 v185, s25, v131
	s_waitcnt vmcnt(54)
	v_readlane_b32 s25, v246, 1
	v_cvt_f32_ubyte0_e32 v132, v26
	v_cvt_f32_ubyte1_e32 v133, v26
	v_cvt_f32_ubyte2_e32 v134, v26
	v_cvt_f32_ubyte3_e32 v135, v26
	v_cvt_f32_ubyte0_e32 v136, v27
	v_cvt_f32_ubyte1_e32 v137, v27
	v_cvt_f32_ubyte2_e32 v138, v27
	v_cvt_f32_ubyte3_e32 v139, v27
	s_lshl_b32 s30, s69, 12
	s_add_u32 s28, s26, s30
	s_addc_u32 s29, s27, 0
	global_load_dwordx2 v[26:27], v162, s[28:29]
	v_fmac_f32_e32 v178, s25, v132
	v_fmac_f32_e32 v179, s25, v133
	v_fmac_f32_e32 v180, s25, v134
	v_fmac_f32_e32 v181, s25, v135
	v_fmac_f32_e32 v182, s25, v136
	v_fmac_f32_e32 v183, s25, v137
	v_fmac_f32_e32 v184, s25, v138
	v_fmac_f32_e32 v185, s25, v139
	s_waitcnt vmcnt(54)
	v_readlane_b32 s25, v246, 2
	v_cvt_f32_ubyte0_e32 v124, v28
	v_cvt_f32_ubyte1_e32 v125, v28
	v_cvt_f32_ubyte2_e32 v126, v28
	v_cvt_f32_ubyte3_e32 v127, v28
	v_cvt_f32_ubyte0_e32 v128, v29
	v_cvt_f32_ubyte1_e32 v129, v29
	v_cvt_f32_ubyte2_e32 v130, v29
	v_cvt_f32_ubyte3_e32 v131, v29
	s_lshl_b32 s30, s70, 12
	s_add_u32 s28, s26, s30
	s_addc_u32 s29, s27, 0
	global_load_dwordx2 v[28:29], v162, s[28:29]
	v_fmac_f32_e32 v178, s25, v124
	v_fmac_f32_e32 v179, s25, v125
	v_fmac_f32_e32 v180, s25, v126
	v_fmac_f32_e32 v181, s25, v127
	v_fmac_f32_e32 v182, s25, v128
	v_fmac_f32_e32 v183, s25, v129
	v_fmac_f32_e32 v184, s25, v130
	v_fmac_f32_e32 v185, s25, v131
	s_waitcnt vmcnt(54)
	v_readlane_b32 s25, v246, 3
	v_cvt_f32_ubyte0_e32 v132, v30
	v_cvt_f32_ubyte1_e32 v133, v30
	v_cvt_f32_ubyte2_e32 v134, v30
	v_cvt_f32_ubyte3_e32 v135, v30
	v_cvt_f32_ubyte0_e32 v136, v31
	v_cvt_f32_ubyte1_e32 v137, v31
	v_cvt_f32_ubyte2_e32 v138, v31
	v_cvt_f32_ubyte3_e32 v139, v31
	s_lshl_b32 s30, s71, 12
	s_add_u32 s28, s26, s30
	s_addc_u32 s29, s27, 0
	global_load_dwordx2 v[30:31], v162, s[28:29]
	v_fmac_f32_e32 v178, s25, v132
	v_fmac_f32_e32 v179, s25, v133
	v_fmac_f32_e32 v180, s25, v134
	v_fmac_f32_e32 v181, s25, v135
	v_fmac_f32_e32 v182, s25, v136
	v_fmac_f32_e32 v183, s25, v137
	v_fmac_f32_e32 v184, s25, v138
	v_fmac_f32_e32 v185, s25, v139
	s_waitcnt vmcnt(54)
	v_readlane_b32 s25, v246, 4
	v_cvt_f32_ubyte0_e32 v124, v32
	v_cvt_f32_ubyte1_e32 v125, v32
	v_cvt_f32_ubyte2_e32 v126, v32
	v_cvt_f32_ubyte3_e32 v127, v32
	v_cvt_f32_ubyte0_e32 v128, v33
	v_cvt_f32_ubyte1_e32 v129, v33
	v_cvt_f32_ubyte2_e32 v130, v33
	v_cvt_f32_ubyte3_e32 v131, v33
	s_lshl_b32 s30, s72, 12
	s_add_u32 s28, s26, s30
	s_addc_u32 s29, s27, 0
	global_load_dwordx2 v[32:33], v162, s[28:29]
	v_fmac_f32_e32 v178, s25, v124
	v_fmac_f32_e32 v179, s25, v125
	v_fmac_f32_e32 v180, s25, v126
	v_fmac_f32_e32 v181, s25, v127
	v_fmac_f32_e32 v182, s25, v128
	v_fmac_f32_e32 v183, s25, v129
	v_fmac_f32_e32 v184, s25, v130
	v_fmac_f32_e32 v185, s25, v131
	s_waitcnt vmcnt(54)
	v_readlane_b32 s25, v246, 5
	v_cvt_f32_ubyte0_e32 v132, v34
	v_cvt_f32_ubyte1_e32 v133, v34
	v_cvt_f32_ubyte2_e32 v134, v34
	v_cvt_f32_ubyte3_e32 v135, v34
	v_cvt_f32_ubyte0_e32 v136, v35
	v_cvt_f32_ubyte1_e32 v137, v35
	v_cvt_f32_ubyte2_e32 v138, v35
	v_cvt_f32_ubyte3_e32 v139, v35
	s_lshl_b32 s30, s73, 12
	s_add_u32 s28, s26, s30
	s_addc_u32 s29, s27, 0
	global_load_dwordx2 v[34:35], v162, s[28:29]
	v_fmac_f32_e32 v178, s25, v132
	v_fmac_f32_e32 v179, s25, v133
	v_fmac_f32_e32 v180, s25, v134
	v_fmac_f32_e32 v181, s25, v135
	v_fmac_f32_e32 v182, s25, v136
	v_fmac_f32_e32 v183, s25, v137
	v_fmac_f32_e32 v184, s25, v138
	v_fmac_f32_e32 v185, s25, v139
	s_waitcnt vmcnt(54)
	v_readlane_b32 s25, v246, 6
	v_cvt_f32_ubyte0_e32 v124, v36
	v_cvt_f32_ubyte1_e32 v125, v36
	v_cvt_f32_ubyte2_e32 v126, v36
	v_cvt_f32_ubyte3_e32 v127, v36
	v_cvt_f32_ubyte0_e32 v128, v37
	v_cvt_f32_ubyte1_e32 v129, v37
	v_cvt_f32_ubyte2_e32 v130, v37
	v_cvt_f32_ubyte3_e32 v131, v37
	s_lshl_b32 s30, s74, 12
	s_add_u32 s28, s26, s30
	s_addc_u32 s29, s27, 0
	global_load_dwordx2 v[36:37], v162, s[28:29]
	v_fmac_f32_e32 v178, s25, v124
	v_fmac_f32_e32 v179, s25, v125
	v_fmac_f32_e32 v180, s25, v126
	v_fmac_f32_e32 v181, s25, v127
	v_fmac_f32_e32 v182, s25, v128
	v_fmac_f32_e32 v183, s25, v129
	v_fmac_f32_e32 v184, s25, v130
	v_fmac_f32_e32 v185, s25, v131
	s_waitcnt vmcnt(54)
	v_readlane_b32 s25, v246, 7
	v_cvt_f32_ubyte0_e32 v132, v38
	v_cvt_f32_ubyte1_e32 v133, v38
	v_cvt_f32_ubyte2_e32 v134, v38
	v_cvt_f32_ubyte3_e32 v135, v38
	v_cvt_f32_ubyte0_e32 v136, v39
	v_cvt_f32_ubyte1_e32 v137, v39
	v_cvt_f32_ubyte2_e32 v138, v39
	v_cvt_f32_ubyte3_e32 v139, v39
	s_lshl_b32 s30, s75, 12
	s_add_u32 s28, s26, s30
	s_addc_u32 s29, s27, 0
	global_load_dwordx2 v[38:39], v162, s[28:29]
	v_fmac_f32_e32 v178, s25, v132
	v_fmac_f32_e32 v179, s25, v133
	v_fmac_f32_e32 v180, s25, v134
	v_fmac_f32_e32 v181, s25, v135
	v_fmac_f32_e32 v182, s25, v136
	v_fmac_f32_e32 v183, s25, v137
	v_fmac_f32_e32 v184, s25, v138
	v_fmac_f32_e32 v185, s25, v139
	s_waitcnt vmcnt(54)
	v_readlane_b32 s25, v246, 8
	v_cvt_f32_ubyte0_e32 v124, v40
	v_cvt_f32_ubyte1_e32 v125, v40
	v_cvt_f32_ubyte2_e32 v126, v40
	v_cvt_f32_ubyte3_e32 v127, v40
	v_cvt_f32_ubyte0_e32 v128, v41
	v_cvt_f32_ubyte1_e32 v129, v41
	v_cvt_f32_ubyte2_e32 v130, v41
	v_cvt_f32_ubyte3_e32 v131, v41
	s_lshl_b32 s30, s76, 12
	s_add_u32 s28, s26, s30
	s_addc_u32 s29, s27, 0
	global_load_dwordx2 v[40:41], v162, s[28:29]
	v_fmac_f32_e32 v178, s25, v124
	v_fmac_f32_e32 v179, s25, v125
	v_fmac_f32_e32 v180, s25, v126
	v_fmac_f32_e32 v181, s25, v127
	v_fmac_f32_e32 v182, s25, v128
	v_fmac_f32_e32 v183, s25, v129
	v_fmac_f32_e32 v184, s25, v130
	v_fmac_f32_e32 v185, s25, v131
	s_waitcnt vmcnt(54)
	v_readlane_b32 s25, v246, 9
	v_cvt_f32_ubyte0_e32 v132, v42
	v_cvt_f32_ubyte1_e32 v133, v42
	v_cvt_f32_ubyte2_e32 v134, v42
	v_cvt_f32_ubyte3_e32 v135, v42
	v_cvt_f32_ubyte0_e32 v136, v43
	v_cvt_f32_ubyte1_e32 v137, v43
	v_cvt_f32_ubyte2_e32 v138, v43
	v_cvt_f32_ubyte3_e32 v139, v43
	s_lshl_b32 s30, s77, 12
	s_add_u32 s28, s26, s30
	s_addc_u32 s29, s27, 0
	global_load_dwordx2 v[42:43], v162, s[28:29]
	v_fmac_f32_e32 v178, s25, v132
	v_fmac_f32_e32 v179, s25, v133
	v_fmac_f32_e32 v180, s25, v134
	v_fmac_f32_e32 v181, s25, v135
	v_fmac_f32_e32 v182, s25, v136
	v_fmac_f32_e32 v183, s25, v137
	v_fmac_f32_e32 v184, s25, v138
	v_fmac_f32_e32 v185, s25, v139
	s_waitcnt vmcnt(54)
	v_readlane_b32 s25, v246, 10
	v_cvt_f32_ubyte0_e32 v124, v44
	v_cvt_f32_ubyte1_e32 v125, v44
	v_cvt_f32_ubyte2_e32 v126, v44
	v_cvt_f32_ubyte3_e32 v127, v44
	v_cvt_f32_ubyte0_e32 v128, v45
	v_cvt_f32_ubyte1_e32 v129, v45
	v_cvt_f32_ubyte2_e32 v130, v45
	v_cvt_f32_ubyte3_e32 v131, v45
	s_lshl_b32 s30, s78, 12
	s_add_u32 s28, s26, s30
	s_addc_u32 s29, s27, 0
	global_load_dwordx2 v[44:45], v162, s[28:29]
	v_fmac_f32_e32 v178, s25, v124
	v_fmac_f32_e32 v179, s25, v125
	v_fmac_f32_e32 v180, s25, v126
	v_fmac_f32_e32 v181, s25, v127
	v_fmac_f32_e32 v182, s25, v128
	v_fmac_f32_e32 v183, s25, v129
	v_fmac_f32_e32 v184, s25, v130
	v_fmac_f32_e32 v185, s25, v131
	s_waitcnt vmcnt(54)
	v_readlane_b32 s25, v246, 11
	v_cvt_f32_ubyte0_e32 v132, v46
	v_cvt_f32_ubyte1_e32 v133, v46
	v_cvt_f32_ubyte2_e32 v134, v46
	v_cvt_f32_ubyte3_e32 v135, v46
	v_cvt_f32_ubyte0_e32 v136, v47
	v_cvt_f32_ubyte1_e32 v137, v47
	v_cvt_f32_ubyte2_e32 v138, v47
	v_cvt_f32_ubyte3_e32 v139, v47
	s_lshl_b32 s30, s79, 12
	s_add_u32 s28, s26, s30
	s_addc_u32 s29, s27, 0
	global_load_dwordx2 v[46:47], v162, s[28:29]
	v_fmac_f32_e32 v178, s25, v132
	v_fmac_f32_e32 v179, s25, v133
	v_fmac_f32_e32 v180, s25, v134
	v_fmac_f32_e32 v181, s25, v135
	v_fmac_f32_e32 v182, s25, v136
	v_fmac_f32_e32 v183, s25, v137
	v_fmac_f32_e32 v184, s25, v138
	v_fmac_f32_e32 v185, s25, v139
	s_waitcnt vmcnt(54)
	v_readlane_b32 s25, v246, 12
	v_cvt_f32_ubyte0_e32 v124, v48
	v_cvt_f32_ubyte1_e32 v125, v48
	v_cvt_f32_ubyte2_e32 v126, v48
	v_cvt_f32_ubyte3_e32 v127, v48
	v_cvt_f32_ubyte0_e32 v128, v49
	v_cvt_f32_ubyte1_e32 v129, v49
	v_cvt_f32_ubyte2_e32 v130, v49
	v_cvt_f32_ubyte3_e32 v131, v49
	s_lshl_b32 s30, s80, 12
	s_add_u32 s28, s26, s30
	s_addc_u32 s29, s27, 0
	global_load_dwordx2 v[48:49], v162, s[28:29]
	v_fmac_f32_e32 v178, s25, v124
	v_fmac_f32_e32 v179, s25, v125
	v_fmac_f32_e32 v180, s25, v126
	v_fmac_f32_e32 v181, s25, v127
	v_fmac_f32_e32 v182, s25, v128
	v_fmac_f32_e32 v183, s25, v129
	v_fmac_f32_e32 v184, s25, v130
	v_fmac_f32_e32 v185, s25, v131
	s_waitcnt vmcnt(54)
	v_readlane_b32 s25, v246, 13
	v_cvt_f32_ubyte0_e32 v132, v50
	v_cvt_f32_ubyte1_e32 v133, v50
	v_cvt_f32_ubyte2_e32 v134, v50
	v_cvt_f32_ubyte3_e32 v135, v50
	v_cvt_f32_ubyte0_e32 v136, v51
	v_cvt_f32_ubyte1_e32 v137, v51
	v_cvt_f32_ubyte2_e32 v138, v51
	v_cvt_f32_ubyte3_e32 v139, v51
	s_lshl_b32 s30, s81, 12
	s_add_u32 s28, s26, s30
	s_addc_u32 s29, s27, 0
	global_load_dwordx2 v[50:51], v162, s[28:29]
	v_fmac_f32_e32 v178, s25, v132
	v_fmac_f32_e32 v179, s25, v133
	v_fmac_f32_e32 v180, s25, v134
	v_fmac_f32_e32 v181, s25, v135
	v_fmac_f32_e32 v182, s25, v136
	v_fmac_f32_e32 v183, s25, v137
	v_fmac_f32_e32 v184, s25, v138
	v_fmac_f32_e32 v185, s25, v139
	s_waitcnt vmcnt(54)
	v_readlane_b32 s25, v246, 14
	v_cvt_f32_ubyte0_e32 v124, v52
	v_cvt_f32_ubyte1_e32 v125, v52
	v_cvt_f32_ubyte2_e32 v126, v52
	v_cvt_f32_ubyte3_e32 v127, v52
	v_cvt_f32_ubyte0_e32 v128, v53
	v_cvt_f32_ubyte1_e32 v129, v53
	v_cvt_f32_ubyte2_e32 v130, v53
	v_cvt_f32_ubyte3_e32 v131, v53
	s_lshl_b32 s30, s82, 12
	s_add_u32 s28, s26, s30
	s_addc_u32 s29, s27, 0
	global_load_dwordx2 v[52:53], v162, s[28:29]
	v_fmac_f32_e32 v178, s25, v124
	v_fmac_f32_e32 v179, s25, v125
	v_fmac_f32_e32 v180, s25, v126
	v_fmac_f32_e32 v181, s25, v127
	v_fmac_f32_e32 v182, s25, v128
	v_fmac_f32_e32 v183, s25, v129
	v_fmac_f32_e32 v184, s25, v130
	v_fmac_f32_e32 v185, s25, v131
	s_waitcnt vmcnt(54)
	v_readlane_b32 s25, v246, 15
	v_cvt_f32_ubyte0_e32 v132, v54
	v_cvt_f32_ubyte1_e32 v133, v54
	v_cvt_f32_ubyte2_e32 v134, v54
	v_cvt_f32_ubyte3_e32 v135, v54
	v_cvt_f32_ubyte0_e32 v136, v55
	v_cvt_f32_ubyte1_e32 v137, v55
	v_cvt_f32_ubyte2_e32 v138, v55
	v_cvt_f32_ubyte3_e32 v139, v55
	s_lshl_b32 s30, s83, 12
	s_add_u32 s28, s26, s30
	s_addc_u32 s29, s27, 0
	global_load_dwordx2 v[54:55], v162, s[28:29]
	v_fmac_f32_e32 v178, s25, v132
	v_fmac_f32_e32 v179, s25, v133
	v_fmac_f32_e32 v180, s25, v134
	v_fmac_f32_e32 v181, s25, v135
	v_fmac_f32_e32 v182, s25, v136
	v_fmac_f32_e32 v183, s25, v137
	v_fmac_f32_e32 v184, s25, v138
	v_fmac_f32_e32 v185, s25, v139
	s_waitcnt vmcnt(54)
	v_readlane_b32 s25, v246, 16
	v_cvt_f32_ubyte0_e32 v124, v56
	v_cvt_f32_ubyte1_e32 v125, v56
	v_cvt_f32_ubyte2_e32 v126, v56
	v_cvt_f32_ubyte3_e32 v127, v56
	v_cvt_f32_ubyte0_e32 v128, v57
	v_cvt_f32_ubyte1_e32 v129, v57
	v_cvt_f32_ubyte2_e32 v130, v57
	v_cvt_f32_ubyte3_e32 v131, v57
	s_waitcnt lgkmcnt(0)
	s_load_dwordx16 s[68:83], s[36:37], 0x100 glc
	s_lshl_b32 s30, s84, 12
	s_add_u32 s28, s26, s30
	s_addc_u32 s29, s27, 0
	global_load_dwordx2 v[56:57], v162, s[28:29]
	v_fmac_f32_e32 v178, s25, v124
	v_fmac_f32_e32 v179, s25, v125
	v_fmac_f32_e32 v180, s25, v126
	v_fmac_f32_e32 v181, s25, v127
	v_fmac_f32_e32 v182, s25, v128
	v_fmac_f32_e32 v183, s25, v129
	v_fmac_f32_e32 v184, s25, v130
	v_fmac_f32_e32 v185, s25, v131
	s_waitcnt vmcnt(54)
	v_readlane_b32 s25, v246, 17
	v_cvt_f32_ubyte0_e32 v132, v58
	v_cvt_f32_ubyte1_e32 v133, v58
	v_cvt_f32_ubyte2_e32 v134, v58
	v_cvt_f32_ubyte3_e32 v135, v58
	v_cvt_f32_ubyte0_e32 v136, v59
	v_cvt_f32_ubyte1_e32 v137, v59
	v_cvt_f32_ubyte2_e32 v138, v59
	v_cvt_f32_ubyte3_e32 v139, v59
	s_lshl_b32 s30, s85, 12
	s_add_u32 s28, s26, s30
	s_addc_u32 s29, s27, 0
	global_load_dwordx2 v[58:59], v162, s[28:29]
	v_fmac_f32_e32 v178, s25, v132
	v_fmac_f32_e32 v179, s25, v133
	v_fmac_f32_e32 v180, s25, v134
	v_fmac_f32_e32 v181, s25, v135
	v_fmac_f32_e32 v182, s25, v136
	v_fmac_f32_e32 v183, s25, v137
	v_fmac_f32_e32 v184, s25, v138
	v_fmac_f32_e32 v185, s25, v139
	s_waitcnt vmcnt(54)
	v_readlane_b32 s25, v246, 18
	v_cvt_f32_ubyte0_e32 v124, v60
	v_cvt_f32_ubyte1_e32 v125, v60
	v_cvt_f32_ubyte2_e32 v126, v60
	v_cvt_f32_ubyte3_e32 v127, v60
	v_cvt_f32_ubyte0_e32 v128, v61
	v_cvt_f32_ubyte1_e32 v129, v61
	v_cvt_f32_ubyte2_e32 v130, v61
	v_cvt_f32_ubyte3_e32 v131, v61
	s_lshl_b32 s30, s86, 12
	s_add_u32 s28, s26, s30
	s_addc_u32 s29, s27, 0
	global_load_dwordx2 v[60:61], v162, s[28:29]
	v_fmac_f32_e32 v178, s25, v124
	v_fmac_f32_e32 v179, s25, v125
	v_fmac_f32_e32 v180, s25, v126
	v_fmac_f32_e32 v181, s25, v127
	v_fmac_f32_e32 v182, s25, v128
	v_fmac_f32_e32 v183, s25, v129
	v_fmac_f32_e32 v184, s25, v130
	v_fmac_f32_e32 v185, s25, v131
	s_waitcnt vmcnt(54)
	v_readlane_b32 s25, v246, 19
	v_cvt_f32_ubyte0_e32 v132, v62
	v_cvt_f32_ubyte1_e32 v133, v62
	v_cvt_f32_ubyte2_e32 v134, v62
	v_cvt_f32_ubyte3_e32 v135, v62
	v_cvt_f32_ubyte0_e32 v136, v63
	v_cvt_f32_ubyte1_e32 v137, v63
	v_cvt_f32_ubyte2_e32 v138, v63
	v_cvt_f32_ubyte3_e32 v139, v63
	s_lshl_b32 s30, s87, 12
	s_add_u32 s28, s26, s30
	s_addc_u32 s29, s27, 0
	global_load_dwordx2 v[62:63], v162, s[28:29]
	v_fmac_f32_e32 v178, s25, v132
	v_fmac_f32_e32 v179, s25, v133
	v_fmac_f32_e32 v180, s25, v134
	v_fmac_f32_e32 v181, s25, v135
	v_fmac_f32_e32 v182, s25, v136
	v_fmac_f32_e32 v183, s25, v137
	v_fmac_f32_e32 v184, s25, v138
	v_fmac_f32_e32 v185, s25, v139
	s_waitcnt vmcnt(54)
	v_readlane_b32 s25, v246, 20
	v_cvt_f32_ubyte0_e32 v124, v64
	v_cvt_f32_ubyte1_e32 v125, v64
	v_cvt_f32_ubyte2_e32 v126, v64
	v_cvt_f32_ubyte3_e32 v127, v64
	v_cvt_f32_ubyte0_e32 v128, v65
	v_cvt_f32_ubyte1_e32 v129, v65
	v_cvt_f32_ubyte2_e32 v130, v65
	v_cvt_f32_ubyte3_e32 v131, v65
	s_lshl_b32 s30, s88, 12
	s_add_u32 s28, s26, s30
	s_addc_u32 s29, s27, 0
	global_load_dwordx2 v[64:65], v162, s[28:29]
	v_fmac_f32_e32 v178, s25, v124
	v_fmac_f32_e32 v179, s25, v125
	v_fmac_f32_e32 v180, s25, v126
	v_fmac_f32_e32 v181, s25, v127
	v_fmac_f32_e32 v182, s25, v128
	v_fmac_f32_e32 v183, s25, v129
	v_fmac_f32_e32 v184, s25, v130
	v_fmac_f32_e32 v185, s25, v131
	s_waitcnt vmcnt(54)
	v_readlane_b32 s25, v246, 21
	v_cvt_f32_ubyte0_e32 v132, v66
	v_cvt_f32_ubyte1_e32 v133, v66
	v_cvt_f32_ubyte2_e32 v134, v66
	v_cvt_f32_ubyte3_e32 v135, v66
	v_cvt_f32_ubyte0_e32 v136, v67
	v_cvt_f32_ubyte1_e32 v137, v67
	v_cvt_f32_ubyte2_e32 v138, v67
	v_cvt_f32_ubyte3_e32 v139, v67
	s_lshl_b32 s30, s89, 12
	s_add_u32 s28, s26, s30
	s_addc_u32 s29, s27, 0
	global_load_dwordx2 v[66:67], v162, s[28:29]
	v_fmac_f32_e32 v178, s25, v132
	v_fmac_f32_e32 v179, s25, v133
	v_fmac_f32_e32 v180, s25, v134
	v_fmac_f32_e32 v181, s25, v135
	v_fmac_f32_e32 v182, s25, v136
	v_fmac_f32_e32 v183, s25, v137
	v_fmac_f32_e32 v184, s25, v138
	v_fmac_f32_e32 v185, s25, v139
	s_waitcnt vmcnt(54)
	v_readlane_b32 s25, v246, 22
	v_cvt_f32_ubyte0_e32 v124, v68
	v_cvt_f32_ubyte1_e32 v125, v68
	v_cvt_f32_ubyte2_e32 v126, v68
	v_cvt_f32_ubyte3_e32 v127, v68
	v_cvt_f32_ubyte0_e32 v128, v69
	v_cvt_f32_ubyte1_e32 v129, v69
	v_cvt_f32_ubyte2_e32 v130, v69
	v_cvt_f32_ubyte3_e32 v131, v69
	s_lshl_b32 s30, s90, 12
	s_add_u32 s28, s26, s30
	s_addc_u32 s29, s27, 0
	global_load_dwordx2 v[68:69], v162, s[28:29]
	v_fmac_f32_e32 v178, s25, v124
	v_fmac_f32_e32 v179, s25, v125
	v_fmac_f32_e32 v180, s25, v126
	v_fmac_f32_e32 v181, s25, v127
	v_fmac_f32_e32 v182, s25, v128
	v_fmac_f32_e32 v183, s25, v129
	v_fmac_f32_e32 v184, s25, v130
	v_fmac_f32_e32 v185, s25, v131
	s_waitcnt vmcnt(54)
	v_readlane_b32 s25, v246, 23
	v_cvt_f32_ubyte0_e32 v132, v70
	v_cvt_f32_ubyte1_e32 v133, v70
	v_cvt_f32_ubyte2_e32 v134, v70
	v_cvt_f32_ubyte3_e32 v135, v70
	v_cvt_f32_ubyte0_e32 v136, v71
	v_cvt_f32_ubyte1_e32 v137, v71
	v_cvt_f32_ubyte2_e32 v138, v71
	v_cvt_f32_ubyte3_e32 v139, v71
	s_lshl_b32 s30, s91, 12
	s_add_u32 s28, s26, s30
	s_addc_u32 s29, s27, 0
	global_load_dwordx2 v[70:71], v162, s[28:29]
	v_fmac_f32_e32 v178, s25, v132
	v_fmac_f32_e32 v179, s25, v133
	v_fmac_f32_e32 v180, s25, v134
	v_fmac_f32_e32 v181, s25, v135
	v_fmac_f32_e32 v182, s25, v136
	v_fmac_f32_e32 v183, s25, v137
	v_fmac_f32_e32 v184, s25, v138
	v_fmac_f32_e32 v185, s25, v139
	s_waitcnt vmcnt(54)
	v_readlane_b32 s25, v246, 24
	v_cvt_f32_ubyte0_e32 v124, v72
	v_cvt_f32_ubyte1_e32 v125, v72
	v_cvt_f32_ubyte2_e32 v126, v72
	v_cvt_f32_ubyte3_e32 v127, v72
	v_cvt_f32_ubyte0_e32 v128, v73
	v_cvt_f32_ubyte1_e32 v129, v73
	v_cvt_f32_ubyte2_e32 v130, v73
	v_cvt_f32_ubyte3_e32 v131, v73
	s_lshl_b32 s30, s92, 12
	s_add_u32 s28, s26, s30
	s_addc_u32 s29, s27, 0
	global_load_dwordx2 v[72:73], v162, s[28:29]
	v_fmac_f32_e32 v178, s25, v124
	v_fmac_f32_e32 v179, s25, v125
	v_fmac_f32_e32 v180, s25, v126
	v_fmac_f32_e32 v181, s25, v127
	v_fmac_f32_e32 v182, s25, v128
	v_fmac_f32_e32 v183, s25, v129
	v_fmac_f32_e32 v184, s25, v130
	v_fmac_f32_e32 v185, s25, v131
	s_waitcnt vmcnt(54)
	v_readlane_b32 s25, v246, 25
	v_cvt_f32_ubyte0_e32 v132, v74
	v_cvt_f32_ubyte1_e32 v133, v74
	v_cvt_f32_ubyte2_e32 v134, v74
	v_cvt_f32_ubyte3_e32 v135, v74
	v_cvt_f32_ubyte0_e32 v136, v75
	v_cvt_f32_ubyte1_e32 v137, v75
	v_cvt_f32_ubyte2_e32 v138, v75
	v_cvt_f32_ubyte3_e32 v139, v75
	s_lshl_b32 s30, s93, 12
	s_add_u32 s28, s26, s30
	s_addc_u32 s29, s27, 0
	global_load_dwordx2 v[74:75], v162, s[28:29]
	v_fmac_f32_e32 v178, s25, v132
	v_fmac_f32_e32 v179, s25, v133
	v_fmac_f32_e32 v180, s25, v134
	v_fmac_f32_e32 v181, s25, v135
	v_fmac_f32_e32 v182, s25, v136
	v_fmac_f32_e32 v183, s25, v137
	v_fmac_f32_e32 v184, s25, v138
	v_fmac_f32_e32 v185, s25, v139
	s_waitcnt vmcnt(54)
	v_readlane_b32 s25, v246, 26
	v_cvt_f32_ubyte0_e32 v124, v76
	v_cvt_f32_ubyte1_e32 v125, v76
	v_cvt_f32_ubyte2_e32 v126, v76
	v_cvt_f32_ubyte3_e32 v127, v76
	v_cvt_f32_ubyte0_e32 v128, v77
	v_cvt_f32_ubyte1_e32 v129, v77
	v_cvt_f32_ubyte2_e32 v130, v77
	v_cvt_f32_ubyte3_e32 v131, v77
	s_lshl_b32 s30, s94, 12
	s_add_u32 s28, s26, s30
	s_addc_u32 s29, s27, 0
	global_load_dwordx2 v[76:77], v162, s[28:29]
	v_fmac_f32_e32 v178, s25, v124
	v_fmac_f32_e32 v179, s25, v125
	v_fmac_f32_e32 v180, s25, v126
	v_fmac_f32_e32 v181, s25, v127
	v_fmac_f32_e32 v182, s25, v128
	v_fmac_f32_e32 v183, s25, v129
	v_fmac_f32_e32 v184, s25, v130
	v_fmac_f32_e32 v185, s25, v131
	s_waitcnt vmcnt(54)
	v_readlane_b32 s25, v246, 27
	v_cvt_f32_ubyte0_e32 v132, v78
	v_cvt_f32_ubyte1_e32 v133, v78
	v_cvt_f32_ubyte2_e32 v134, v78
	v_cvt_f32_ubyte3_e32 v135, v78
	v_cvt_f32_ubyte0_e32 v136, v79
	v_cvt_f32_ubyte1_e32 v137, v79
	v_cvt_f32_ubyte2_e32 v138, v79
	v_cvt_f32_ubyte3_e32 v139, v79
	s_lshl_b32 s30, s95, 12
	s_add_u32 s28, s26, s30
	s_addc_u32 s29, s27, 0
	global_load_dwordx2 v[78:79], v162, s[28:29]
	v_fmac_f32_e32 v178, s25, v132
	v_fmac_f32_e32 v179, s25, v133
	v_fmac_f32_e32 v180, s25, v134
	v_fmac_f32_e32 v181, s25, v135
	v_fmac_f32_e32 v182, s25, v136
	v_fmac_f32_e32 v183, s25, v137
	v_fmac_f32_e32 v184, s25, v138
	v_fmac_f32_e32 v185, s25, v139
	s_waitcnt vmcnt(54)
	v_readlane_b32 s25, v246, 28
	v_cvt_f32_ubyte0_e32 v124, v80
	v_cvt_f32_ubyte1_e32 v125, v80
	v_cvt_f32_ubyte2_e32 v126, v80
	v_cvt_f32_ubyte3_e32 v127, v80
	v_cvt_f32_ubyte0_e32 v128, v81
	v_cvt_f32_ubyte1_e32 v129, v81
	v_cvt_f32_ubyte2_e32 v130, v81
	v_cvt_f32_ubyte3_e32 v131, v81
	s_lshl_b32 s30, s96, 12
	s_add_u32 s28, s26, s30
	s_addc_u32 s29, s27, 0
	global_load_dwordx2 v[80:81], v162, s[28:29]
	v_fmac_f32_e32 v178, s25, v124
	v_fmac_f32_e32 v179, s25, v125
	v_fmac_f32_e32 v180, s25, v126
	v_fmac_f32_e32 v181, s25, v127
	v_fmac_f32_e32 v182, s25, v128
	v_fmac_f32_e32 v183, s25, v129
	v_fmac_f32_e32 v184, s25, v130
	v_fmac_f32_e32 v185, s25, v131
	s_waitcnt vmcnt(54)
	v_readlane_b32 s25, v246, 29
	v_cvt_f32_ubyte0_e32 v132, v82
	v_cvt_f32_ubyte1_e32 v133, v82
	v_cvt_f32_ubyte2_e32 v134, v82
	v_cvt_f32_ubyte3_e32 v135, v82
	v_cvt_f32_ubyte0_e32 v136, v83
	v_cvt_f32_ubyte1_e32 v137, v83
	v_cvt_f32_ubyte2_e32 v138, v83
	v_cvt_f32_ubyte3_e32 v139, v83
	s_lshl_b32 s30, s97, 12
	s_add_u32 s28, s26, s30
	s_addc_u32 s29, s27, 0
	global_load_dwordx2 v[82:83], v162, s[28:29]
	v_fmac_f32_e32 v178, s25, v132
	v_fmac_f32_e32 v179, s25, v133
	v_fmac_f32_e32 v180, s25, v134
	v_fmac_f32_e32 v181, s25, v135
	v_fmac_f32_e32 v182, s25, v136
	v_fmac_f32_e32 v183, s25, v137
	v_fmac_f32_e32 v184, s25, v138
	v_fmac_f32_e32 v185, s25, v139
	s_waitcnt vmcnt(54)
	v_readlane_b32 s25, v246, 30
	v_cvt_f32_ubyte0_e32 v124, v84
	v_cvt_f32_ubyte1_e32 v125, v84
	v_cvt_f32_ubyte2_e32 v126, v84
	v_cvt_f32_ubyte3_e32 v127, v84
	v_cvt_f32_ubyte0_e32 v128, v85
	v_cvt_f32_ubyte1_e32 v129, v85
	v_cvt_f32_ubyte2_e32 v130, v85
	v_cvt_f32_ubyte3_e32 v131, v85
	s_lshl_b32 s30, s98, 12
	s_add_u32 s28, s26, s30
	s_addc_u32 s29, s27, 0
	global_load_dwordx2 v[84:85], v162, s[28:29]
	v_fmac_f32_e32 v178, s25, v124
	v_fmac_f32_e32 v179, s25, v125
	v_fmac_f32_e32 v180, s25, v126
	v_fmac_f32_e32 v181, s25, v127
	v_fmac_f32_e32 v182, s25, v128
	v_fmac_f32_e32 v183, s25, v129
	v_fmac_f32_e32 v184, s25, v130
	v_fmac_f32_e32 v185, s25, v131
	s_waitcnt vmcnt(54)
	v_readlane_b32 s25, v246, 31
	v_cvt_f32_ubyte0_e32 v132, v86
	v_cvt_f32_ubyte1_e32 v133, v86
	v_cvt_f32_ubyte2_e32 v134, v86
	v_cvt_f32_ubyte3_e32 v135, v86
	v_cvt_f32_ubyte0_e32 v136, v87
	v_cvt_f32_ubyte1_e32 v137, v87
	v_cvt_f32_ubyte2_e32 v138, v87
	v_cvt_f32_ubyte3_e32 v139, v87
	s_lshl_b32 s30, s99, 12
	s_add_u32 s28, s26, s30
	s_addc_u32 s29, s27, 0
	global_load_dwordx2 v[86:87], v162, s[28:29]
	v_fmac_f32_e32 v178, s25, v132
	v_fmac_f32_e32 v179, s25, v133
	v_fmac_f32_e32 v180, s25, v134
	v_fmac_f32_e32 v181, s25, v135
	v_fmac_f32_e32 v182, s25, v136
	v_fmac_f32_e32 v183, s25, v137
	v_fmac_f32_e32 v184, s25, v138
	v_fmac_f32_e32 v185, s25, v139
	s_waitcnt vmcnt(31)
	v_readlane_b32 s25, v246, 32
	v_cvt_f32_ubyte0_e32 v124, v24
	v_cvt_f32_ubyte1_e32 v125, v24
	v_cvt_f32_ubyte2_e32 v126, v24
	v_cvt_f32_ubyte3_e32 v127, v24
	v_cvt_f32_ubyte0_e32 v128, v25
	v_cvt_f32_ubyte1_e32 v129, v25
	v_cvt_f32_ubyte2_e32 v130, v25
	v_cvt_f32_ubyte3_e32 v131, v25
	s_waitcnt lgkmcnt(0)
	s_load_dwordx16 s[84:99], s[36:37], 0x140 glc
	s_lshl_b32 s30, s68, 12
	s_add_u32 s28, s26, s30
	s_addc_u32 s29, s27, 0
	global_load_dwordx2 v[24:25], v162, s[28:29]
	v_fmac_f32_e32 v178, s25, v124
	v_fmac_f32_e32 v179, s25, v125
	v_fmac_f32_e32 v180, s25, v126
	v_fmac_f32_e32 v181, s25, v127
	v_fmac_f32_e32 v182, s25, v128
	v_fmac_f32_e32 v183, s25, v129
	v_fmac_f32_e32 v184, s25, v130
	v_fmac_f32_e32 v185, s25, v131
	s_waitcnt vmcnt(31)
	v_readlane_b32 s25, v246, 33
	v_cvt_f32_ubyte0_e32 v132, v26
	v_cvt_f32_ubyte1_e32 v133, v26
	v_cvt_f32_ubyte2_e32 v134, v26
	v_cvt_f32_ubyte3_e32 v135, v26
	v_cvt_f32_ubyte0_e32 v136, v27
	v_cvt_f32_ubyte1_e32 v137, v27
	v_cvt_f32_ubyte2_e32 v138, v27
	v_cvt_f32_ubyte3_e32 v139, v27
	s_lshl_b32 s30, s69, 12
	s_add_u32 s28, s26, s30
	s_addc_u32 s29, s27, 0
	global_load_dwordx2 v[26:27], v162, s[28:29]
	v_fmac_f32_e32 v178, s25, v132
	v_fmac_f32_e32 v179, s25, v133
	v_fmac_f32_e32 v180, s25, v134
	v_fmac_f32_e32 v181, s25, v135
	v_fmac_f32_e32 v182, s25, v136
	v_fmac_f32_e32 v183, s25, v137
	v_fmac_f32_e32 v184, s25, v138
	v_fmac_f32_e32 v185, s25, v139
	s_waitcnt vmcnt(31)
	v_readlane_b32 s25, v246, 34
	v_cvt_f32_ubyte0_e32 v124, v28
	v_cvt_f32_ubyte1_e32 v125, v28
	v_cvt_f32_ubyte2_e32 v126, v28
	v_cvt_f32_ubyte3_e32 v127, v28
	v_cvt_f32_ubyte0_e32 v128, v29
	v_cvt_f32_ubyte1_e32 v129, v29
	v_cvt_f32_ubyte2_e32 v130, v29
	v_cvt_f32_ubyte3_e32 v131, v29
	s_lshl_b32 s30, s70, 12
	s_add_u32 s28, s26, s30
	s_addc_u32 s29, s27, 0
	global_load_dwordx2 v[28:29], v162, s[28:29]
	v_fmac_f32_e32 v178, s25, v124
	v_fmac_f32_e32 v179, s25, v125
	v_fmac_f32_e32 v180, s25, v126
	v_fmac_f32_e32 v181, s25, v127
	v_fmac_f32_e32 v182, s25, v128
	v_fmac_f32_e32 v183, s25, v129
	v_fmac_f32_e32 v184, s25, v130
	v_fmac_f32_e32 v185, s25, v131
	s_waitcnt vmcnt(31)
	v_readlane_b32 s25, v246, 35
	v_cvt_f32_ubyte0_e32 v132, v30
	v_cvt_f32_ubyte1_e32 v133, v30
	v_cvt_f32_ubyte2_e32 v134, v30
	v_cvt_f32_ubyte3_e32 v135, v30
	v_cvt_f32_ubyte0_e32 v136, v31
	v_cvt_f32_ubyte1_e32 v137, v31
	v_cvt_f32_ubyte2_e32 v138, v31
	v_cvt_f32_ubyte3_e32 v139, v31
	s_lshl_b32 s30, s71, 12
	s_add_u32 s28, s26, s30
	s_addc_u32 s29, s27, 0
	global_load_dwordx2 v[30:31], v162, s[28:29]
	v_fmac_f32_e32 v178, s25, v132
	v_fmac_f32_e32 v179, s25, v133
	v_fmac_f32_e32 v180, s25, v134
	v_fmac_f32_e32 v181, s25, v135
	v_fmac_f32_e32 v182, s25, v136
	v_fmac_f32_e32 v183, s25, v137
	v_fmac_f32_e32 v184, s25, v138
	v_fmac_f32_e32 v185, s25, v139
	s_waitcnt vmcnt(31)
	v_readlane_b32 s25, v246, 36
	v_cvt_f32_ubyte0_e32 v124, v32
	v_cvt_f32_ubyte1_e32 v125, v32
	v_cvt_f32_ubyte2_e32 v126, v32
	v_cvt_f32_ubyte3_e32 v127, v32
	v_cvt_f32_ubyte0_e32 v128, v33
	v_cvt_f32_ubyte1_e32 v129, v33
	v_cvt_f32_ubyte2_e32 v130, v33
	v_cvt_f32_ubyte3_e32 v131, v33
	s_lshl_b32 s30, s72, 12
	s_add_u32 s28, s26, s30
	s_addc_u32 s29, s27, 0
	global_load_dwordx2 v[32:33], v162, s[28:29]
	v_fmac_f32_e32 v178, s25, v124
	v_fmac_f32_e32 v179, s25, v125
	v_fmac_f32_e32 v180, s25, v126
	v_fmac_f32_e32 v181, s25, v127
	v_fmac_f32_e32 v182, s25, v128
	v_fmac_f32_e32 v183, s25, v129
	v_fmac_f32_e32 v184, s25, v130
	v_fmac_f32_e32 v185, s25, v131
	s_waitcnt vmcnt(31)
	v_readlane_b32 s25, v246, 37
	v_cvt_f32_ubyte0_e32 v132, v34
	v_cvt_f32_ubyte1_e32 v133, v34
	v_cvt_f32_ubyte2_e32 v134, v34
	v_cvt_f32_ubyte3_e32 v135, v34
	v_cvt_f32_ubyte0_e32 v136, v35
	v_cvt_f32_ubyte1_e32 v137, v35
	v_cvt_f32_ubyte2_e32 v138, v35
	v_cvt_f32_ubyte3_e32 v139, v35
	s_lshl_b32 s30, s73, 12
	s_add_u32 s28, s26, s30
	s_addc_u32 s29, s27, 0
	global_load_dwordx2 v[34:35], v162, s[28:29]
	v_fmac_f32_e32 v178, s25, v132
	v_fmac_f32_e32 v179, s25, v133
	v_fmac_f32_e32 v180, s25, v134
	v_fmac_f32_e32 v181, s25, v135
	v_fmac_f32_e32 v182, s25, v136
	v_fmac_f32_e32 v183, s25, v137
	v_fmac_f32_e32 v184, s25, v138
	v_fmac_f32_e32 v185, s25, v139
	s_waitcnt vmcnt(31)
	v_readlane_b32 s25, v246, 38
	v_cvt_f32_ubyte0_e32 v124, v36
	v_cvt_f32_ubyte1_e32 v125, v36
	v_cvt_f32_ubyte2_e32 v126, v36
	v_cvt_f32_ubyte3_e32 v127, v36
	v_cvt_f32_ubyte0_e32 v128, v37
	v_cvt_f32_ubyte1_e32 v129, v37
	v_cvt_f32_ubyte2_e32 v130, v37
	v_cvt_f32_ubyte3_e32 v131, v37
	s_lshl_b32 s30, s74, 12
	s_add_u32 s28, s26, s30
	s_addc_u32 s29, s27, 0
	global_load_dwordx2 v[36:37], v162, s[28:29]
	v_fmac_f32_e32 v178, s25, v124
	v_fmac_f32_e32 v179, s25, v125
	v_fmac_f32_e32 v180, s25, v126
	v_fmac_f32_e32 v181, s25, v127
	v_fmac_f32_e32 v182, s25, v128
	v_fmac_f32_e32 v183, s25, v129
	v_fmac_f32_e32 v184, s25, v130
	v_fmac_f32_e32 v185, s25, v131
	s_waitcnt vmcnt(31)
	v_readlane_b32 s25, v246, 39
	v_cvt_f32_ubyte0_e32 v132, v38
	v_cvt_f32_ubyte1_e32 v133, v38
	v_cvt_f32_ubyte2_e32 v134, v38
	v_cvt_f32_ubyte3_e32 v135, v38
	v_cvt_f32_ubyte0_e32 v136, v39
	v_cvt_f32_ubyte1_e32 v137, v39
	v_cvt_f32_ubyte2_e32 v138, v39
	v_cvt_f32_ubyte3_e32 v139, v39
	s_lshl_b32 s30, s75, 12
	s_add_u32 s28, s26, s30
	s_addc_u32 s29, s27, 0
	global_load_dwordx2 v[38:39], v162, s[28:29]
	v_fmac_f32_e32 v178, s25, v132
	v_fmac_f32_e32 v179, s25, v133
	v_fmac_f32_e32 v180, s25, v134
	v_fmac_f32_e32 v181, s25, v135
	v_fmac_f32_e32 v182, s25, v136
	v_fmac_f32_e32 v183, s25, v137
	v_fmac_f32_e32 v184, s25, v138
	v_fmac_f32_e32 v185, s25, v139
	s_waitcnt vmcnt(31)
	v_readlane_b32 s25, v246, 40
	v_cvt_f32_ubyte0_e32 v124, v40
	v_cvt_f32_ubyte1_e32 v125, v40
	v_cvt_f32_ubyte2_e32 v126, v40
	v_cvt_f32_ubyte3_e32 v127, v40
	v_cvt_f32_ubyte0_e32 v128, v41
	v_cvt_f32_ubyte1_e32 v129, v41
	v_cvt_f32_ubyte2_e32 v130, v41
	v_cvt_f32_ubyte3_e32 v131, v41
	s_lshl_b32 s30, s76, 12
	s_add_u32 s28, s26, s30
	s_addc_u32 s29, s27, 0
	global_load_dwordx2 v[40:41], v162, s[28:29]
	v_fmac_f32_e32 v178, s25, v124
	v_fmac_f32_e32 v179, s25, v125
	v_fmac_f32_e32 v180, s25, v126
	v_fmac_f32_e32 v181, s25, v127
	v_fmac_f32_e32 v182, s25, v128
	v_fmac_f32_e32 v183, s25, v129
	v_fmac_f32_e32 v184, s25, v130
	v_fmac_f32_e32 v185, s25, v131
	s_waitcnt vmcnt(31)
	v_readlane_b32 s25, v246, 41
	v_cvt_f32_ubyte0_e32 v132, v42
	v_cvt_f32_ubyte1_e32 v133, v42
	v_cvt_f32_ubyte2_e32 v134, v42
	v_cvt_f32_ubyte3_e32 v135, v42
	v_cvt_f32_ubyte0_e32 v136, v43
	v_cvt_f32_ubyte1_e32 v137, v43
	v_cvt_f32_ubyte2_e32 v138, v43
	v_cvt_f32_ubyte3_e32 v139, v43
	s_lshl_b32 s30, s77, 12
	s_add_u32 s28, s26, s30
	s_addc_u32 s29, s27, 0
	global_load_dwordx2 v[42:43], v162, s[28:29]
	v_fmac_f32_e32 v178, s25, v132
	v_fmac_f32_e32 v179, s25, v133
	v_fmac_f32_e32 v180, s25, v134
	v_fmac_f32_e32 v181, s25, v135
	v_fmac_f32_e32 v182, s25, v136
	v_fmac_f32_e32 v183, s25, v137
	v_fmac_f32_e32 v184, s25, v138
	v_fmac_f32_e32 v185, s25, v139
	s_waitcnt vmcnt(31)
	v_readlane_b32 s25, v246, 42
	v_cvt_f32_ubyte0_e32 v124, v44
	v_cvt_f32_ubyte1_e32 v125, v44
	v_cvt_f32_ubyte2_e32 v126, v44
	v_cvt_f32_ubyte3_e32 v127, v44
	v_cvt_f32_ubyte0_e32 v128, v45
	v_cvt_f32_ubyte1_e32 v129, v45
	v_cvt_f32_ubyte2_e32 v130, v45
	v_cvt_f32_ubyte3_e32 v131, v45
	s_lshl_b32 s30, s78, 12
	s_add_u32 s28, s26, s30
	s_addc_u32 s29, s27, 0
	global_load_dwordx2 v[44:45], v162, s[28:29]
	v_fmac_f32_e32 v178, s25, v124
	v_fmac_f32_e32 v179, s25, v125
	v_fmac_f32_e32 v180, s25, v126
	v_fmac_f32_e32 v181, s25, v127
	v_fmac_f32_e32 v182, s25, v128
	v_fmac_f32_e32 v183, s25, v129
	v_fmac_f32_e32 v184, s25, v130
	v_fmac_f32_e32 v185, s25, v131
	s_waitcnt vmcnt(31)
	v_readlane_b32 s25, v246, 43
	v_cvt_f32_ubyte0_e32 v132, v46
	v_cvt_f32_ubyte1_e32 v133, v46
	v_cvt_f32_ubyte2_e32 v134, v46
	v_cvt_f32_ubyte3_e32 v135, v46
	v_cvt_f32_ubyte0_e32 v136, v47
	v_cvt_f32_ubyte1_e32 v137, v47
	v_cvt_f32_ubyte2_e32 v138, v47
	v_cvt_f32_ubyte3_e32 v139, v47
	s_lshl_b32 s30, s79, 12
	s_add_u32 s28, s26, s30
	s_addc_u32 s29, s27, 0
	global_load_dwordx2 v[46:47], v162, s[28:29]
	v_fmac_f32_e32 v178, s25, v132
	v_fmac_f32_e32 v179, s25, v133
	v_fmac_f32_e32 v180, s25, v134
	v_fmac_f32_e32 v181, s25, v135
	v_fmac_f32_e32 v182, s25, v136
	v_fmac_f32_e32 v183, s25, v137
	v_fmac_f32_e32 v184, s25, v138
	v_fmac_f32_e32 v185, s25, v139
	s_waitcnt vmcnt(31)
	v_readlane_b32 s25, v246, 44
	v_cvt_f32_ubyte0_e32 v124, v48
	v_cvt_f32_ubyte1_e32 v125, v48
	v_cvt_f32_ubyte2_e32 v126, v48
	v_cvt_f32_ubyte3_e32 v127, v48
	v_cvt_f32_ubyte0_e32 v128, v49
	v_cvt_f32_ubyte1_e32 v129, v49
	v_cvt_f32_ubyte2_e32 v130, v49
	v_cvt_f32_ubyte3_e32 v131, v49
	s_lshl_b32 s30, s80, 12
	s_add_u32 s28, s26, s30
	s_addc_u32 s29, s27, 0
	global_load_dwordx2 v[48:49], v162, s[28:29]
	v_fmac_f32_e32 v178, s25, v124
	v_fmac_f32_e32 v179, s25, v125
	v_fmac_f32_e32 v180, s25, v126
	v_fmac_f32_e32 v181, s25, v127
	v_fmac_f32_e32 v182, s25, v128
	v_fmac_f32_e32 v183, s25, v129
	v_fmac_f32_e32 v184, s25, v130
	v_fmac_f32_e32 v185, s25, v131
	s_waitcnt vmcnt(31)
	v_readlane_b32 s25, v246, 45
	v_cvt_f32_ubyte0_e32 v132, v50
	v_cvt_f32_ubyte1_e32 v133, v50
	v_cvt_f32_ubyte2_e32 v134, v50
	v_cvt_f32_ubyte3_e32 v135, v50
	v_cvt_f32_ubyte0_e32 v136, v51
	v_cvt_f32_ubyte1_e32 v137, v51
	v_cvt_f32_ubyte2_e32 v138, v51
	v_cvt_f32_ubyte3_e32 v139, v51
	s_lshl_b32 s30, s81, 12
	s_add_u32 s28, s26, s30
	s_addc_u32 s29, s27, 0
	global_load_dwordx2 v[50:51], v162, s[28:29]
	v_fmac_f32_e32 v178, s25, v132
	v_fmac_f32_e32 v179, s25, v133
	v_fmac_f32_e32 v180, s25, v134
	v_fmac_f32_e32 v181, s25, v135
	v_fmac_f32_e32 v182, s25, v136
	v_fmac_f32_e32 v183, s25, v137
	v_fmac_f32_e32 v184, s25, v138
	v_fmac_f32_e32 v185, s25, v139
	s_waitcnt vmcnt(31)
	v_readlane_b32 s25, v246, 46
	v_cvt_f32_ubyte0_e32 v124, v52
	v_cvt_f32_ubyte1_e32 v125, v52
	v_cvt_f32_ubyte2_e32 v126, v52
	v_cvt_f32_ubyte3_e32 v127, v52
	v_cvt_f32_ubyte0_e32 v128, v53
	v_cvt_f32_ubyte1_e32 v129, v53
	v_cvt_f32_ubyte2_e32 v130, v53
	v_cvt_f32_ubyte3_e32 v131, v53
	s_lshl_b32 s30, s82, 12
	s_add_u32 s28, s26, s30
	s_addc_u32 s29, s27, 0
	global_load_dwordx2 v[52:53], v162, s[28:29]
	v_fmac_f32_e32 v178, s25, v124
	v_fmac_f32_e32 v179, s25, v125
	v_fmac_f32_e32 v180, s25, v126
	v_fmac_f32_e32 v181, s25, v127
	v_fmac_f32_e32 v182, s25, v128
	v_fmac_f32_e32 v183, s25, v129
	v_fmac_f32_e32 v184, s25, v130
	v_fmac_f32_e32 v185, s25, v131
	s_waitcnt vmcnt(31)
	v_readlane_b32 s25, v246, 47
	v_cvt_f32_ubyte0_e32 v132, v54
	v_cvt_f32_ubyte1_e32 v133, v54
	v_cvt_f32_ubyte2_e32 v134, v54
	v_cvt_f32_ubyte3_e32 v135, v54
	v_cvt_f32_ubyte0_e32 v136, v55
	v_cvt_f32_ubyte1_e32 v137, v55
	v_cvt_f32_ubyte2_e32 v138, v55
	v_cvt_f32_ubyte3_e32 v139, v55
	s_lshl_b32 s30, s83, 12
	s_add_u32 s28, s26, s30
	s_addc_u32 s29, s27, 0
	global_load_dwordx2 v[54:55], v162, s[28:29]
	v_fmac_f32_e32 v178, s25, v132
	v_fmac_f32_e32 v179, s25, v133
	v_fmac_f32_e32 v180, s25, v134
	v_fmac_f32_e32 v181, s25, v135
	v_fmac_f32_e32 v182, s25, v136
	v_fmac_f32_e32 v183, s25, v137
	v_fmac_f32_e32 v184, s25, v138
	v_fmac_f32_e32 v185, s25, v139
	s_waitcnt vmcnt(31)
	v_readlane_b32 s25, v246, 48
	v_cvt_f32_ubyte0_e32 v124, v56
	v_cvt_f32_ubyte1_e32 v125, v56
	v_cvt_f32_ubyte2_e32 v126, v56
	v_cvt_f32_ubyte3_e32 v127, v56
	v_cvt_f32_ubyte0_e32 v128, v57
	v_cvt_f32_ubyte1_e32 v129, v57
	v_cvt_f32_ubyte2_e32 v130, v57
	v_cvt_f32_ubyte3_e32 v131, v57
	s_waitcnt lgkmcnt(0)
	s_load_dwordx16 s[68:83], s[36:37], 0x180 glc
	s_lshl_b32 s30, s84, 12
	s_add_u32 s28, s26, s30
	s_addc_u32 s29, s27, 0
	global_load_dwordx2 v[56:57], v162, s[28:29]
	v_fmac_f32_e32 v178, s25, v124
	v_fmac_f32_e32 v179, s25, v125
	v_fmac_f32_e32 v180, s25, v126
	v_fmac_f32_e32 v181, s25, v127
	v_fmac_f32_e32 v182, s25, v128
	v_fmac_f32_e32 v183, s25, v129
	v_fmac_f32_e32 v184, s25, v130
	v_fmac_f32_e32 v185, s25, v131
	s_waitcnt vmcnt(31)
	v_readlane_b32 s25, v246, 49
	v_cvt_f32_ubyte0_e32 v132, v58
	v_cvt_f32_ubyte1_e32 v133, v58
	v_cvt_f32_ubyte2_e32 v134, v58
	v_cvt_f32_ubyte3_e32 v135, v58
	v_cvt_f32_ubyte0_e32 v136, v59
	v_cvt_f32_ubyte1_e32 v137, v59
	v_cvt_f32_ubyte2_e32 v138, v59
	v_cvt_f32_ubyte3_e32 v139, v59
	s_lshl_b32 s30, s85, 12
	s_add_u32 s28, s26, s30
	s_addc_u32 s29, s27, 0
	global_load_dwordx2 v[58:59], v162, s[28:29]
	v_fmac_f32_e32 v178, s25, v132
	v_fmac_f32_e32 v179, s25, v133
	v_fmac_f32_e32 v180, s25, v134
	v_fmac_f32_e32 v181, s25, v135
	v_fmac_f32_e32 v182, s25, v136
	v_fmac_f32_e32 v183, s25, v137
	v_fmac_f32_e32 v184, s25, v138
	v_fmac_f32_e32 v185, s25, v139
	s_waitcnt vmcnt(31)
	v_readlane_b32 s25, v246, 50
	v_cvt_f32_ubyte0_e32 v124, v60
	v_cvt_f32_ubyte1_e32 v125, v60
	v_cvt_f32_ubyte2_e32 v126, v60
	v_cvt_f32_ubyte3_e32 v127, v60
	v_cvt_f32_ubyte0_e32 v128, v61
	v_cvt_f32_ubyte1_e32 v129, v61
	v_cvt_f32_ubyte2_e32 v130, v61
	v_cvt_f32_ubyte3_e32 v131, v61
	s_lshl_b32 s30, s86, 12
	s_add_u32 s28, s26, s30
	s_addc_u32 s29, s27, 0
	global_load_dwordx2 v[60:61], v162, s[28:29]
	v_fmac_f32_e32 v178, s25, v124
	v_fmac_f32_e32 v179, s25, v125
	v_fmac_f32_e32 v180, s25, v126
	v_fmac_f32_e32 v181, s25, v127
	v_fmac_f32_e32 v182, s25, v128
	v_fmac_f32_e32 v183, s25, v129
	v_fmac_f32_e32 v184, s25, v130
	v_fmac_f32_e32 v185, s25, v131
	s_waitcnt vmcnt(31)
	v_readlane_b32 s25, v246, 51
	v_cvt_f32_ubyte0_e32 v132, v62
	v_cvt_f32_ubyte1_e32 v133, v62
	v_cvt_f32_ubyte2_e32 v134, v62
	v_cvt_f32_ubyte3_e32 v135, v62
	v_cvt_f32_ubyte0_e32 v136, v63
	v_cvt_f32_ubyte1_e32 v137, v63
	v_cvt_f32_ubyte2_e32 v138, v63
	v_cvt_f32_ubyte3_e32 v139, v63
	s_lshl_b32 s30, s87, 12
	s_add_u32 s28, s26, s30
	s_addc_u32 s29, s27, 0
	global_load_dwordx2 v[62:63], v162, s[28:29]
	v_fmac_f32_e32 v178, s25, v132
	v_fmac_f32_e32 v179, s25, v133
	v_fmac_f32_e32 v180, s25, v134
	v_fmac_f32_e32 v181, s25, v135
	v_fmac_f32_e32 v182, s25, v136
	v_fmac_f32_e32 v183, s25, v137
	v_fmac_f32_e32 v184, s25, v138
	v_fmac_f32_e32 v185, s25, v139
	s_waitcnt vmcnt(31)
	v_readlane_b32 s25, v246, 52
	v_cvt_f32_ubyte0_e32 v124, v64
	v_cvt_f32_ubyte1_e32 v125, v64
	v_cvt_f32_ubyte2_e32 v126, v64
	v_cvt_f32_ubyte3_e32 v127, v64
	v_cvt_f32_ubyte0_e32 v128, v65
	v_cvt_f32_ubyte1_e32 v129, v65
	v_cvt_f32_ubyte2_e32 v130, v65
	v_cvt_f32_ubyte3_e32 v131, v65
	s_lshl_b32 s30, s88, 12
	s_add_u32 s28, s26, s30
	s_addc_u32 s29, s27, 0
	global_load_dwordx2 v[64:65], v162, s[28:29]
	v_fmac_f32_e32 v178, s25, v124
	v_fmac_f32_e32 v179, s25, v125
	v_fmac_f32_e32 v180, s25, v126
	v_fmac_f32_e32 v181, s25, v127
	v_fmac_f32_e32 v182, s25, v128
	v_fmac_f32_e32 v183, s25, v129
	v_fmac_f32_e32 v184, s25, v130
	v_fmac_f32_e32 v185, s25, v131
	s_waitcnt vmcnt(31)
	v_readlane_b32 s25, v246, 53
	v_cvt_f32_ubyte0_e32 v132, v66
	v_cvt_f32_ubyte1_e32 v133, v66
	v_cvt_f32_ubyte2_e32 v134, v66
	v_cvt_f32_ubyte3_e32 v135, v66
	v_cvt_f32_ubyte0_e32 v136, v67
	v_cvt_f32_ubyte1_e32 v137, v67
	v_cvt_f32_ubyte2_e32 v138, v67
	v_cvt_f32_ubyte3_e32 v139, v67
	s_lshl_b32 s30, s89, 12
	s_add_u32 s28, s26, s30
	s_addc_u32 s29, s27, 0
	global_load_dwordx2 v[66:67], v162, s[28:29]
	v_fmac_f32_e32 v178, s25, v132
	v_fmac_f32_e32 v179, s25, v133
	v_fmac_f32_e32 v180, s25, v134
	v_fmac_f32_e32 v181, s25, v135
	v_fmac_f32_e32 v182, s25, v136
	v_fmac_f32_e32 v183, s25, v137
	v_fmac_f32_e32 v184, s25, v138
	v_fmac_f32_e32 v185, s25, v139
	s_waitcnt vmcnt(31)
	v_readlane_b32 s25, v246, 54
	v_cvt_f32_ubyte0_e32 v124, v68
	v_cvt_f32_ubyte1_e32 v125, v68
	v_cvt_f32_ubyte2_e32 v126, v68
	v_cvt_f32_ubyte3_e32 v127, v68
	v_cvt_f32_ubyte0_e32 v128, v69
	v_cvt_f32_ubyte1_e32 v129, v69
	v_cvt_f32_ubyte2_e32 v130, v69
	v_cvt_f32_ubyte3_e32 v131, v69
	s_lshl_b32 s30, s90, 12
	s_add_u32 s28, s26, s30
	s_addc_u32 s29, s27, 0
	global_load_dwordx2 v[68:69], v162, s[28:29]
	v_fmac_f32_e32 v178, s25, v124
	v_fmac_f32_e32 v179, s25, v125
	v_fmac_f32_e32 v180, s25, v126
	v_fmac_f32_e32 v181, s25, v127
	v_fmac_f32_e32 v182, s25, v128
	v_fmac_f32_e32 v183, s25, v129
	v_fmac_f32_e32 v184, s25, v130
	v_fmac_f32_e32 v185, s25, v131
	s_waitcnt vmcnt(31)
	v_readlane_b32 s25, v246, 55
	v_cvt_f32_ubyte0_e32 v132, v70
	v_cvt_f32_ubyte1_e32 v133, v70
	v_cvt_f32_ubyte2_e32 v134, v70
	v_cvt_f32_ubyte3_e32 v135, v70
	v_cvt_f32_ubyte0_e32 v136, v71
	v_cvt_f32_ubyte1_e32 v137, v71
	v_cvt_f32_ubyte2_e32 v138, v71
	v_cvt_f32_ubyte3_e32 v139, v71
	s_lshl_b32 s30, s91, 12
	s_add_u32 s28, s26, s30
	s_addc_u32 s29, s27, 0
	global_load_dwordx2 v[70:71], v162, s[28:29]
	v_fmac_f32_e32 v178, s25, v132
	v_fmac_f32_e32 v179, s25, v133
	v_fmac_f32_e32 v180, s25, v134
	v_fmac_f32_e32 v181, s25, v135
	v_fmac_f32_e32 v182, s25, v136
	v_fmac_f32_e32 v183, s25, v137
	v_fmac_f32_e32 v184, s25, v138
	v_fmac_f32_e32 v185, s25, v139
	s_waitcnt vmcnt(31)
	v_readlane_b32 s25, v246, 56
	v_cvt_f32_ubyte0_e32 v124, v72
	v_cvt_f32_ubyte1_e32 v125, v72
	v_cvt_f32_ubyte2_e32 v126, v72
	v_cvt_f32_ubyte3_e32 v127, v72
	v_cvt_f32_ubyte0_e32 v128, v73
	v_cvt_f32_ubyte1_e32 v129, v73
	v_cvt_f32_ubyte2_e32 v130, v73
	v_cvt_f32_ubyte3_e32 v131, v73
	s_lshl_b32 s30, s92, 12
	s_add_u32 s28, s26, s30
	s_addc_u32 s29, s27, 0
	global_load_dwordx2 v[72:73], v162, s[28:29]
	v_fmac_f32_e32 v178, s25, v124
	v_fmac_f32_e32 v179, s25, v125
	v_fmac_f32_e32 v180, s25, v126
	v_fmac_f32_e32 v181, s25, v127
	v_fmac_f32_e32 v182, s25, v128
	v_fmac_f32_e32 v183, s25, v129
	v_fmac_f32_e32 v184, s25, v130
	v_fmac_f32_e32 v185, s25, v131
	s_waitcnt vmcnt(31)
	v_readlane_b32 s25, v246, 57
	v_cvt_f32_ubyte0_e32 v132, v74
	v_cvt_f32_ubyte1_e32 v133, v74
	v_cvt_f32_ubyte2_e32 v134, v74
	v_cvt_f32_ubyte3_e32 v135, v74
	v_cvt_f32_ubyte0_e32 v136, v75
	v_cvt_f32_ubyte1_e32 v137, v75
	v_cvt_f32_ubyte2_e32 v138, v75
	v_cvt_f32_ubyte3_e32 v139, v75
	s_lshl_b32 s30, s93, 12
	s_add_u32 s28, s26, s30
	s_addc_u32 s29, s27, 0
	global_load_dwordx2 v[74:75], v162, s[28:29]
	v_fmac_f32_e32 v178, s25, v132
	v_fmac_f32_e32 v179, s25, v133
	v_fmac_f32_e32 v180, s25, v134
	v_fmac_f32_e32 v181, s25, v135
	v_fmac_f32_e32 v182, s25, v136
	v_fmac_f32_e32 v183, s25, v137
	v_fmac_f32_e32 v184, s25, v138
	v_fmac_f32_e32 v185, s25, v139
	s_waitcnt vmcnt(31)
	v_readlane_b32 s25, v246, 58
	v_cvt_f32_ubyte0_e32 v124, v76
	v_cvt_f32_ubyte1_e32 v125, v76
	v_cvt_f32_ubyte2_e32 v126, v76
	v_cvt_f32_ubyte3_e32 v127, v76
	v_cvt_f32_ubyte0_e32 v128, v77
	v_cvt_f32_ubyte1_e32 v129, v77
	v_cvt_f32_ubyte2_e32 v130, v77
	v_cvt_f32_ubyte3_e32 v131, v77
	s_lshl_b32 s30, s94, 12
	s_add_u32 s28, s26, s30
	s_addc_u32 s29, s27, 0
	global_load_dwordx2 v[76:77], v162, s[28:29]
	v_fmac_f32_e32 v178, s25, v124
	v_fmac_f32_e32 v179, s25, v125
	v_fmac_f32_e32 v180, s25, v126
	v_fmac_f32_e32 v181, s25, v127
	v_fmac_f32_e32 v182, s25, v128
	v_fmac_f32_e32 v183, s25, v129
	v_fmac_f32_e32 v184, s25, v130
	v_fmac_f32_e32 v185, s25, v131
	s_waitcnt vmcnt(31)
	v_readlane_b32 s25, v246, 59
	v_cvt_f32_ubyte0_e32 v132, v78
	v_cvt_f32_ubyte1_e32 v133, v78
	v_cvt_f32_ubyte2_e32 v134, v78
	v_cvt_f32_ubyte3_e32 v135, v78
	v_cvt_f32_ubyte0_e32 v136, v79
	v_cvt_f32_ubyte1_e32 v137, v79
	v_cvt_f32_ubyte2_e32 v138, v79
	v_cvt_f32_ubyte3_e32 v139, v79
	s_lshl_b32 s30, s95, 12
	s_add_u32 s28, s26, s30
	s_addc_u32 s29, s27, 0
	global_load_dwordx2 v[78:79], v162, s[28:29]
	v_fmac_f32_e32 v178, s25, v132
	v_fmac_f32_e32 v179, s25, v133
	v_fmac_f32_e32 v180, s25, v134
	v_fmac_f32_e32 v181, s25, v135
	v_fmac_f32_e32 v182, s25, v136
	v_fmac_f32_e32 v183, s25, v137
	v_fmac_f32_e32 v184, s25, v138
	v_fmac_f32_e32 v185, s25, v139
	s_waitcnt vmcnt(31)
	v_readlane_b32 s25, v246, 60
	v_cvt_f32_ubyte0_e32 v124, v80
	v_cvt_f32_ubyte1_e32 v125, v80
	v_cvt_f32_ubyte2_e32 v126, v80
	v_cvt_f32_ubyte3_e32 v127, v80
	v_cvt_f32_ubyte0_e32 v128, v81
	v_cvt_f32_ubyte1_e32 v129, v81
	v_cvt_f32_ubyte2_e32 v130, v81
	v_cvt_f32_ubyte3_e32 v131, v81
	s_lshl_b32 s30, s96, 12
	s_add_u32 s28, s26, s30
	s_addc_u32 s29, s27, 0
	global_load_dwordx2 v[80:81], v162, s[28:29]
	v_fmac_f32_e32 v178, s25, v124
	v_fmac_f32_e32 v179, s25, v125
	v_fmac_f32_e32 v180, s25, v126
	v_fmac_f32_e32 v181, s25, v127
	v_fmac_f32_e32 v182, s25, v128
	v_fmac_f32_e32 v183, s25, v129
	v_fmac_f32_e32 v184, s25, v130
	v_fmac_f32_e32 v185, s25, v131
	s_waitcnt vmcnt(31)
	v_readlane_b32 s25, v246, 61
	v_cvt_f32_ubyte0_e32 v132, v82
	v_cvt_f32_ubyte1_e32 v133, v82
	v_cvt_f32_ubyte2_e32 v134, v82
	v_cvt_f32_ubyte3_e32 v135, v82
	v_cvt_f32_ubyte0_e32 v136, v83
	v_cvt_f32_ubyte1_e32 v137, v83
	v_cvt_f32_ubyte2_e32 v138, v83
	v_cvt_f32_ubyte3_e32 v139, v83
	s_lshl_b32 s30, s97, 12
	s_add_u32 s28, s26, s30
	s_addc_u32 s29, s27, 0
	global_load_dwordx2 v[82:83], v162, s[28:29]
	v_fmac_f32_e32 v178, s25, v132
	v_fmac_f32_e32 v179, s25, v133
	v_fmac_f32_e32 v180, s25, v134
	v_fmac_f32_e32 v181, s25, v135
	v_fmac_f32_e32 v182, s25, v136
	v_fmac_f32_e32 v183, s25, v137
	v_fmac_f32_e32 v184, s25, v138
	v_fmac_f32_e32 v185, s25, v139
	s_waitcnt vmcnt(31)
	v_readlane_b32 s25, v246, 62
	v_cvt_f32_ubyte0_e32 v124, v84
	v_cvt_f32_ubyte1_e32 v125, v84
	v_cvt_f32_ubyte2_e32 v126, v84
	v_cvt_f32_ubyte3_e32 v127, v84
	v_cvt_f32_ubyte0_e32 v128, v85
	v_cvt_f32_ubyte1_e32 v129, v85
	v_cvt_f32_ubyte2_e32 v130, v85
	v_cvt_f32_ubyte3_e32 v131, v85
	s_lshl_b32 s30, s98, 12
	s_add_u32 s28, s26, s30
	s_addc_u32 s29, s27, 0
	global_load_dwordx2 v[84:85], v162, s[28:29]
	v_fmac_f32_e32 v178, s25, v124
	v_fmac_f32_e32 v179, s25, v125
	v_fmac_f32_e32 v180, s25, v126
	v_fmac_f32_e32 v181, s25, v127
	v_fmac_f32_e32 v182, s25, v128
	v_fmac_f32_e32 v183, s25, v129
	v_fmac_f32_e32 v184, s25, v130
	v_fmac_f32_e32 v185, s25, v131
	s_waitcnt vmcnt(31)
	v_readlane_b32 s25, v246, 63
	v_cvt_f32_ubyte0_e32 v132, v86
	v_cvt_f32_ubyte1_e32 v133, v86
	v_cvt_f32_ubyte2_e32 v134, v86
	v_cvt_f32_ubyte3_e32 v135, v86
	v_cvt_f32_ubyte0_e32 v136, v87
	v_cvt_f32_ubyte1_e32 v137, v87
	v_cvt_f32_ubyte2_e32 v138, v87
	v_cvt_f32_ubyte3_e32 v139, v87
	s_lshl_b32 s30, s99, 12
	s_add_u32 s28, s26, s30
	s_addc_u32 s29, s27, 0
	global_load_dwordx2 v[86:87], v162, s[28:29]
	v_fmac_f32_e32 v178, s25, v132
	v_fmac_f32_e32 v179, s25, v133
	v_fmac_f32_e32 v180, s25, v134
	v_fmac_f32_e32 v181, s25, v135
	v_fmac_f32_e32 v182, s25, v136
	v_fmac_f32_e32 v183, s25, v137
	v_fmac_f32_e32 v184, s25, v138
	v_fmac_f32_e32 v185, s25, v139
	s_waitcnt vmcnt(31)
	v_readlane_b32 s25, v247, 0
	v_cvt_f32_ubyte0_e32 v124, v24
	v_cvt_f32_ubyte1_e32 v125, v24
	v_cvt_f32_ubyte2_e32 v126, v24
	v_cvt_f32_ubyte3_e32 v127, v24
	v_cvt_f32_ubyte0_e32 v128, v25
	v_cvt_f32_ubyte1_e32 v129, v25
	v_cvt_f32_ubyte2_e32 v130, v25
	v_cvt_f32_ubyte3_e32 v131, v25
	s_waitcnt lgkmcnt(0)
	s_load_dwordx16 s[84:99], s[36:37], 0x1c0 glc
	s_lshl_b32 s30, s68, 12
	s_add_u32 s28, s26, s30
	s_addc_u32 s29, s27, 0
	global_load_dwordx2 v[24:25], v162, s[28:29]
	v_lshlrev_b32_e32 v16, 2, v122
	v_lshlrev_b32_e32 v17, 2, v123
	global_load_dword v238, v16, s[64:65]
	global_load_dword v240, v16, s[60:61]
	global_load_dword v239, v17, s[64:65]
	global_load_dword v241, v17, s[60:61]
	v_fmac_f32_e32 v178, s25, v124
	v_fmac_f32_e32 v179, s25, v125
	v_fmac_f32_e32 v180, s25, v126
	v_fmac_f32_e32 v181, s25, v127
	v_fmac_f32_e32 v182, s25, v128
	v_fmac_f32_e32 v183, s25, v129
	v_fmac_f32_e32 v184, s25, v130
	v_fmac_f32_e32 v185, s25, v131
	s_waitcnt vmcnt(35)
	v_readlane_b32 s25, v247, 1
	v_cvt_f32_ubyte0_e32 v132, v26
	v_cvt_f32_ubyte1_e32 v133, v26
	v_cvt_f32_ubyte2_e32 v134, v26
	v_cvt_f32_ubyte3_e32 v135, v26
	v_cvt_f32_ubyte0_e32 v136, v27
	v_cvt_f32_ubyte1_e32 v137, v27
	v_cvt_f32_ubyte2_e32 v138, v27
	v_cvt_f32_ubyte3_e32 v139, v27
	s_lshl_b32 s30, s69, 12
	s_add_u32 s28, s26, s30
	s_addc_u32 s29, s27, 0
	global_load_dwordx2 v[26:27], v162, s[28:29]
	v_fmac_f32_e32 v178, s25, v132
	v_fmac_f32_e32 v179, s25, v133
	v_fmac_f32_e32 v180, s25, v134
	v_fmac_f32_e32 v181, s25, v135
	v_fmac_f32_e32 v182, s25, v136
	v_fmac_f32_e32 v183, s25, v137
	v_fmac_f32_e32 v184, s25, v138
	v_fmac_f32_e32 v185, s25, v139
	s_waitcnt vmcnt(35)
	v_readlane_b32 s25, v247, 2
	v_cvt_f32_ubyte0_e32 v124, v28
	v_cvt_f32_ubyte1_e32 v125, v28
	v_cvt_f32_ubyte2_e32 v126, v28
	v_cvt_f32_ubyte3_e32 v127, v28
	v_cvt_f32_ubyte0_e32 v128, v29
	v_cvt_f32_ubyte1_e32 v129, v29
	v_cvt_f32_ubyte2_e32 v130, v29
	v_cvt_f32_ubyte3_e32 v131, v29
	s_lshl_b32 s30, s70, 12
	s_add_u32 s28, s26, s30
	s_addc_u32 s29, s27, 0
	global_load_dwordx2 v[28:29], v162, s[28:29]
	v_fmac_f32_e32 v178, s25, v124
	v_fmac_f32_e32 v179, s25, v125
	v_fmac_f32_e32 v180, s25, v126
	v_fmac_f32_e32 v181, s25, v127
	v_fmac_f32_e32 v182, s25, v128
	v_fmac_f32_e32 v183, s25, v129
	v_fmac_f32_e32 v184, s25, v130
	v_fmac_f32_e32 v185, s25, v131
	s_waitcnt vmcnt(35)
	v_readlane_b32 s25, v247, 3
	v_cvt_f32_ubyte0_e32 v132, v30
	v_cvt_f32_ubyte1_e32 v133, v30
	v_cvt_f32_ubyte2_e32 v134, v30
	v_cvt_f32_ubyte3_e32 v135, v30
	v_cvt_f32_ubyte0_e32 v136, v31
	v_cvt_f32_ubyte1_e32 v137, v31
	v_cvt_f32_ubyte2_e32 v138, v31
	v_cvt_f32_ubyte3_e32 v139, v31
	s_lshl_b32 s30, s71, 12
	s_add_u32 s28, s26, s30
	s_addc_u32 s29, s27, 0
	global_load_dwordx2 v[30:31], v162, s[28:29]
	v_fmac_f32_e32 v178, s25, v132
	v_fmac_f32_e32 v179, s25, v133
	v_fmac_f32_e32 v180, s25, v134
	v_fmac_f32_e32 v181, s25, v135
	v_fmac_f32_e32 v182, s25, v136
	v_fmac_f32_e32 v183, s25, v137
	v_fmac_f32_e32 v184, s25, v138
	v_fmac_f32_e32 v185, s25, v139
	s_waitcnt vmcnt(35)
	v_readlane_b32 s25, v247, 4
	v_cvt_f32_ubyte0_e32 v124, v32
	v_cvt_f32_ubyte1_e32 v125, v32
	v_cvt_f32_ubyte2_e32 v126, v32
	v_cvt_f32_ubyte3_e32 v127, v32
	v_cvt_f32_ubyte0_e32 v128, v33
	v_cvt_f32_ubyte1_e32 v129, v33
	v_cvt_f32_ubyte2_e32 v130, v33
	v_cvt_f32_ubyte3_e32 v131, v33
	s_lshl_b32 s30, s72, 12
	s_add_u32 s28, s26, s30
	s_addc_u32 s29, s27, 0
	global_load_dwordx2 v[32:33], v162, s[28:29]
	v_fmac_f32_e32 v178, s25, v124
	v_fmac_f32_e32 v179, s25, v125
	v_fmac_f32_e32 v180, s25, v126
	v_fmac_f32_e32 v181, s25, v127
	v_fmac_f32_e32 v182, s25, v128
	v_fmac_f32_e32 v183, s25, v129
	v_fmac_f32_e32 v184, s25, v130
	v_fmac_f32_e32 v185, s25, v131
	s_waitcnt vmcnt(35)
	v_readlane_b32 s25, v247, 5
	v_cvt_f32_ubyte0_e32 v132, v34
	v_cvt_f32_ubyte1_e32 v133, v34
	v_cvt_f32_ubyte2_e32 v134, v34
	v_cvt_f32_ubyte3_e32 v135, v34
	v_cvt_f32_ubyte0_e32 v136, v35
	v_cvt_f32_ubyte1_e32 v137, v35
	v_cvt_f32_ubyte2_e32 v138, v35
	v_cvt_f32_ubyte3_e32 v139, v35
	s_lshl_b32 s30, s73, 12
	s_add_u32 s28, s26, s30
	s_addc_u32 s29, s27, 0
	global_load_dwordx2 v[34:35], v162, s[28:29]
	v_fmac_f32_e32 v178, s25, v132
	v_fmac_f32_e32 v179, s25, v133
	v_fmac_f32_e32 v180, s25, v134
	v_fmac_f32_e32 v181, s25, v135
	v_fmac_f32_e32 v182, s25, v136
	v_fmac_f32_e32 v183, s25, v137
	v_fmac_f32_e32 v184, s25, v138
	v_fmac_f32_e32 v185, s25, v139
	s_waitcnt vmcnt(35)
	v_readlane_b32 s25, v247, 6
	v_cvt_f32_ubyte0_e32 v124, v36
	v_cvt_f32_ubyte1_e32 v125, v36
	v_cvt_f32_ubyte2_e32 v126, v36
	v_cvt_f32_ubyte3_e32 v127, v36
	v_cvt_f32_ubyte0_e32 v128, v37
	v_cvt_f32_ubyte1_e32 v129, v37
	v_cvt_f32_ubyte2_e32 v130, v37
	v_cvt_f32_ubyte3_e32 v131, v37
	s_lshl_b32 s30, s74, 12
	s_add_u32 s28, s26, s30
	s_addc_u32 s29, s27, 0
	global_load_dwordx2 v[36:37], v162, s[28:29]
	v_fmac_f32_e32 v178, s25, v124
	v_fmac_f32_e32 v179, s25, v125
	v_fmac_f32_e32 v180, s25, v126
	v_fmac_f32_e32 v181, s25, v127
	v_fmac_f32_e32 v182, s25, v128
	v_fmac_f32_e32 v183, s25, v129
	v_fmac_f32_e32 v184, s25, v130
	v_fmac_f32_e32 v185, s25, v131
	s_waitcnt vmcnt(35)
	v_readlane_b32 s25, v247, 7
	v_cvt_f32_ubyte0_e32 v132, v38
	v_cvt_f32_ubyte1_e32 v133, v38
	v_cvt_f32_ubyte2_e32 v134, v38
	v_cvt_f32_ubyte3_e32 v135, v38
	v_cvt_f32_ubyte0_e32 v136, v39
	v_cvt_f32_ubyte1_e32 v137, v39
	v_cvt_f32_ubyte2_e32 v138, v39
	v_cvt_f32_ubyte3_e32 v139, v39
	s_lshl_b32 s30, s75, 12
	s_add_u32 s28, s26, s30
	s_addc_u32 s29, s27, 0
	global_load_dwordx2 v[38:39], v162, s[28:29]
	v_fmac_f32_e32 v178, s25, v132
	v_fmac_f32_e32 v179, s25, v133
	v_fmac_f32_e32 v180, s25, v134
	v_fmac_f32_e32 v181, s25, v135
	v_fmac_f32_e32 v182, s25, v136
	v_fmac_f32_e32 v183, s25, v137
	v_fmac_f32_e32 v184, s25, v138
	v_fmac_f32_e32 v185, s25, v139
	s_waitcnt vmcnt(35)
	v_readlane_b32 s25, v247, 8
	v_cvt_f32_ubyte0_e32 v124, v40
	v_cvt_f32_ubyte1_e32 v125, v40
	v_cvt_f32_ubyte2_e32 v126, v40
	v_cvt_f32_ubyte3_e32 v127, v40
	v_cvt_f32_ubyte0_e32 v128, v41
	v_cvt_f32_ubyte1_e32 v129, v41
	v_cvt_f32_ubyte2_e32 v130, v41
	v_cvt_f32_ubyte3_e32 v131, v41
	s_lshl_b32 s30, s76, 12
	s_add_u32 s28, s26, s30
	s_addc_u32 s29, s27, 0
	global_load_dwordx2 v[40:41], v162, s[28:29]
	v_fmac_f32_e32 v178, s25, v124
	v_fmac_f32_e32 v179, s25, v125
	v_fmac_f32_e32 v180, s25, v126
	v_fmac_f32_e32 v181, s25, v127
	v_fmac_f32_e32 v182, s25, v128
	v_fmac_f32_e32 v183, s25, v129
	v_fmac_f32_e32 v184, s25, v130
	v_fmac_f32_e32 v185, s25, v131
	s_waitcnt vmcnt(35)
	v_readlane_b32 s25, v247, 9
	v_cvt_f32_ubyte0_e32 v132, v42
	v_cvt_f32_ubyte1_e32 v133, v42
	v_cvt_f32_ubyte2_e32 v134, v42
	v_cvt_f32_ubyte3_e32 v135, v42
	v_cvt_f32_ubyte0_e32 v136, v43
	v_cvt_f32_ubyte1_e32 v137, v43
	v_cvt_f32_ubyte2_e32 v138, v43
	v_cvt_f32_ubyte3_e32 v139, v43
	s_lshl_b32 s30, s77, 12
	s_add_u32 s28, s26, s30
	s_addc_u32 s29, s27, 0
	global_load_dwordx2 v[42:43], v162, s[28:29]
	v_fmac_f32_e32 v178, s25, v132
	v_fmac_f32_e32 v179, s25, v133
	v_fmac_f32_e32 v180, s25, v134
	v_fmac_f32_e32 v181, s25, v135
	v_fmac_f32_e32 v182, s25, v136
	v_fmac_f32_e32 v183, s25, v137
	v_fmac_f32_e32 v184, s25, v138
	v_fmac_f32_e32 v185, s25, v139
	s_waitcnt vmcnt(35)
	v_readlane_b32 s25, v247, 10
	v_cvt_f32_ubyte0_e32 v124, v44
	v_cvt_f32_ubyte1_e32 v125, v44
	v_cvt_f32_ubyte2_e32 v126, v44
	v_cvt_f32_ubyte3_e32 v127, v44
	v_cvt_f32_ubyte0_e32 v128, v45
	v_cvt_f32_ubyte1_e32 v129, v45
	v_cvt_f32_ubyte2_e32 v130, v45
	v_cvt_f32_ubyte3_e32 v131, v45
	s_lshl_b32 s30, s78, 12
	s_add_u32 s28, s26, s30
	s_addc_u32 s29, s27, 0
	global_load_dwordx2 v[44:45], v162, s[28:29]
	v_fmac_f32_e32 v178, s25, v124
	v_fmac_f32_e32 v179, s25, v125
	v_fmac_f32_e32 v180, s25, v126
	v_fmac_f32_e32 v181, s25, v127
	v_fmac_f32_e32 v182, s25, v128
	v_fmac_f32_e32 v183, s25, v129
	v_fmac_f32_e32 v184, s25, v130
	v_fmac_f32_e32 v185, s25, v131
	s_waitcnt vmcnt(35)
	v_readlane_b32 s25, v247, 11
	v_cvt_f32_ubyte0_e32 v132, v46
	v_cvt_f32_ubyte1_e32 v133, v46
	v_cvt_f32_ubyte2_e32 v134, v46
	v_cvt_f32_ubyte3_e32 v135, v46
	v_cvt_f32_ubyte0_e32 v136, v47
	v_cvt_f32_ubyte1_e32 v137, v47
	v_cvt_f32_ubyte2_e32 v138, v47
	v_cvt_f32_ubyte3_e32 v139, v47
	s_lshl_b32 s30, s79, 12
	s_add_u32 s28, s26, s30
	s_addc_u32 s29, s27, 0
	global_load_dwordx2 v[46:47], v162, s[28:29]
	v_fmac_f32_e32 v178, s25, v132
	v_fmac_f32_e32 v179, s25, v133
	v_fmac_f32_e32 v180, s25, v134
	v_fmac_f32_e32 v181, s25, v135
	v_fmac_f32_e32 v182, s25, v136
	v_fmac_f32_e32 v183, s25, v137
	v_fmac_f32_e32 v184, s25, v138
	v_fmac_f32_e32 v185, s25, v139
	s_waitcnt vmcnt(35)
	v_readlane_b32 s25, v247, 12
	v_cvt_f32_ubyte0_e32 v124, v48
	v_cvt_f32_ubyte1_e32 v125, v48
	v_cvt_f32_ubyte2_e32 v126, v48
	v_cvt_f32_ubyte3_e32 v127, v48
	v_cvt_f32_ubyte0_e32 v128, v49
	v_cvt_f32_ubyte1_e32 v129, v49
	v_cvt_f32_ubyte2_e32 v130, v49
	v_cvt_f32_ubyte3_e32 v131, v49
	s_lshl_b32 s30, s80, 12
	s_add_u32 s28, s26, s30
	s_addc_u32 s29, s27, 0
	global_load_dwordx2 v[48:49], v162, s[28:29]
	v_fmac_f32_e32 v178, s25, v124
	v_fmac_f32_e32 v179, s25, v125
	v_fmac_f32_e32 v180, s25, v126
	v_fmac_f32_e32 v181, s25, v127
	v_fmac_f32_e32 v182, s25, v128
	v_fmac_f32_e32 v183, s25, v129
	v_fmac_f32_e32 v184, s25, v130
	v_fmac_f32_e32 v185, s25, v131
	s_waitcnt vmcnt(35)
	v_readlane_b32 s25, v247, 13
	v_cvt_f32_ubyte0_e32 v132, v50
	v_cvt_f32_ubyte1_e32 v133, v50
	v_cvt_f32_ubyte2_e32 v134, v50
	v_cvt_f32_ubyte3_e32 v135, v50
	v_cvt_f32_ubyte0_e32 v136, v51
	v_cvt_f32_ubyte1_e32 v137, v51
	v_cvt_f32_ubyte2_e32 v138, v51
	v_cvt_f32_ubyte3_e32 v139, v51
	s_lshl_b32 s30, s81, 12
	s_add_u32 s28, s26, s30
	s_addc_u32 s29, s27, 0
	global_load_dwordx2 v[50:51], v162, s[28:29]
	v_fmac_f32_e32 v178, s25, v132
	v_fmac_f32_e32 v179, s25, v133
	v_fmac_f32_e32 v180, s25, v134
	v_fmac_f32_e32 v181, s25, v135
	v_fmac_f32_e32 v182, s25, v136
	v_fmac_f32_e32 v183, s25, v137
	v_fmac_f32_e32 v184, s25, v138
	v_fmac_f32_e32 v185, s25, v139
	s_waitcnt vmcnt(35)
	v_readlane_b32 s25, v247, 14
	v_cvt_f32_ubyte0_e32 v124, v52
	v_cvt_f32_ubyte1_e32 v125, v52
	v_cvt_f32_ubyte2_e32 v126, v52
	v_cvt_f32_ubyte3_e32 v127, v52
	v_cvt_f32_ubyte0_e32 v128, v53
	v_cvt_f32_ubyte1_e32 v129, v53
	v_cvt_f32_ubyte2_e32 v130, v53
	v_cvt_f32_ubyte3_e32 v131, v53
	s_lshl_b32 s30, s82, 12
	s_add_u32 s28, s26, s30
	s_addc_u32 s29, s27, 0
	global_load_dwordx2 v[52:53], v162, s[28:29]
	v_fmac_f32_e32 v178, s25, v124
	v_fmac_f32_e32 v179, s25, v125
	v_fmac_f32_e32 v180, s25, v126
	v_fmac_f32_e32 v181, s25, v127
	v_fmac_f32_e32 v182, s25, v128
	v_fmac_f32_e32 v183, s25, v129
	v_fmac_f32_e32 v184, s25, v130
	v_fmac_f32_e32 v185, s25, v131
	s_waitcnt vmcnt(35)
	v_readlane_b32 s25, v247, 15
	v_cvt_f32_ubyte0_e32 v132, v54
	v_cvt_f32_ubyte1_e32 v133, v54
	v_cvt_f32_ubyte2_e32 v134, v54
	v_cvt_f32_ubyte3_e32 v135, v54
	v_cvt_f32_ubyte0_e32 v136, v55
	v_cvt_f32_ubyte1_e32 v137, v55
	v_cvt_f32_ubyte2_e32 v138, v55
	v_cvt_f32_ubyte3_e32 v139, v55
	s_lshl_b32 s30, s83, 12
	s_add_u32 s28, s26, s30
	s_addc_u32 s29, s27, 0
	global_load_dwordx2 v[54:55], v162, s[28:29]
	v_fmac_f32_e32 v178, s25, v132
	v_fmac_f32_e32 v179, s25, v133
	v_fmac_f32_e32 v180, s25, v134
	v_fmac_f32_e32 v181, s25, v135
	v_fmac_f32_e32 v182, s25, v136
	v_fmac_f32_e32 v183, s25, v137
	v_fmac_f32_e32 v184, s25, v138
	v_fmac_f32_e32 v185, s25, v139
	s_waitcnt vmcnt(35)
	v_readlane_b32 s25, v247, 16
	v_cvt_f32_ubyte0_e32 v124, v56
	v_cvt_f32_ubyte1_e32 v125, v56
	v_cvt_f32_ubyte2_e32 v126, v56
	v_cvt_f32_ubyte3_e32 v127, v56
	v_cvt_f32_ubyte0_e32 v128, v57
	v_cvt_f32_ubyte1_e32 v129, v57
	v_cvt_f32_ubyte2_e32 v130, v57
	v_cvt_f32_ubyte3_e32 v131, v57
	s_waitcnt lgkmcnt(0)
	s_load_dwordx16 s[68:83], s[38:39], 0x0 glc
	s_lshl_b32 s30, s84, 12
	s_add_u32 s28, s26, s30
	s_addc_u32 s29, s27, 0
	global_load_dwordx2 v[56:57], v162, s[28:29]
	v_fmac_f32_e32 v178, s25, v124
	v_fmac_f32_e32 v179, s25, v125
	v_fmac_f32_e32 v180, s25, v126
	v_fmac_f32_e32 v181, s25, v127
	v_fmac_f32_e32 v182, s25, v128
	v_fmac_f32_e32 v183, s25, v129
	v_fmac_f32_e32 v184, s25, v130
	v_fmac_f32_e32 v185, s25, v131
	s_waitcnt vmcnt(35)
	v_readlane_b32 s25, v247, 17
	v_cvt_f32_ubyte0_e32 v132, v58
	v_cvt_f32_ubyte1_e32 v133, v58
	v_cvt_f32_ubyte2_e32 v134, v58
	v_cvt_f32_ubyte3_e32 v135, v58
	v_cvt_f32_ubyte0_e32 v136, v59
	v_cvt_f32_ubyte1_e32 v137, v59
	v_cvt_f32_ubyte2_e32 v138, v59
	v_cvt_f32_ubyte3_e32 v139, v59
	s_lshl_b32 s30, s85, 12
	s_add_u32 s28, s26, s30
	s_addc_u32 s29, s27, 0
	global_load_dwordx2 v[58:59], v162, s[28:29]
	v_fmac_f32_e32 v178, s25, v132
	v_fmac_f32_e32 v179, s25, v133
	v_fmac_f32_e32 v180, s25, v134
	v_fmac_f32_e32 v181, s25, v135
	v_fmac_f32_e32 v182, s25, v136
	v_fmac_f32_e32 v183, s25, v137
	v_fmac_f32_e32 v184, s25, v138
	v_fmac_f32_e32 v185, s25, v139
	s_waitcnt vmcnt(35)
	v_readlane_b32 s25, v247, 18
	v_cvt_f32_ubyte0_e32 v124, v60
	v_cvt_f32_ubyte1_e32 v125, v60
	v_cvt_f32_ubyte2_e32 v126, v60
	v_cvt_f32_ubyte3_e32 v127, v60
	v_cvt_f32_ubyte0_e32 v128, v61
	v_cvt_f32_ubyte1_e32 v129, v61
	v_cvt_f32_ubyte2_e32 v130, v61
	v_cvt_f32_ubyte3_e32 v131, v61
	s_lshl_b32 s30, s86, 12
	s_add_u32 s28, s26, s30
	s_addc_u32 s29, s27, 0
	global_load_dwordx2 v[60:61], v162, s[28:29]
	v_fmac_f32_e32 v178, s25, v124
	v_fmac_f32_e32 v179, s25, v125
	v_fmac_f32_e32 v180, s25, v126
	v_fmac_f32_e32 v181, s25, v127
	v_fmac_f32_e32 v182, s25, v128
	v_fmac_f32_e32 v183, s25, v129
	v_fmac_f32_e32 v184, s25, v130
	v_fmac_f32_e32 v185, s25, v131
	s_waitcnt vmcnt(35)
	v_readlane_b32 s25, v247, 19
	v_cvt_f32_ubyte0_e32 v132, v62
	v_cvt_f32_ubyte1_e32 v133, v62
	v_cvt_f32_ubyte2_e32 v134, v62
	v_cvt_f32_ubyte3_e32 v135, v62
	v_cvt_f32_ubyte0_e32 v136, v63
	v_cvt_f32_ubyte1_e32 v137, v63
	v_cvt_f32_ubyte2_e32 v138, v63
	v_cvt_f32_ubyte3_e32 v139, v63
	s_lshl_b32 s30, s87, 12
	s_add_u32 s28, s26, s30
	s_addc_u32 s29, s27, 0
	global_load_dwordx2 v[62:63], v162, s[28:29]
	v_fmac_f32_e32 v178, s25, v132
	v_fmac_f32_e32 v179, s25, v133
	v_fmac_f32_e32 v180, s25, v134
	v_fmac_f32_e32 v181, s25, v135
	v_fmac_f32_e32 v182, s25, v136
	v_fmac_f32_e32 v183, s25, v137
	v_fmac_f32_e32 v184, s25, v138
	v_fmac_f32_e32 v185, s25, v139
	s_waitcnt vmcnt(35)
	v_readlane_b32 s25, v247, 20
	v_cvt_f32_ubyte0_e32 v124, v64
	v_cvt_f32_ubyte1_e32 v125, v64
	v_cvt_f32_ubyte2_e32 v126, v64
	v_cvt_f32_ubyte3_e32 v127, v64
	v_cvt_f32_ubyte0_e32 v128, v65
	v_cvt_f32_ubyte1_e32 v129, v65
	v_cvt_f32_ubyte2_e32 v130, v65
	v_cvt_f32_ubyte3_e32 v131, v65
	s_lshl_b32 s30, s88, 12
	s_add_u32 s28, s26, s30
	s_addc_u32 s29, s27, 0
	global_load_dwordx2 v[64:65], v162, s[28:29]
	v_fmac_f32_e32 v178, s25, v124
	v_fmac_f32_e32 v179, s25, v125
	v_fmac_f32_e32 v180, s25, v126
	v_fmac_f32_e32 v181, s25, v127
	v_fmac_f32_e32 v182, s25, v128
	v_fmac_f32_e32 v183, s25, v129
	v_fmac_f32_e32 v184, s25, v130
	v_fmac_f32_e32 v185, s25, v131
	s_waitcnt vmcnt(35)
	v_readlane_b32 s25, v247, 21
	v_cvt_f32_ubyte0_e32 v132, v66
	v_cvt_f32_ubyte1_e32 v133, v66
	v_cvt_f32_ubyte2_e32 v134, v66
	v_cvt_f32_ubyte3_e32 v135, v66
	v_cvt_f32_ubyte0_e32 v136, v67
	v_cvt_f32_ubyte1_e32 v137, v67
	v_cvt_f32_ubyte2_e32 v138, v67
	v_cvt_f32_ubyte3_e32 v139, v67
	s_lshl_b32 s30, s89, 12
	s_add_u32 s28, s26, s30
	s_addc_u32 s29, s27, 0
	global_load_dwordx2 v[66:67], v162, s[28:29]
	v_fmac_f32_e32 v178, s25, v132
	v_fmac_f32_e32 v179, s25, v133
	v_fmac_f32_e32 v180, s25, v134
	v_fmac_f32_e32 v181, s25, v135
	v_fmac_f32_e32 v182, s25, v136
	v_fmac_f32_e32 v183, s25, v137
	v_fmac_f32_e32 v184, s25, v138
	v_fmac_f32_e32 v185, s25, v139
	s_waitcnt vmcnt(35)
	v_readlane_b32 s25, v247, 22
	v_cvt_f32_ubyte0_e32 v124, v68
	v_cvt_f32_ubyte1_e32 v125, v68
	v_cvt_f32_ubyte2_e32 v126, v68
	v_cvt_f32_ubyte3_e32 v127, v68
	v_cvt_f32_ubyte0_e32 v128, v69
	v_cvt_f32_ubyte1_e32 v129, v69
	v_cvt_f32_ubyte2_e32 v130, v69
	v_cvt_f32_ubyte3_e32 v131, v69
	s_lshl_b32 s30, s90, 12
	s_add_u32 s28, s26, s30
	s_addc_u32 s29, s27, 0
	global_load_dwordx2 v[68:69], v162, s[28:29]
	v_fmac_f32_e32 v178, s25, v124
	v_fmac_f32_e32 v179, s25, v125
	v_fmac_f32_e32 v180, s25, v126
	v_fmac_f32_e32 v181, s25, v127
	v_fmac_f32_e32 v182, s25, v128
	v_fmac_f32_e32 v183, s25, v129
	v_fmac_f32_e32 v184, s25, v130
	v_fmac_f32_e32 v185, s25, v131
	s_waitcnt vmcnt(35)
	v_readlane_b32 s25, v247, 23
	v_cvt_f32_ubyte0_e32 v132, v70
	v_cvt_f32_ubyte1_e32 v133, v70
	v_cvt_f32_ubyte2_e32 v134, v70
	v_cvt_f32_ubyte3_e32 v135, v70
	v_cvt_f32_ubyte0_e32 v136, v71
	v_cvt_f32_ubyte1_e32 v137, v71
	v_cvt_f32_ubyte2_e32 v138, v71
	v_cvt_f32_ubyte3_e32 v139, v71
	s_lshl_b32 s30, s91, 12
	s_add_u32 s28, s26, s30
	s_addc_u32 s29, s27, 0
	global_load_dwordx2 v[70:71], v162, s[28:29]
	v_fmac_f32_e32 v178, s25, v132
	v_fmac_f32_e32 v179, s25, v133
	v_fmac_f32_e32 v180, s25, v134
	v_fmac_f32_e32 v181, s25, v135
	v_fmac_f32_e32 v182, s25, v136
	v_fmac_f32_e32 v183, s25, v137
	v_fmac_f32_e32 v184, s25, v138
	v_fmac_f32_e32 v185, s25, v139
	s_waitcnt vmcnt(35)
	v_readlane_b32 s25, v247, 24
	v_cvt_f32_ubyte0_e32 v124, v72
	v_cvt_f32_ubyte1_e32 v125, v72
	v_cvt_f32_ubyte2_e32 v126, v72
	v_cvt_f32_ubyte3_e32 v127, v72
	v_cvt_f32_ubyte0_e32 v128, v73
	v_cvt_f32_ubyte1_e32 v129, v73
	v_cvt_f32_ubyte2_e32 v130, v73
	v_cvt_f32_ubyte3_e32 v131, v73
	s_lshl_b32 s30, s92, 12
	s_add_u32 s28, s26, s30
	s_addc_u32 s29, s27, 0
	global_load_dwordx2 v[72:73], v162, s[28:29]
	v_fmac_f32_e32 v178, s25, v124
	v_fmac_f32_e32 v179, s25, v125
	v_fmac_f32_e32 v180, s25, v126
	v_fmac_f32_e32 v181, s25, v127
	v_fmac_f32_e32 v182, s25, v128
	v_fmac_f32_e32 v183, s25, v129
	v_fmac_f32_e32 v184, s25, v130
	v_fmac_f32_e32 v185, s25, v131
	s_waitcnt vmcnt(35)
	v_readlane_b32 s25, v247, 25
	v_cvt_f32_ubyte0_e32 v132, v74
	v_cvt_f32_ubyte1_e32 v133, v74
	v_cvt_f32_ubyte2_e32 v134, v74
	v_cvt_f32_ubyte3_e32 v135, v74
	v_cvt_f32_ubyte0_e32 v136, v75
	v_cvt_f32_ubyte1_e32 v137, v75
	v_cvt_f32_ubyte2_e32 v138, v75
	v_cvt_f32_ubyte3_e32 v139, v75
	s_lshl_b32 s30, s93, 12
	s_add_u32 s28, s26, s30
	s_addc_u32 s29, s27, 0
	global_load_dwordx2 v[74:75], v162, s[28:29]
	v_fmac_f32_e32 v178, s25, v132
	v_fmac_f32_e32 v179, s25, v133
	v_fmac_f32_e32 v180, s25, v134
	v_fmac_f32_e32 v181, s25, v135
	v_fmac_f32_e32 v182, s25, v136
	v_fmac_f32_e32 v183, s25, v137
	v_fmac_f32_e32 v184, s25, v138
	v_fmac_f32_e32 v185, s25, v139
	s_waitcnt vmcnt(35)
	v_readlane_b32 s25, v247, 26
	v_cvt_f32_ubyte0_e32 v124, v76
	v_cvt_f32_ubyte1_e32 v125, v76
	v_cvt_f32_ubyte2_e32 v126, v76
	v_cvt_f32_ubyte3_e32 v127, v76
	v_cvt_f32_ubyte0_e32 v128, v77
	v_cvt_f32_ubyte1_e32 v129, v77
	v_cvt_f32_ubyte2_e32 v130, v77
	v_cvt_f32_ubyte3_e32 v131, v77
	s_lshl_b32 s30, s94, 12
	s_add_u32 s28, s26, s30
	s_addc_u32 s29, s27, 0
	global_load_dwordx2 v[76:77], v162, s[28:29]
	v_fmac_f32_e32 v178, s25, v124
	v_fmac_f32_e32 v179, s25, v125
	v_fmac_f32_e32 v180, s25, v126
	v_fmac_f32_e32 v181, s25, v127
	v_fmac_f32_e32 v182, s25, v128
	v_fmac_f32_e32 v183, s25, v129
	v_fmac_f32_e32 v184, s25, v130
	v_fmac_f32_e32 v185, s25, v131
	s_waitcnt vmcnt(35)
	v_readlane_b32 s25, v247, 27
	v_cvt_f32_ubyte0_e32 v132, v78
	v_cvt_f32_ubyte1_e32 v133, v78
	v_cvt_f32_ubyte2_e32 v134, v78
	v_cvt_f32_ubyte3_e32 v135, v78
	v_cvt_f32_ubyte0_e32 v136, v79
	v_cvt_f32_ubyte1_e32 v137, v79
	v_cvt_f32_ubyte2_e32 v138, v79
	v_cvt_f32_ubyte3_e32 v139, v79
	s_lshl_b32 s30, s95, 12
	s_add_u32 s28, s26, s30
	s_addc_u32 s29, s27, 0
	global_load_dwordx2 v[78:79], v162, s[28:29]
	v_fmac_f32_e32 v178, s25, v132
	v_fmac_f32_e32 v179, s25, v133
	v_fmac_f32_e32 v180, s25, v134
	v_fmac_f32_e32 v181, s25, v135
	v_fmac_f32_e32 v182, s25, v136
	v_fmac_f32_e32 v183, s25, v137
	v_fmac_f32_e32 v184, s25, v138
	v_fmac_f32_e32 v185, s25, v139
	s_waitcnt vmcnt(35)
	v_readlane_b32 s25, v247, 28
	v_cvt_f32_ubyte0_e32 v124, v80
	v_cvt_f32_ubyte1_e32 v125, v80
	v_cvt_f32_ubyte2_e32 v126, v80
	v_cvt_f32_ubyte3_e32 v127, v80
	v_cvt_f32_ubyte0_e32 v128, v81
	v_cvt_f32_ubyte1_e32 v129, v81
	v_cvt_f32_ubyte2_e32 v130, v81
	v_cvt_f32_ubyte3_e32 v131, v81
	s_lshl_b32 s30, s96, 12
	s_add_u32 s28, s26, s30
	s_addc_u32 s29, s27, 0
	global_load_dwordx2 v[80:81], v162, s[28:29]
	v_fmac_f32_e32 v178, s25, v124
	v_fmac_f32_e32 v179, s25, v125
	v_fmac_f32_e32 v180, s25, v126
	v_fmac_f32_e32 v181, s25, v127
	v_fmac_f32_e32 v182, s25, v128
	v_fmac_f32_e32 v183, s25, v129
	v_fmac_f32_e32 v184, s25, v130
	v_fmac_f32_e32 v185, s25, v131
	s_waitcnt vmcnt(35)
	v_readlane_b32 s25, v247, 29
	v_cvt_f32_ubyte0_e32 v132, v82
	v_cvt_f32_ubyte1_e32 v133, v82
	v_cvt_f32_ubyte2_e32 v134, v82
	v_cvt_f32_ubyte3_e32 v135, v82
	v_cvt_f32_ubyte0_e32 v136, v83
	v_cvt_f32_ubyte1_e32 v137, v83
	v_cvt_f32_ubyte2_e32 v138, v83
	v_cvt_f32_ubyte3_e32 v139, v83
	s_lshl_b32 s30, s97, 12
	s_add_u32 s28, s26, s30
	s_addc_u32 s29, s27, 0
	global_load_dwordx2 v[82:83], v162, s[28:29]
	v_fmac_f32_e32 v178, s25, v132
	v_fmac_f32_e32 v179, s25, v133
	v_fmac_f32_e32 v180, s25, v134
	v_fmac_f32_e32 v181, s25, v135
	v_fmac_f32_e32 v182, s25, v136
	v_fmac_f32_e32 v183, s25, v137
	v_fmac_f32_e32 v184, s25, v138
	v_fmac_f32_e32 v185, s25, v139
	s_waitcnt vmcnt(35)
	v_readlane_b32 s25, v247, 30
	v_cvt_f32_ubyte0_e32 v124, v84
	v_cvt_f32_ubyte1_e32 v125, v84
	v_cvt_f32_ubyte2_e32 v126, v84
	v_cvt_f32_ubyte3_e32 v127, v84
	v_cvt_f32_ubyte0_e32 v128, v85
	v_cvt_f32_ubyte1_e32 v129, v85
	v_cvt_f32_ubyte2_e32 v130, v85
	v_cvt_f32_ubyte3_e32 v131, v85
	s_lshl_b32 s30, s98, 12
	s_add_u32 s28, s26, s30
	s_addc_u32 s29, s27, 0
	global_load_dwordx2 v[84:85], v162, s[28:29]
	v_fmac_f32_e32 v178, s25, v124
	v_fmac_f32_e32 v179, s25, v125
	v_fmac_f32_e32 v180, s25, v126
	v_fmac_f32_e32 v181, s25, v127
	v_fmac_f32_e32 v182, s25, v128
	v_fmac_f32_e32 v183, s25, v129
	v_fmac_f32_e32 v184, s25, v130
	v_fmac_f32_e32 v185, s25, v131
	s_waitcnt vmcnt(35)
	v_readlane_b32 s25, v247, 31
	v_cvt_f32_ubyte0_e32 v132, v86
	v_cvt_f32_ubyte1_e32 v133, v86
	v_cvt_f32_ubyte2_e32 v134, v86
	v_cvt_f32_ubyte3_e32 v135, v86
	v_cvt_f32_ubyte0_e32 v136, v87
	v_cvt_f32_ubyte1_e32 v137, v87
	v_cvt_f32_ubyte2_e32 v138, v87
	v_cvt_f32_ubyte3_e32 v139, v87
	s_lshl_b32 s30, s99, 12
	s_add_u32 s28, s26, s30
	s_addc_u32 s29, s27, 0
	global_load_dwordx2 v[86:87], v162, s[28:29]
	v_fmac_f32_e32 v178, s25, v132
	v_fmac_f32_e32 v179, s25, v133
	v_fmac_f32_e32 v180, s25, v134
	v_fmac_f32_e32 v181, s25, v135
	v_fmac_f32_e32 v182, s25, v136
	v_fmac_f32_e32 v183, s25, v137
	v_fmac_f32_e32 v184, s25, v138
	v_fmac_f32_e32 v185, s25, v139
	s_waitcnt vmcnt(35)
	v_readlane_b32 s25, v247, 32
	v_cvt_f32_ubyte0_e32 v124, v24
	v_cvt_f32_ubyte1_e32 v125, v24
	v_cvt_f32_ubyte2_e32 v126, v24
	v_cvt_f32_ubyte3_e32 v127, v24
	v_cvt_f32_ubyte0_e32 v128, v25
	v_cvt_f32_ubyte1_e32 v129, v25
	v_cvt_f32_ubyte2_e32 v130, v25
	v_cvt_f32_ubyte3_e32 v131, v25
	v_fmac_f32_e32 v178, s25, v124
	v_fmac_f32_e32 v179, s25, v125
	v_fmac_f32_e32 v180, s25, v126
	v_fmac_f32_e32 v181, s25, v127
	v_fmac_f32_e32 v182, s25, v128
	v_fmac_f32_e32 v183, s25, v129
	v_fmac_f32_e32 v184, s25, v130
	v_fmac_f32_e32 v185, s25, v131
	s_waitcnt vmcnt(30)
	v_readlane_b32 s25, v247, 33
	v_cvt_f32_ubyte0_e32 v132, v26
	v_cvt_f32_ubyte1_e32 v133, v26
	v_cvt_f32_ubyte2_e32 v134, v26
	v_cvt_f32_ubyte3_e32 v135, v26
	v_cvt_f32_ubyte0_e32 v136, v27
	v_cvt_f32_ubyte1_e32 v137, v27
	v_cvt_f32_ubyte2_e32 v138, v27
	v_cvt_f32_ubyte3_e32 v139, v27
	v_fmac_f32_e32 v178, s25, v132
	v_fmac_f32_e32 v179, s25, v133
	v_fmac_f32_e32 v180, s25, v134
	v_fmac_f32_e32 v181, s25, v135
	v_fmac_f32_e32 v182, s25, v136
	v_fmac_f32_e32 v183, s25, v137
	v_fmac_f32_e32 v184, s25, v138
	v_fmac_f32_e32 v185, s25, v139
	s_waitcnt vmcnt(29)
	v_readlane_b32 s25, v247, 34
	v_cvt_f32_ubyte0_e32 v124, v28
	v_cvt_f32_ubyte1_e32 v125, v28
	v_cvt_f32_ubyte2_e32 v126, v28
	v_cvt_f32_ubyte3_e32 v127, v28
	v_cvt_f32_ubyte0_e32 v128, v29
	v_cvt_f32_ubyte1_e32 v129, v29
	v_cvt_f32_ubyte2_e32 v130, v29
	v_cvt_f32_ubyte3_e32 v131, v29
	v_fmac_f32_e32 v178, s25, v124
	v_fmac_f32_e32 v179, s25, v125
	v_fmac_f32_e32 v180, s25, v126
	v_fmac_f32_e32 v181, s25, v127
	v_fmac_f32_e32 v182, s25, v128
	v_fmac_f32_e32 v183, s25, v129
	v_fmac_f32_e32 v184, s25, v130
	v_fmac_f32_e32 v185, s25, v131
	s_waitcnt vmcnt(28)
	v_readlane_b32 s25, v247, 35
	v_cvt_f32_ubyte0_e32 v132, v30
	v_cvt_f32_ubyte1_e32 v133, v30
	v_cvt_f32_ubyte2_e32 v134, v30
	v_cvt_f32_ubyte3_e32 v135, v30
	v_cvt_f32_ubyte0_e32 v136, v31
	v_cvt_f32_ubyte1_e32 v137, v31
	v_cvt_f32_ubyte2_e32 v138, v31
	v_cvt_f32_ubyte3_e32 v139, v31
	v_fmac_f32_e32 v178, s25, v132
	v_fmac_f32_e32 v179, s25, v133
	v_fmac_f32_e32 v180, s25, v134
	v_fmac_f32_e32 v181, s25, v135
	v_fmac_f32_e32 v182, s25, v136
	v_fmac_f32_e32 v183, s25, v137
	v_fmac_f32_e32 v184, s25, v138
	v_fmac_f32_e32 v185, s25, v139
	s_waitcnt vmcnt(27)
	v_readlane_b32 s25, v247, 36
	v_cvt_f32_ubyte0_e32 v124, v32
	v_cvt_f32_ubyte1_e32 v125, v32
	v_cvt_f32_ubyte2_e32 v126, v32
	v_cvt_f32_ubyte3_e32 v127, v32
	v_cvt_f32_ubyte0_e32 v128, v33
	v_cvt_f32_ubyte1_e32 v129, v33
	v_cvt_f32_ubyte2_e32 v130, v33
	v_cvt_f32_ubyte3_e32 v131, v33
	v_fmac_f32_e32 v178, s25, v124
	v_fmac_f32_e32 v179, s25, v125
	v_fmac_f32_e32 v180, s25, v126
	v_fmac_f32_e32 v181, s25, v127
	v_fmac_f32_e32 v182, s25, v128
	v_fmac_f32_e32 v183, s25, v129
	v_fmac_f32_e32 v184, s25, v130
	v_fmac_f32_e32 v185, s25, v131
	s_waitcnt vmcnt(26)
	v_readlane_b32 s25, v247, 37
	v_cvt_f32_ubyte0_e32 v132, v34
	v_cvt_f32_ubyte1_e32 v133, v34
	v_cvt_f32_ubyte2_e32 v134, v34
	v_cvt_f32_ubyte3_e32 v135, v34
	v_cvt_f32_ubyte0_e32 v136, v35
	v_cvt_f32_ubyte1_e32 v137, v35
	v_cvt_f32_ubyte2_e32 v138, v35
	v_cvt_f32_ubyte3_e32 v139, v35
	v_fmac_f32_e32 v178, s25, v132
	v_fmac_f32_e32 v179, s25, v133
	v_fmac_f32_e32 v180, s25, v134
	v_fmac_f32_e32 v181, s25, v135
	v_fmac_f32_e32 v182, s25, v136
	v_fmac_f32_e32 v183, s25, v137
	v_fmac_f32_e32 v184, s25, v138
	v_fmac_f32_e32 v185, s25, v139
	s_waitcnt vmcnt(25)
	v_readlane_b32 s25, v247, 38
	v_cvt_f32_ubyte0_e32 v124, v36
	v_cvt_f32_ubyte1_e32 v125, v36
	v_cvt_f32_ubyte2_e32 v126, v36
	v_cvt_f32_ubyte3_e32 v127, v36
	v_cvt_f32_ubyte0_e32 v128, v37
	v_cvt_f32_ubyte1_e32 v129, v37
	v_cvt_f32_ubyte2_e32 v130, v37
	v_cvt_f32_ubyte3_e32 v131, v37
	v_fmac_f32_e32 v178, s25, v124
	v_fmac_f32_e32 v179, s25, v125
	v_fmac_f32_e32 v180, s25, v126
	v_fmac_f32_e32 v181, s25, v127
	v_fmac_f32_e32 v182, s25, v128
	v_fmac_f32_e32 v183, s25, v129
	v_fmac_f32_e32 v184, s25, v130
	v_fmac_f32_e32 v185, s25, v131
	s_waitcnt vmcnt(24)
	v_readlane_b32 s25, v247, 39
	v_cvt_f32_ubyte0_e32 v132, v38
	v_cvt_f32_ubyte1_e32 v133, v38
	v_cvt_f32_ubyte2_e32 v134, v38
	v_cvt_f32_ubyte3_e32 v135, v38
	v_cvt_f32_ubyte0_e32 v136, v39
	v_cvt_f32_ubyte1_e32 v137, v39
	v_cvt_f32_ubyte2_e32 v138, v39
	v_cvt_f32_ubyte3_e32 v139, v39
	v_fmac_f32_e32 v178, s25, v132
	v_fmac_f32_e32 v179, s25, v133
	v_fmac_f32_e32 v180, s25, v134
	v_fmac_f32_e32 v181, s25, v135
	v_fmac_f32_e32 v182, s25, v136
	v_fmac_f32_e32 v183, s25, v137
	v_fmac_f32_e32 v184, s25, v138
	v_fmac_f32_e32 v185, s25, v139
	s_waitcnt vmcnt(23)
	v_readlane_b32 s25, v247, 40
	v_cvt_f32_ubyte0_e32 v124, v40
	v_cvt_f32_ubyte1_e32 v125, v40
	v_cvt_f32_ubyte2_e32 v126, v40
	v_cvt_f32_ubyte3_e32 v127, v40
	v_cvt_f32_ubyte0_e32 v128, v41
	v_cvt_f32_ubyte1_e32 v129, v41
	v_cvt_f32_ubyte2_e32 v130, v41
	v_cvt_f32_ubyte3_e32 v131, v41
	v_fmac_f32_e32 v178, s25, v124
	v_fmac_f32_e32 v179, s25, v125
	v_fmac_f32_e32 v180, s25, v126
	v_fmac_f32_e32 v181, s25, v127
	v_fmac_f32_e32 v182, s25, v128
	v_fmac_f32_e32 v183, s25, v129
	v_fmac_f32_e32 v184, s25, v130
	v_fmac_f32_e32 v185, s25, v131
	s_waitcnt vmcnt(22)
	v_readlane_b32 s25, v247, 41
	v_cvt_f32_ubyte0_e32 v132, v42
	v_cvt_f32_ubyte1_e32 v133, v42
	v_cvt_f32_ubyte2_e32 v134, v42
	v_cvt_f32_ubyte3_e32 v135, v42
	v_cvt_f32_ubyte0_e32 v136, v43
	v_cvt_f32_ubyte1_e32 v137, v43
	v_cvt_f32_ubyte2_e32 v138, v43
	v_cvt_f32_ubyte3_e32 v139, v43
	v_fmac_f32_e32 v178, s25, v132
	v_fmac_f32_e32 v179, s25, v133
	v_fmac_f32_e32 v180, s25, v134
	v_fmac_f32_e32 v181, s25, v135
	v_fmac_f32_e32 v182, s25, v136
	v_fmac_f32_e32 v183, s25, v137
	v_fmac_f32_e32 v184, s25, v138
	v_fmac_f32_e32 v185, s25, v139
	s_waitcnt vmcnt(21)
	v_readlane_b32 s25, v247, 42
	v_cvt_f32_ubyte0_e32 v124, v44
	v_cvt_f32_ubyte1_e32 v125, v44
	v_cvt_f32_ubyte2_e32 v126, v44
	v_cvt_f32_ubyte3_e32 v127, v44
	v_cvt_f32_ubyte0_e32 v128, v45
	v_cvt_f32_ubyte1_e32 v129, v45
	v_cvt_f32_ubyte2_e32 v130, v45
	v_cvt_f32_ubyte3_e32 v131, v45
	v_fmac_f32_e32 v178, s25, v124
	v_fmac_f32_e32 v179, s25, v125
	v_fmac_f32_e32 v180, s25, v126
	v_fmac_f32_e32 v181, s25, v127
	v_fmac_f32_e32 v182, s25, v128
	v_fmac_f32_e32 v183, s25, v129
	v_fmac_f32_e32 v184, s25, v130
	v_fmac_f32_e32 v185, s25, v131
	s_waitcnt vmcnt(20)
	v_readlane_b32 s25, v247, 43
	v_cvt_f32_ubyte0_e32 v132, v46
	v_cvt_f32_ubyte1_e32 v133, v46
	v_cvt_f32_ubyte2_e32 v134, v46
	v_cvt_f32_ubyte3_e32 v135, v46
	v_cvt_f32_ubyte0_e32 v136, v47
	v_cvt_f32_ubyte1_e32 v137, v47
	v_cvt_f32_ubyte2_e32 v138, v47
	v_cvt_f32_ubyte3_e32 v139, v47
	v_fmac_f32_e32 v178, s25, v132
	v_fmac_f32_e32 v179, s25, v133
	v_fmac_f32_e32 v180, s25, v134
	v_fmac_f32_e32 v181, s25, v135
	v_fmac_f32_e32 v182, s25, v136
	v_fmac_f32_e32 v183, s25, v137
	v_fmac_f32_e32 v184, s25, v138
	v_fmac_f32_e32 v185, s25, v139
	s_waitcnt vmcnt(19)
	v_readlane_b32 s25, v247, 44
	v_cvt_f32_ubyte0_e32 v124, v48
	v_cvt_f32_ubyte1_e32 v125, v48
	v_cvt_f32_ubyte2_e32 v126, v48
	v_cvt_f32_ubyte3_e32 v127, v48
	v_cvt_f32_ubyte0_e32 v128, v49
	v_cvt_f32_ubyte1_e32 v129, v49
	v_cvt_f32_ubyte2_e32 v130, v49
	v_cvt_f32_ubyte3_e32 v131, v49
	v_fmac_f32_e32 v178, s25, v124
	v_fmac_f32_e32 v179, s25, v125
	v_fmac_f32_e32 v180, s25, v126
	v_fmac_f32_e32 v181, s25, v127
	v_fmac_f32_e32 v182, s25, v128
	v_fmac_f32_e32 v183, s25, v129
	v_fmac_f32_e32 v184, s25, v130
	v_fmac_f32_e32 v185, s25, v131
	s_waitcnt vmcnt(18)
	v_readlane_b32 s25, v247, 45
	v_cvt_f32_ubyte0_e32 v132, v50
	v_cvt_f32_ubyte1_e32 v133, v50
	v_cvt_f32_ubyte2_e32 v134, v50
	v_cvt_f32_ubyte3_e32 v135, v50
	v_cvt_f32_ubyte0_e32 v136, v51
	v_cvt_f32_ubyte1_e32 v137, v51
	v_cvt_f32_ubyte2_e32 v138, v51
	v_cvt_f32_ubyte3_e32 v139, v51
	v_fmac_f32_e32 v178, s25, v132
	v_fmac_f32_e32 v179, s25, v133
	v_fmac_f32_e32 v180, s25, v134
	v_fmac_f32_e32 v181, s25, v135
	v_fmac_f32_e32 v182, s25, v136
	v_fmac_f32_e32 v183, s25, v137
	v_fmac_f32_e32 v184, s25, v138
	v_fmac_f32_e32 v185, s25, v139
	s_waitcnt vmcnt(17)
	v_readlane_b32 s25, v247, 46
	v_cvt_f32_ubyte0_e32 v124, v52
	v_cvt_f32_ubyte1_e32 v125, v52
	v_cvt_f32_ubyte2_e32 v126, v52
	v_cvt_f32_ubyte3_e32 v127, v52
	v_cvt_f32_ubyte0_e32 v128, v53
	v_cvt_f32_ubyte1_e32 v129, v53
	v_cvt_f32_ubyte2_e32 v130, v53
	v_cvt_f32_ubyte3_e32 v131, v53
	v_fmac_f32_e32 v178, s25, v124
	v_fmac_f32_e32 v179, s25, v125
	v_fmac_f32_e32 v180, s25, v126
	v_fmac_f32_e32 v181, s25, v127
	v_fmac_f32_e32 v182, s25, v128
	v_fmac_f32_e32 v183, s25, v129
	v_fmac_f32_e32 v184, s25, v130
	v_fmac_f32_e32 v185, s25, v131
	s_waitcnt vmcnt(16)
	v_readlane_b32 s25, v247, 47
	v_cvt_f32_ubyte0_e32 v132, v54
	v_cvt_f32_ubyte1_e32 v133, v54
	v_cvt_f32_ubyte2_e32 v134, v54
	v_cvt_f32_ubyte3_e32 v135, v54
	v_cvt_f32_ubyte0_e32 v136, v55
	v_cvt_f32_ubyte1_e32 v137, v55
	v_cvt_f32_ubyte2_e32 v138, v55
	v_cvt_f32_ubyte3_e32 v139, v55
	v_fmac_f32_e32 v178, s25, v132
	v_fmac_f32_e32 v179, s25, v133
	v_fmac_f32_e32 v180, s25, v134
	v_fmac_f32_e32 v181, s25, v135
	v_fmac_f32_e32 v182, s25, v136
	v_fmac_f32_e32 v183, s25, v137
	v_fmac_f32_e32 v184, s25, v138
	v_fmac_f32_e32 v185, s25, v139
	s_waitcnt vmcnt(15)
	v_readlane_b32 s25, v247, 48
	v_cvt_f32_ubyte0_e32 v124, v56
	v_cvt_f32_ubyte1_e32 v125, v56
	v_cvt_f32_ubyte2_e32 v126, v56
	v_cvt_f32_ubyte3_e32 v127, v56
	v_cvt_f32_ubyte0_e32 v128, v57
	v_cvt_f32_ubyte1_e32 v129, v57
	v_cvt_f32_ubyte2_e32 v130, v57
	v_cvt_f32_ubyte3_e32 v131, v57
	v_fmac_f32_e32 v178, s25, v124
	v_fmac_f32_e32 v179, s25, v125
	v_fmac_f32_e32 v180, s25, v126
	v_fmac_f32_e32 v181, s25, v127
	v_fmac_f32_e32 v182, s25, v128
	v_fmac_f32_e32 v183, s25, v129
	v_fmac_f32_e32 v184, s25, v130
	v_fmac_f32_e32 v185, s25, v131
	s_waitcnt vmcnt(14)
	v_readlane_b32 s25, v247, 49
	v_cvt_f32_ubyte0_e32 v132, v58
	v_cvt_f32_ubyte1_e32 v133, v58
	v_cvt_f32_ubyte2_e32 v134, v58
	v_cvt_f32_ubyte3_e32 v135, v58
	v_cvt_f32_ubyte0_e32 v136, v59
	v_cvt_f32_ubyte1_e32 v137, v59
	v_cvt_f32_ubyte2_e32 v138, v59
	v_cvt_f32_ubyte3_e32 v139, v59
	v_fmac_f32_e32 v178, s25, v132
	v_fmac_f32_e32 v179, s25, v133
	v_fmac_f32_e32 v180, s25, v134
	v_fmac_f32_e32 v181, s25, v135
	v_fmac_f32_e32 v182, s25, v136
	v_fmac_f32_e32 v183, s25, v137
	v_fmac_f32_e32 v184, s25, v138
	v_fmac_f32_e32 v185, s25, v139
	s_waitcnt vmcnt(13)
	v_readlane_b32 s25, v247, 50
	v_cvt_f32_ubyte0_e32 v124, v60
	v_cvt_f32_ubyte1_e32 v125, v60
	v_cvt_f32_ubyte2_e32 v126, v60
	v_cvt_f32_ubyte3_e32 v127, v60
	v_cvt_f32_ubyte0_e32 v128, v61
	v_cvt_f32_ubyte1_e32 v129, v61
	v_cvt_f32_ubyte2_e32 v130, v61
	v_cvt_f32_ubyte3_e32 v131, v61
	v_fmac_f32_e32 v178, s25, v124
	v_fmac_f32_e32 v179, s25, v125
	v_fmac_f32_e32 v180, s25, v126
	v_fmac_f32_e32 v181, s25, v127
	v_fmac_f32_e32 v182, s25, v128
	v_fmac_f32_e32 v183, s25, v129
	v_fmac_f32_e32 v184, s25, v130
	v_fmac_f32_e32 v185, s25, v131
	s_waitcnt vmcnt(12)
	v_readlane_b32 s25, v247, 51
	v_cvt_f32_ubyte0_e32 v132, v62
	v_cvt_f32_ubyte1_e32 v133, v62
	v_cvt_f32_ubyte2_e32 v134, v62
	v_cvt_f32_ubyte3_e32 v135, v62
	v_cvt_f32_ubyte0_e32 v136, v63
	v_cvt_f32_ubyte1_e32 v137, v63
	v_cvt_f32_ubyte2_e32 v138, v63
	v_cvt_f32_ubyte3_e32 v139, v63
	v_fmac_f32_e32 v178, s25, v132
	v_fmac_f32_e32 v179, s25, v133
	v_fmac_f32_e32 v180, s25, v134
	v_fmac_f32_e32 v181, s25, v135
	v_fmac_f32_e32 v182, s25, v136
	v_fmac_f32_e32 v183, s25, v137
	v_fmac_f32_e32 v184, s25, v138
	v_fmac_f32_e32 v185, s25, v139
	s_waitcnt vmcnt(11)
	v_readlane_b32 s25, v247, 52
	v_cvt_f32_ubyte0_e32 v124, v64
	v_cvt_f32_ubyte1_e32 v125, v64
	v_cvt_f32_ubyte2_e32 v126, v64
	v_cvt_f32_ubyte3_e32 v127, v64
	v_cvt_f32_ubyte0_e32 v128, v65
	v_cvt_f32_ubyte1_e32 v129, v65
	v_cvt_f32_ubyte2_e32 v130, v65
	v_cvt_f32_ubyte3_e32 v131, v65
	v_fmac_f32_e32 v178, s25, v124
	v_fmac_f32_e32 v179, s25, v125
	v_fmac_f32_e32 v180, s25, v126
	v_fmac_f32_e32 v181, s25, v127
	v_fmac_f32_e32 v182, s25, v128
	v_fmac_f32_e32 v183, s25, v129
	v_fmac_f32_e32 v184, s25, v130
	v_fmac_f32_e32 v185, s25, v131
	s_waitcnt vmcnt(10)
	v_readlane_b32 s25, v247, 53
	v_cvt_f32_ubyte0_e32 v132, v66
	v_cvt_f32_ubyte1_e32 v133, v66
	v_cvt_f32_ubyte2_e32 v134, v66
	v_cvt_f32_ubyte3_e32 v135, v66
	v_cvt_f32_ubyte0_e32 v136, v67
	v_cvt_f32_ubyte1_e32 v137, v67
	v_cvt_f32_ubyte2_e32 v138, v67
	v_cvt_f32_ubyte3_e32 v139, v67
	v_fmac_f32_e32 v178, s25, v132
	v_fmac_f32_e32 v179, s25, v133
	v_fmac_f32_e32 v180, s25, v134
	v_fmac_f32_e32 v181, s25, v135
	v_fmac_f32_e32 v182, s25, v136
	v_fmac_f32_e32 v183, s25, v137
	v_fmac_f32_e32 v184, s25, v138
	v_fmac_f32_e32 v185, s25, v139
	s_waitcnt vmcnt(9)
	v_readlane_b32 s25, v247, 54
	v_cvt_f32_ubyte0_e32 v124, v68
	v_cvt_f32_ubyte1_e32 v125, v68
	v_cvt_f32_ubyte2_e32 v126, v68
	v_cvt_f32_ubyte3_e32 v127, v68
	v_cvt_f32_ubyte0_e32 v128, v69
	v_cvt_f32_ubyte1_e32 v129, v69
	v_cvt_f32_ubyte2_e32 v130, v69
	v_cvt_f32_ubyte3_e32 v131, v69
	v_fmac_f32_e32 v178, s25, v124
	v_fmac_f32_e32 v179, s25, v125
	v_fmac_f32_e32 v180, s25, v126
	v_fmac_f32_e32 v181, s25, v127
	v_fmac_f32_e32 v182, s25, v128
	v_fmac_f32_e32 v183, s25, v129
	v_fmac_f32_e32 v184, s25, v130
	v_fmac_f32_e32 v185, s25, v131
	s_waitcnt vmcnt(8)
	v_readlane_b32 s25, v247, 55
	v_cvt_f32_ubyte0_e32 v132, v70
	v_cvt_f32_ubyte1_e32 v133, v70
	v_cvt_f32_ubyte2_e32 v134, v70
	v_cvt_f32_ubyte3_e32 v135, v70
	v_cvt_f32_ubyte0_e32 v136, v71
	v_cvt_f32_ubyte1_e32 v137, v71
	v_cvt_f32_ubyte2_e32 v138, v71
	v_cvt_f32_ubyte3_e32 v139, v71
	v_fmac_f32_e32 v178, s25, v132
	v_fmac_f32_e32 v179, s25, v133
	v_fmac_f32_e32 v180, s25, v134
	v_fmac_f32_e32 v181, s25, v135
	v_fmac_f32_e32 v182, s25, v136
	v_fmac_f32_e32 v183, s25, v137
	v_fmac_f32_e32 v184, s25, v138
	v_fmac_f32_e32 v185, s25, v139
	s_waitcnt vmcnt(7)
	v_readlane_b32 s25, v247, 56
	v_cvt_f32_ubyte0_e32 v124, v72
	v_cvt_f32_ubyte1_e32 v125, v72
	v_cvt_f32_ubyte2_e32 v126, v72
	v_cvt_f32_ubyte3_e32 v127, v72
	v_cvt_f32_ubyte0_e32 v128, v73
	v_cvt_f32_ubyte1_e32 v129, v73
	v_cvt_f32_ubyte2_e32 v130, v73
	v_cvt_f32_ubyte3_e32 v131, v73
	v_fmac_f32_e32 v178, s25, v124
	v_fmac_f32_e32 v179, s25, v125
	v_fmac_f32_e32 v180, s25, v126
	v_fmac_f32_e32 v181, s25, v127
	v_fmac_f32_e32 v182, s25, v128
	v_fmac_f32_e32 v183, s25, v129
	v_fmac_f32_e32 v184, s25, v130
	v_fmac_f32_e32 v185, s25, v131
	s_waitcnt vmcnt(6)
	v_readlane_b32 s25, v247, 57
	v_cvt_f32_ubyte0_e32 v132, v74
	v_cvt_f32_ubyte1_e32 v133, v74
	v_cvt_f32_ubyte2_e32 v134, v74
	v_cvt_f32_ubyte3_e32 v135, v74
	v_cvt_f32_ubyte0_e32 v136, v75
	v_cvt_f32_ubyte1_e32 v137, v75
	v_cvt_f32_ubyte2_e32 v138, v75
	v_cvt_f32_ubyte3_e32 v139, v75
	v_fmac_f32_e32 v178, s25, v132
	v_fmac_f32_e32 v179, s25, v133
	v_fmac_f32_e32 v180, s25, v134
	v_fmac_f32_e32 v181, s25, v135
	v_fmac_f32_e32 v182, s25, v136
	v_fmac_f32_e32 v183, s25, v137
	v_fmac_f32_e32 v184, s25, v138
	v_fmac_f32_e32 v185, s25, v139
	s_waitcnt vmcnt(5)
	v_readlane_b32 s25, v247, 58
	v_cvt_f32_ubyte0_e32 v124, v76
	v_cvt_f32_ubyte1_e32 v125, v76
	v_cvt_f32_ubyte2_e32 v126, v76
	v_cvt_f32_ubyte3_e32 v127, v76
	v_cvt_f32_ubyte0_e32 v128, v77
	v_cvt_f32_ubyte1_e32 v129, v77
	v_cvt_f32_ubyte2_e32 v130, v77
	v_cvt_f32_ubyte3_e32 v131, v77
	v_fmac_f32_e32 v178, s25, v124
	v_fmac_f32_e32 v179, s25, v125
	v_fmac_f32_e32 v180, s25, v126
	v_fmac_f32_e32 v181, s25, v127
	v_fmac_f32_e32 v182, s25, v128
	v_fmac_f32_e32 v183, s25, v129
	v_fmac_f32_e32 v184, s25, v130
	v_fmac_f32_e32 v185, s25, v131
	s_waitcnt vmcnt(4)
	v_readlane_b32 s25, v247, 59
	v_cvt_f32_ubyte0_e32 v132, v78
	v_cvt_f32_ubyte1_e32 v133, v78
	v_cvt_f32_ubyte2_e32 v134, v78
	v_cvt_f32_ubyte3_e32 v135, v78
	v_cvt_f32_ubyte0_e32 v136, v79
	v_cvt_f32_ubyte1_e32 v137, v79
	v_cvt_f32_ubyte2_e32 v138, v79
	v_cvt_f32_ubyte3_e32 v139, v79
	v_fmac_f32_e32 v178, s25, v132
	v_fmac_f32_e32 v179, s25, v133
	v_fmac_f32_e32 v180, s25, v134
	v_fmac_f32_e32 v181, s25, v135
	v_fmac_f32_e32 v182, s25, v136
	v_fmac_f32_e32 v183, s25, v137
	v_fmac_f32_e32 v184, s25, v138
	v_fmac_f32_e32 v185, s25, v139
	s_waitcnt vmcnt(3)
	v_readlane_b32 s25, v247, 60
	v_cvt_f32_ubyte0_e32 v124, v80
	v_cvt_f32_ubyte1_e32 v125, v80
	v_cvt_f32_ubyte2_e32 v126, v80
	v_cvt_f32_ubyte3_e32 v127, v80
	v_cvt_f32_ubyte0_e32 v128, v81
	v_cvt_f32_ubyte1_e32 v129, v81
	v_cvt_f32_ubyte2_e32 v130, v81
	v_cvt_f32_ubyte3_e32 v131, v81
	v_fmac_f32_e32 v178, s25, v124
	v_fmac_f32_e32 v179, s25, v125
	v_fmac_f32_e32 v180, s25, v126
	v_fmac_f32_e32 v181, s25, v127
	v_fmac_f32_e32 v182, s25, v128
	v_fmac_f32_e32 v183, s25, v129
	v_fmac_f32_e32 v184, s25, v130
	v_fmac_f32_e32 v185, s25, v131
	s_waitcnt vmcnt(2)
	v_readlane_b32 s25, v247, 61
	v_cvt_f32_ubyte0_e32 v132, v82
	v_cvt_f32_ubyte1_e32 v133, v82
	v_cvt_f32_ubyte2_e32 v134, v82
	v_cvt_f32_ubyte3_e32 v135, v82
	v_cvt_f32_ubyte0_e32 v136, v83
	v_cvt_f32_ubyte1_e32 v137, v83
	v_cvt_f32_ubyte2_e32 v138, v83
	v_cvt_f32_ubyte3_e32 v139, v83
	v_fmac_f32_e32 v178, s25, v132
	v_fmac_f32_e32 v179, s25, v133
	v_fmac_f32_e32 v180, s25, v134
	v_fmac_f32_e32 v181, s25, v135
	v_fmac_f32_e32 v182, s25, v136
	v_fmac_f32_e32 v183, s25, v137
	v_fmac_f32_e32 v184, s25, v138
	v_fmac_f32_e32 v185, s25, v139
	s_waitcnt vmcnt(1)
	v_readlane_b32 s25, v247, 62
	v_cvt_f32_ubyte0_e32 v124, v84
	v_cvt_f32_ubyte1_e32 v125, v84
	v_cvt_f32_ubyte2_e32 v126, v84
	v_cvt_f32_ubyte3_e32 v127, v84
	v_cvt_f32_ubyte0_e32 v128, v85
	v_cvt_f32_ubyte1_e32 v129, v85
	v_cvt_f32_ubyte2_e32 v130, v85
	v_cvt_f32_ubyte3_e32 v131, v85
	v_fmac_f32_e32 v178, s25, v124
	v_fmac_f32_e32 v179, s25, v125
	v_fmac_f32_e32 v180, s25, v126
	v_fmac_f32_e32 v181, s25, v127
	v_fmac_f32_e32 v182, s25, v128
	v_fmac_f32_e32 v183, s25, v129
	v_fmac_f32_e32 v184, s25, v130
	v_fmac_f32_e32 v185, s25, v131
	s_waitcnt vmcnt(0)
	v_readlane_b32 s25, v247, 63
	v_cvt_f32_ubyte0_e32 v132, v86
	v_cvt_f32_ubyte1_e32 v133, v86
	v_cvt_f32_ubyte2_e32 v134, v86
	v_cvt_f32_ubyte3_e32 v135, v86
	v_cvt_f32_ubyte0_e32 v136, v87
	v_cvt_f32_ubyte1_e32 v137, v87
	v_cvt_f32_ubyte2_e32 v138, v87
	v_cvt_f32_ubyte3_e32 v139, v87
	v_fmac_f32_e32 v178, s25, v132
	v_fmac_f32_e32 v179, s25, v133
	v_fmac_f32_e32 v180, s25, v134
	v_fmac_f32_e32 v181, s25, v135
	v_fmac_f32_e32 v182, s25, v136
	v_fmac_f32_e32 v183, s25, v137
	v_fmac_f32_e32 v184, s25, v138
	v_fmac_f32_e32 v185, s25, v139
	v_lshlrev_b32_e32 v132, 16, v242
	v_and_b32_e32 v133, 0xffff0000, v242
	v_lshlrev_b32_e32 v134, 16, v243
	v_and_b32_e32 v135, 0xffff0000, v243
	v_lshlrev_b32_e32 v136, 16, v244
	v_and_b32_e32 v137, 0xffff0000, v244
	v_lshlrev_b32_e32 v138, 16, v245
	v_and_b32_e32 v139, 0xffff0000, v245
	v_add_f32_e32 v178, v178, v248
	v_add_f32_e32 v179, v179, v248
	v_add_f32_e32 v180, v180, v248
	v_add_f32_e32 v181, v181, v248
	v_add_f32_e32 v182, v182, v248
	v_add_f32_e32 v183, v183, v248
	v_add_f32_e32 v184, v184, v248
	v_add_f32_e32 v185, v185, v248
	v_add_f32_e32 v124, v132, v178
	v_add_f32_e32 v125, v133, v179
	v_add_f32_e32 v126, v134, v180
	v_add_f32_e32 v127, v135, v181
	v_add_f32_e32 v128, v136, v182
	v_add_f32_e32 v129, v137, v183
	v_add_f32_e32 v130, v138, v184
	v_add_f32_e32 v131, v139, v185
	v_mul_f32_e32 v16, v124, v124
	v_fmac_f32_e32 v16, v125, v125
	v_fmac_f32_e32 v16, v126, v126
	v_fmac_f32_e32 v16, v127, v127
	v_fmac_f32_e32 v16, v128, v128
	v_fmac_f32_e32 v16, v129, v129
	v_fmac_f32_e32 v16, v130, v130
	v_fmac_f32_e32 v16, v131, v131
	s_nop 1
	v_add_f32_dpp v17, v16, v16 quad_perm:[1,0,3,2] row_mask:0xf bank_mask:0xf
	s_nop 1
	v_add_f32_dpp v16, v17, v17 quad_perm:[2,3,0,1] row_mask:0xf bank_mask:0xf
	s_nop 1
	v_add_f32_dpp v17, v16, v16 row_half_mirror row_mask:0xf bank_mask:0xf
	s_nop 1
	v_add_f32_dpp v16, v17, v17 row_ror:8 row_mask:0xf bank_mask:0xf
	v_mov_b32_e32 v17, v16
	s_nop 1
	v_permlane16_swap_b32_e32 v16, v17
	v_add_f32_e32 v16, v16, v17
	v_mov_b32_e32 v17, v16
	s_nop 1
	v_permlane32_swap_b32_e32 v16, v17
	v_add_f32_e32 v16, v16, v17
	global_store_dwordx4 v[20:21], v[124:127], off
	global_store_dwordx4 v[20:21], v[128:131], off offset:16
	s_lshl_b32 s30, s16, 7
	s_add_u32 s28, s62, s30
	s_addc_u32 s29, s63, 0
	v_lshlrev_b32_e32 v18, 1, v1
	s_mov_b64 exec, s[2:3]
	global_store_dword v18, v16, s[28:29]
	s_mov_b64 exec, -1
	s_waitcnt lgkmcnt(0)
	s_load_dwordx16 s[84:99], s[38:39], 0x40 glc
	s_lshl_b32 s30, s68, 12
	s_add_u32 s28, s26, s30
	s_addc_u32 s29, s27, 0
	global_load_dwordx2 v[24:25], v162, s[28:29]
	s_lshl_b32 s30, s69, 12
	s_add_u32 s28, s26, s30
	s_addc_u32 s29, s27, 0
	global_load_dwordx2 v[26:27], v162, s[28:29]
	s_lshl_b32 s30, s70, 12
	s_add_u32 s28, s26, s30
	s_addc_u32 s29, s27, 0
	global_load_dwordx2 v[28:29], v162, s[28:29]
	s_lshl_b32 s30, s71, 12
	s_add_u32 s28, s26, s30
	s_addc_u32 s29, s27, 0
	global_load_dwordx2 v[30:31], v162, s[28:29]
	s_lshl_b32 s30, s72, 12
	s_add_u32 s28, s26, s30
	s_addc_u32 s29, s27, 0
	global_load_dwordx2 v[32:33], v162, s[28:29]
	s_lshl_b32 s30, s73, 12
	s_add_u32 s28, s26, s30
	s_addc_u32 s29, s27, 0
	global_load_dwordx2 v[34:35], v162, s[28:29]
	s_lshl_b32 s30, s74, 12
	s_add_u32 s28, s26, s30
	s_addc_u32 s29, s27, 0
	global_load_dwordx2 v[36:37], v162, s[28:29]
	s_lshl_b32 s30, s75, 12
	s_add_u32 s28, s26, s30
	s_addc_u32 s29, s27, 0
	global_load_dwordx2 v[38:39], v162, s[28:29]
	s_lshl_b32 s30, s76, 12
	s_add_u32 s28, s26, s30
	s_addc_u32 s29, s27, 0
	global_load_dwordx2 v[40:41], v162, s[28:29]
	s_lshl_b32 s30, s77, 12
	s_add_u32 s28, s26, s30
	s_addc_u32 s29, s27, 0
	global_load_dwordx2 v[42:43], v162, s[28:29]
	s_lshl_b32 s30, s78, 12
	s_add_u32 s28, s26, s30
	s_addc_u32 s29, s27, 0
	global_load_dwordx2 v[44:45], v162, s[28:29]
	s_lshl_b32 s30, s79, 12
	s_add_u32 s28, s26, s30
	s_addc_u32 s29, s27, 0
	global_load_dwordx2 v[46:47], v162, s[28:29]
	s_lshl_b32 s30, s80, 12
	s_add_u32 s28, s26, s30
	s_addc_u32 s29, s27, 0
	global_load_dwordx2 v[48:49], v162, s[28:29]
	s_lshl_b32 s30, s81, 12
	s_add_u32 s28, s26, s30
	s_addc_u32 s29, s27, 0
	global_load_dwordx2 v[50:51], v162, s[28:29]
	s_lshl_b32 s30, s82, 12
	s_add_u32 s28, s26, s30
	s_addc_u32 s29, s27, 0
	global_load_dwordx2 v[52:53], v162, s[28:29]
	s_lshl_b32 s30, s83, 12
	s_add_u32 s28, s26, s30
	s_addc_u32 s29, s27, 0
	global_load_dwordx2 v[54:55], v162, s[28:29]
	s_waitcnt lgkmcnt(0)
	s_load_dwordx16 s[68:83], s[38:39], 0x80 glc
	s_lshl_b32 s30, s84, 12
	s_add_u32 s28, s26, s30
	s_addc_u32 s29, s27, 0
	global_load_dwordx2 v[56:57], v162, s[28:29]
	s_lshl_b32 s30, s85, 12
	s_add_u32 s28, s26, s30
	s_addc_u32 s29, s27, 0
	global_load_dwordx2 v[58:59], v162, s[28:29]
	s_lshl_b32 s30, s86, 12
	s_add_u32 s28, s26, s30
	s_addc_u32 s29, s27, 0
	global_load_dwordx2 v[60:61], v162, s[28:29]
	s_lshl_b32 s30, s87, 12
	s_add_u32 s28, s26, s30
	s_addc_u32 s29, s27, 0
	global_load_dwordx2 v[62:63], v162, s[28:29]
	s_lshl_b32 s30, s88, 12
	s_add_u32 s28, s26, s30
	s_addc_u32 s29, s27, 0
	global_load_dwordx2 v[64:65], v162, s[28:29]
	s_lshl_b32 s30, s89, 12
	s_add_u32 s28, s26, s30
	s_addc_u32 s29, s27, 0
	global_load_dwordx2 v[66:67], v162, s[28:29]
	s_lshl_b32 s30, s90, 12
	s_add_u32 s28, s26, s30
	s_addc_u32 s29, s27, 0
	global_load_dwordx2 v[68:69], v162, s[28:29]
	s_lshl_b32 s30, s91, 12
	s_add_u32 s28, s26, s30
	s_addc_u32 s29, s27, 0
	global_load_dwordx2 v[70:71], v162, s[28:29]
	s_lshl_b32 s30, s92, 12
	s_add_u32 s28, s26, s30
	s_addc_u32 s29, s27, 0
	global_load_dwordx2 v[72:73], v162, s[28:29]
	s_lshl_b32 s30, s93, 12
	s_add_u32 s28, s26, s30
	s_addc_u32 s29, s27, 0
	global_load_dwordx2 v[74:75], v162, s[28:29]
	s_lshl_b32 s30, s94, 12
	s_add_u32 s28, s26, s30
	s_addc_u32 s29, s27, 0
	global_load_dwordx2 v[76:77], v162, s[28:29]
	s_lshl_b32 s30, s95, 12
	s_add_u32 s28, s26, s30
	s_addc_u32 s29, s27, 0
	global_load_dwordx2 v[78:79], v162, s[28:29]
	s_lshl_b32 s30, s96, 12
	s_add_u32 s28, s26, s30
	s_addc_u32 s29, s27, 0
	global_load_dwordx2 v[80:81], v162, s[28:29]
	s_lshl_b32 s30, s97, 12
	s_add_u32 s28, s26, s30
	s_addc_u32 s29, s27, 0
	global_load_dwordx2 v[82:83], v162, s[28:29]
	s_lshl_b32 s30, s98, 12
	s_add_u32 s28, s26, s30
	s_addc_u32 s29, s27, 0
	global_load_dwordx2 v[84:85], v162, s[28:29]
	s_lshl_b32 s30, s99, 12
	s_add_u32 s28, s26, s30
	s_addc_u32 s29, s27, 0
	global_load_dwordx2 v[86:87], v162, s[28:29]
	s_add_i32 s16, s16, 1
	s_cmp_lt_i32 s16, s17
	s_cbranch_scc1 .Lpb_tok
	s_waitcnt vmcnt(0)
	s_waitcnt vmcnt(0)
	v_cmp_eq_u32_e32 vcc, 0, v0
	s_waitcnt vmcnt(0) lgkmcnt(0)
	s_barrier
	s_and_saveexec_b64 s[2:3], vcc
	s_cbranch_execz .Lgbc_1444
	v_readlane_b32 s4, v237, 5
	s_waitcnt vmcnt(0) expcnt(0) lgkmcnt(0)
	s_nop 0
	v_mov_b32_e32 v1, s4
	ds_read_b32 v3, v1
	ds_read_b32 v1, v1 offset:4
	s_waitcnt lgkmcnt(1)
	v_cmp_ne_u32_e32 vcc, 0, v3
	s_branch .Lgbc_1412
	v_readlane_b32 s4, v237, 2
	v_readlane_b32 s5, v237, 3
	s_load_dwordx2 s[8:9], s[6:7], 0x4
	s_lshl_b64 s[4:5], s[4:5], 2
	v_readlane_b32 s6, v237, 0
	s_add_u32 s4, s6, s4
	v_readlane_b32 s6, v237, 1
	s_addc_u32 s5, s6, s5
	s_add_u32 s6, s4, 0x1000
	s_addc_u32 s7, s5, 0
	s_waitcnt lgkmcnt(0)
	s_mul_i32 s20, s8, s38
	s_add_u32 s8, s4, 0x1100
	s_mul_i32 s20, s20, s9
	s_addc_u32 s9, s5, 0
	s_add_u32 s10, s4, 0x1200
	s_addc_u32 s11, s5, 0
	s_add_u32 s12, s4, 0x1300
	s_addc_u32 s13, s5, 0
	s_mov_b32 s21, 1
	v_mov_b32_e32 v17, 0
	s_branch .Lgbc_1400
